# K-loops: all per-block priority changes removed (on top of the mLSTM edits)
# baseline (speedup 1.0000x reference)
.LBB0_276:
	s_or_b64 exec, exec, s[60:61]
	s_add_u32 s62, s56, 0x10000
	s_addc_u32 s63, s57, 0
	s_and_b64 s[60:61], s[34:35], exec
	s_cselect_b32 s67, s51, s63
	s_cselect_b32 s66, s50, s62
	s_add_u32 s62, s58, 0x10000
	s_addc_u32 s63, s59, 0
	s_and_b64 s[60:61], s[34:35], exec
	s_cselect_b32 s63, s53, s63
	s_cselect_b32 s62, s52, s62
	s_add_u32 s60, s66, 0x8000
	s_addc_u32 s61, s67, 0
	s_add_u32 s64, s62, 0x8000
	s_addc_u32 s65, s63, 0
	s_add_i32 s84, 0, 0x10000
	s_add_i32 s85, 0, 0x14000
	v_add_u32_e32 v132, s84, v141
	v_add_u32_e32 v133, s85, v141
	ds_read_b128 v[2:5], v132
	ds_read_b128 v[6:9], v132 offset:1024
	ds_read_b128 v[10:13], v132 offset:2048
	ds_read_b128 v[14:17], v132 offset:3072
	ds_read_b128 v[18:21], v133
	ds_read_b128 v[22:25], v133 offset:1024
	ds_read_b128 v[26:29], v133 offset:2048
	ds_read_b128 v[30:33], v133 offset:3072
	s_add_u32 s82, s56, 0xc000
	s_addc_u32 s83, s57, 0
	s_add_i32 s80, s15, 0xc000
	s_mov_b32 m0, s80
	s_add_i32 s81, s15, 0xe000
	ds_read_b128 v[34:37], v143
	ds_read_b128 v[38:41], v143 offset:1024
	ds_read_b128 v[42:45], v143 offset:2048
	ds_read_b128 v[46:49], v143 offset:3072
	ds_read_b128 v[50:53], v143 offset:4096
	ds_read_b128 v[54:57], v143 offset:5120
	ds_read_b128 v[58:61], v143 offset:6144
	ds_read_b128 v[62:65], v143 offset:7168
	s_nop 0
	global_load_lds_dwordx4 v137, s[82:83]
	s_mov_b32 m0, s81
	s_nop 0
	global_load_lds_dwordx4 v139, s[82:83]
	s_waitcnt vmcnt(8)
	s_waitcnt lgkmcnt(0)
	s_barrier
	s_waitcnt lgkmcnt(0)
	v_mfma_f32_16x16x32_bf16 v[86:89], v[10:13], v[50:53], 0
	v_mfma_f32_16x16x32_bf16 v[90:93], v[14:17], v[54:57], v[86:89]
	v_mfma_f32_16x16x32_bf16 v[86:89], v[2:5], v[58:61], 0
	v_mfma_f32_16x16x32_bf16 v[66:69], v[2:5], v[34:37], 0
	v_mfma_f32_16x16x32_bf16 v[70:73], v[10:13], v[34:37], 0
	v_mfma_f32_16x16x32_bf16 v[74:77], v[2:5], v[42:45], 0
	v_mfma_f32_16x16x32_bf16 v[78:81], v[10:13], v[42:45], 0
	v_mfma_f32_16x16x32_bf16 v[82:85], v[2:5], v[50:53], 0
	v_mfma_f32_16x16x32_bf16 v[94:97], v[6:9], v[62:65], v[86:89]
	v_mfma_f32_16x16x32_bf16 v[86:89], v[10:13], v[58:61], 0
	v_mfma_f32_16x16x32_bf16 v[66:69], v[6:9], v[38:41], v[66:69]
	v_mfma_f32_16x16x32_bf16 v[70:73], v[14:17], v[38:41], v[70:73]
	v_mfma_f32_16x16x32_bf16 v[74:77], v[6:9], v[46:49], v[74:77]
	v_mfma_f32_16x16x32_bf16 v[78:81], v[14:17], v[46:49], v[78:81]
	v_mfma_f32_16x16x32_bf16 v[82:85], v[6:9], v[54:57], v[82:85]
	v_mfma_f32_16x16x32_bf16 v[106:109], v[14:17], v[62:65], v[86:89]
	v_mfma_f32_16x16x32_bf16 v[86:89], v[18:21], v[34:37], 0
	v_mfma_f32_16x16x32_bf16 v[34:37], v[26:29], v[34:37], 0
	v_mfma_f32_16x16x32_bf16 v[110:113], v[22:25], v[38:41], v[86:89]
	v_mfma_f32_16x16x32_bf16 v[34:37], v[30:33], v[38:41], v[34:37]
	v_mfma_f32_16x16x32_bf16 v[38:41], v[18:21], v[42:45], 0
	v_mfma_f32_16x16x32_bf16 v[42:45], v[26:29], v[42:45], 0
	v_mfma_f32_16x16x32_bf16 v[38:41], v[22:25], v[46:49], v[38:41]
	v_mfma_f32_16x16x32_bf16 v[42:45], v[30:33], v[46:49], v[42:45]
	v_mfma_f32_16x16x32_bf16 v[46:49], v[18:21], v[50:53], 0
	v_mfma_f32_16x16x32_bf16 v[50:53], v[26:29], v[50:53], 0
	v_mfma_f32_16x16x32_bf16 v[46:49], v[22:25], v[54:57], v[46:49]
	v_mfma_f32_16x16x32_bf16 v[50:53], v[30:33], v[54:57], v[50:53]
	v_mfma_f32_16x16x32_bf16 v[54:57], v[18:21], v[58:61], 0
	v_mfma_f32_16x16x32_bf16 v[144:147], v[22:25], v[62:65], v[54:57]
	v_mfma_f32_16x16x32_bf16 v[54:57], v[26:29], v[58:61], 0
	v_mfma_f32_16x16x32_bf16 v[58:61], v[30:33], v[62:65], v[54:57]
	s_barrier
	s_add_i32 s82, s84, s14
	s_add_i32 s83, s82, 0x2000
	s_mov_b32 m0, s82
	s_add_u32 s86, s62, 0x4000
	s_nop 0
	ds_read_b128 v[54:57], v143 offset:16384
	ds_read_b128 v[62:65], v143 offset:17408
	ds_read_b128 v[86:89], v143 offset:18432
	ds_read_b128 v[98:101], v143 offset:19456
	ds_read_b128 v[102:105], v143 offset:20480
	ds_read_b128 v[114:117], v143 offset:21504
	ds_read_b128 v[118:121], v143 offset:22528
	ds_read_b128 v[122:125], v143 offset:23552
	s_addc_u32 s87, s63, 0
	global_load_lds_dwordx4 v138, s[62:63]
	s_mov_b32 m0, s83
	s_add_i32 s84, s85, s14
	s_add_i32 s85, s84, 0x2000
	global_load_lds_dwordx4 v140, s[62:63]
	s_mov_b32 m0, s84
	s_nop 0
	global_load_lds_dwordx4 v138, s[86:87]
	s_mov_b32 m0, s85
	s_nop 0
	global_load_lds_dwordx4 v140, s[86:87]
	s_mov_b32 m0, s15
	s_nop 0
	global_load_lds_dwordx4 v137, s[66:67]
	s_mov_b32 m0, s18
	s_nop 0
	global_load_lds_dwordx4 v139, s[66:67]
	s_waitcnt vmcnt(8)
	s_waitcnt lgkmcnt(0)
	s_barrier
	s_waitcnt lgkmcnt(0)
	v_mfma_f32_16x16x32_bf16 v[126:129], v[2:5], v[54:57], 0
	v_mfma_f32_16x16x32_bf16 v[148:151], v[6:9], v[62:65], v[126:129]
	v_mfma_f32_16x16x32_bf16 v[126:129], v[10:13], v[54:57], 0
	v_mfma_f32_16x16x32_bf16 v[152:155], v[14:17], v[62:65], v[126:129]
	v_mfma_f32_16x16x32_bf16 v[126:129], v[2:5], v[86:89], 0
	v_mfma_f32_16x16x32_bf16 v[156:159], v[6:9], v[98:101], v[126:129]
	v_mfma_f32_16x16x32_bf16 v[126:129], v[10:13], v[86:89], 0
	v_mfma_f32_16x16x32_bf16 v[160:163], v[14:17], v[98:101], v[126:129]
	v_mfma_f32_16x16x32_bf16 v[126:129], v[2:5], v[102:105], 0
	v_mfma_f32_16x16x32_bf16 v[2:5], v[2:5], v[118:121], 0
	v_mfma_f32_16x16x32_bf16 v[164:167], v[6:9], v[114:117], v[126:129]
	v_mfma_f32_16x16x32_bf16 v[2:5], v[6:9], v[122:125], v[2:5]
	v_mfma_f32_16x16x32_bf16 v[6:9], v[10:13], v[118:121], 0
	v_mfma_f32_16x16x32_bf16 v[126:129], v[10:13], v[102:105], 0
	v_mfma_f32_16x16x32_bf16 v[10:13], v[14:17], v[122:125], v[6:9]
	v_mfma_f32_16x16x32_bf16 v[168:171], v[14:17], v[114:117], v[126:129]
	v_mfma_f32_16x16x32_bf16 v[6:9], v[18:21], v[54:57], 0
	v_mfma_f32_16x16x32_bf16 v[14:17], v[22:25], v[62:65], v[6:9]
	v_mfma_f32_16x16x32_bf16 v[6:9], v[26:29], v[54:57], 0
	v_mfma_f32_16x16x32_bf16 v[172:175], v[30:33], v[62:65], v[6:9]
	v_mfma_f32_16x16x32_bf16 v[6:9], v[18:21], v[86:89], 0
	v_mfma_f32_16x16x32_bf16 v[176:179], v[22:25], v[98:101], v[6:9]
	v_mfma_f32_16x16x32_bf16 v[6:9], v[26:29], v[86:89], 0
	v_mfma_f32_16x16x32_bf16 v[180:183], v[30:33], v[98:101], v[6:9]
	v_mfma_f32_16x16x32_bf16 v[6:9], v[18:21], v[102:105], 0
	v_mfma_f32_16x16x32_bf16 v[184:187], v[22:25], v[114:117], v[6:9]
	v_mfma_f32_16x16x32_bf16 v[6:9], v[26:29], v[102:105], 0
	v_mfma_f32_16x16x32_bf16 v[210:213], v[30:33], v[114:117], v[6:9]
	v_mfma_f32_16x16x32_bf16 v[6:9], v[18:21], v[118:121], 0
	v_mfma_f32_16x16x32_bf16 v[214:217], v[22:25], v[122:125], v[6:9]
	v_mfma_f32_16x16x32_bf16 v[6:9], v[26:29], v[118:121], 0
	v_mfma_f32_16x16x32_bf16 v[218:221], v[30:33], v[122:125], v[6:9]
	s_barrier
	s_add_i32 s86, 0, 0x18000
	s_add_i32 s87, 0, 0x1c000
	v_add_u32_e32 v134, s86, v141
	v_add_u32_e32 v135, s87, v141
	s_nop 0
	ds_read_b128 v[6:9], v134
	ds_read_b128 v[26:29], v134 offset:1024
	ds_read_b128 v[30:33], v134 offset:2048
	ds_read_b128 v[222:225], v134 offset:3072
	ds_read_b128 v[236:239], v135
	ds_read_b128 v[240:243], v135 offset:1024
	ds_read_b128 v[244:247], v135 offset:2048
	ds_read_b128 v[232:235], v135 offset:3072
	s_add_u32 s66, s66, 0x4000
	s_addc_u32 s67, s67, 0
	s_mov_b32 m0, s20
	ds_read_b128 v[18:21], v143 offset:32768
	ds_read_b128 v[22:25], v143 offset:33792
	ds_read_b128 v[194:197], v143 offset:34816
	ds_read_b128 v[202:205], v143 offset:35840
	ds_read_b128 v[188:191], v143 offset:36864
	ds_read_b128 v[206:209], v143 offset:37888
	ds_read_b128 v[198:201], v143 offset:38912
	ds_read_b128 v[226:229], v143 offset:39936
	s_nop 0
	global_load_lds_dwordx4 v137, s[66:67]
	s_mov_b32 m0, s21
	s_nop 0
	global_load_lds_dwordx4 v139, s[66:67]
	s_waitcnt vmcnt(8)
	s_waitcnt lgkmcnt(0)
	s_barrier
	s_waitcnt lgkmcnt(0)
	v_mfma_f32_16x16x32_bf16 v[54:57], v[6:9], v[18:21], v[66:69]
	v_mfma_f32_16x16x32_bf16 v[118:121], v[26:29], v[22:25], v[54:57]
	v_mfma_f32_16x16x32_bf16 v[54:57], v[30:33], v[18:21], v[70:73]
	v_mfma_f32_16x16x32_bf16 v[114:117], v[222:225], v[22:25], v[54:57]
	v_mfma_f32_16x16x32_bf16 v[54:57], v[6:9], v[194:197], v[74:77]
	v_mfma_f32_16x16x32_bf16 v[102:105], v[26:29], v[202:205], v[54:57]
	v_mfma_f32_16x16x32_bf16 v[54:57], v[30:33], v[194:197], v[78:81]
	v_mfma_f32_16x16x32_bf16 v[98:101], v[222:225], v[202:205], v[54:57]
	v_mfma_f32_16x16x32_bf16 v[54:57], v[6:9], v[188:191], v[82:85]
	v_mfma_f32_16x16x32_bf16 v[86:89], v[26:29], v[206:209], v[54:57]
	v_mfma_f32_16x16x32_bf16 v[54:57], v[30:33], v[188:191], v[90:93]
	v_mfma_f32_16x16x32_bf16 v[82:85], v[222:225], v[206:209], v[54:57]
	v_mfma_f32_16x16x32_bf16 v[54:57], v[6:9], v[198:201], v[94:97]
	v_mfma_f32_16x16x32_bf16 v[62:65], v[26:29], v[226:229], v[54:57]
	v_mfma_f32_16x16x32_bf16 v[54:57], v[30:33], v[198:201], v[106:109]
	v_mfma_f32_16x16x32_bf16 v[54:57], v[222:225], v[226:229], v[54:57]
	v_mfma_f32_16x16x32_bf16 v[66:69], v[236:239], v[18:21], v[110:113]
	v_mfma_f32_16x16x32_bf16 v[18:21], v[244:247], v[18:21], v[34:37]
	v_mfma_f32_16x16x32_bf16 v[122:125], v[232:235], v[22:25], v[18:21]
	v_mfma_f32_16x16x32_bf16 v[18:21], v[236:239], v[194:197], v[38:41]
	v_mfma_f32_16x16x32_bf16 v[110:113], v[240:243], v[202:205], v[18:21]
	v_mfma_f32_16x16x32_bf16 v[18:21], v[244:247], v[194:197], v[42:45]
	v_mfma_f32_16x16x32_bf16 v[106:109], v[232:235], v[202:205], v[18:21]
	v_mfma_f32_16x16x32_bf16 v[18:21], v[236:239], v[188:191], v[46:49]
	v_mfma_f32_16x16x32_bf16 v[94:97], v[240:243], v[206:209], v[18:21]
	v_mfma_f32_16x16x32_bf16 v[18:21], v[244:247], v[188:191], v[50:53]
	v_mfma_f32_16x16x32_bf16 v[90:93], v[232:235], v[206:209], v[18:21]
	v_mfma_f32_16x16x32_bf16 v[18:21], v[236:239], v[198:201], v[144:147]
	v_mfma_f32_16x16x32_bf16 v[78:81], v[240:243], v[226:229], v[18:21]
	v_mfma_f32_16x16x32_bf16 v[18:21], v[244:247], v[198:201], v[58:61]
	v_mfma_f32_16x16x32_bf16 v[126:129], v[240:243], v[22:25], v[66:69]
	v_mfma_f32_16x16x32_bf16 v[70:73], v[232:235], v[226:229], v[18:21]
	s_barrier
	s_add_i32 s66, s86, s14
	s_add_i32 s67, s66, 0x2000
	s_mov_b32 m0, s66
	s_add_u32 s62, s62, 0xc000
	ds_read_b128 v[42:45], v143 offset:49152
	ds_read_b128 v[46:49], v143 offset:50176
	ds_read_b128 v[144:147], v143 offset:51200
	ds_read_b128 v[188:191], v143 offset:52224
	ds_read_b128 v[194:197], v143 offset:53248
	ds_read_b128 v[198:201], v143 offset:54272
	ds_read_b128 v[202:205], v143 offset:55296
	ds_read_b128 v[206:209], v143 offset:56320
	s_addc_u32 s63, s63, 0
	global_load_lds_dwordx4 v138, s[64:65]
	s_mov_b32 m0, s67
	s_add_i32 s86, s87, s14
	s_add_i32 s87, s86, 0x2000
	global_load_lds_dwordx4 v140, s[64:65]
	s_mov_b32 m0, s86
	s_nop 0
	global_load_lds_dwordx4 v138, s[62:63]
	s_mov_b32 m0, s87
	s_nop 0
	global_load_lds_dwordx4 v140, s[62:63]
	s_mov_b32 m0, s69
	s_nop 0
	global_load_lds_dwordx4 v137, s[60:61]
	s_mov_b32 m0, s70
	s_nop 0
	global_load_lds_dwordx4 v139, s[60:61]
	s_waitcnt vmcnt(8)
	s_waitcnt lgkmcnt(0)
	s_barrier
	s_waitcnt lgkmcnt(0)
	v_mfma_f32_16x16x32_bf16 v[18:21], v[6:9], v[42:45], v[148:151]
	v_mfma_f32_16x16x32_bf16 v[58:61], v[26:29], v[46:49], v[18:21]
	v_mfma_f32_16x16x32_bf16 v[18:21], v[30:33], v[42:45], v[152:155]
	v_mfma_f32_16x16x32_bf16 v[50:53], v[222:225], v[46:49], v[18:21]
	v_mfma_f32_16x16x32_bf16 v[18:21], v[6:9], v[144:147], v[156:159]
	v_mfma_f32_16x16x32_bf16 v[38:41], v[26:29], v[188:191], v[18:21]
	v_mfma_f32_16x16x32_bf16 v[18:21], v[30:33], v[144:147], v[160:163]
	v_mfma_f32_16x16x32_bf16 v[34:37], v[222:225], v[188:191], v[18:21]
	v_mfma_f32_16x16x32_bf16 v[18:21], v[6:9], v[194:197], v[164:167]
	v_mfma_f32_16x16x32_bf16 v[2:5], v[6:9], v[202:205], v[2:5]
	v_mfma_f32_16x16x32_bf16 v[22:25], v[26:29], v[198:201], v[18:21]
	v_mfma_f32_16x16x32_bf16 v[18:21], v[30:33], v[194:197], v[168:171]
	v_mfma_f32_16x16x32_bf16 v[6:9], v[26:29], v[206:209], v[2:5]
	v_mfma_f32_16x16x32_bf16 v[2:5], v[30:33], v[202:205], v[10:13]
	v_mfma_f32_16x16x32_bf16 v[18:21], v[222:225], v[198:201], v[18:21]
	v_mfma_f32_16x16x32_bf16 v[2:5], v[222:225], v[206:209], v[2:5]
	v_mfma_f32_16x16x32_bf16 v[10:13], v[236:239], v[42:45], v[14:17]
	v_mfma_f32_16x16x32_bf16 v[74:77], v[240:243], v[46:49], v[10:13]
	v_mfma_f32_16x16x32_bf16 v[10:13], v[244:247], v[42:45], v[172:175]
	v_mfma_f32_16x16x32_bf16 v[66:69], v[232:235], v[46:49], v[10:13]
	v_mfma_f32_16x16x32_bf16 v[10:13], v[236:239], v[144:147], v[176:179]
	v_mfma_f32_16x16x32_bf16 v[46:49], v[240:243], v[188:191], v[10:13]
	v_mfma_f32_16x16x32_bf16 v[10:13], v[244:247], v[144:147], v[180:183]
	v_mfma_f32_16x16x32_bf16 v[42:45], v[232:235], v[188:191], v[10:13]
	v_mfma_f32_16x16x32_bf16 v[10:13], v[236:239], v[194:197], v[184:187]
	v_mfma_f32_16x16x32_bf16 v[30:33], v[240:243], v[198:201], v[10:13]
	v_mfma_f32_16x16x32_bf16 v[10:13], v[244:247], v[194:197], v[210:213]
	v_mfma_f32_16x16x32_bf16 v[26:29], v[232:235], v[198:201], v[10:13]
	v_mfma_f32_16x16x32_bf16 v[10:13], v[236:239], v[202:205], v[214:217]
	v_mfma_f32_16x16x32_bf16 v[14:17], v[240:243], v[206:209], v[10:13]
	v_mfma_f32_16x16x32_bf16 v[10:13], v[244:247], v[202:205], v[218:221]
	v_mfma_f32_16x16x32_bf16 v[10:13], v[232:235], v[206:209], v[10:13]
	s_barrier
	s_andn2_b64 vcc, exec, s[44:45]
	s_cbranch_vccnz .LBB0_282
	s_lshl_b32 s60, s74, 10
	s_xor_b32 s88, s60, 0x400
	s_add_u32 s89, s58, 0x20000
	s_addc_u32 s90, s59, 0
	v_ashrrev_i32_e32 v131, 31, v130
	s_add_u32 s56, s56, 0x1c000
	v_lshl_add_u64 v[130:131], v[130:131], 3, s[26:27]
	s_addc_u32 s57, s57, 0
	s_mov_b32 s91, 4

.LBB0_280:
	s_or_b64 exec, exec, s[60:61]
	ds_read_b128 v[144:147], v132
	ds_read_b128 v[148:151], v132 offset:1024
	ds_read_b128 v[152:155], v132 offset:2048
	ds_read_b128 v[156:159], v132 offset:3072
	ds_read_b128 v[160:163], v133
	ds_read_b128 v[164:167], v133 offset:1024
	ds_read_b128 v[168:171], v133 offset:2048
	ds_read_b128 v[172:175], v133 offset:3072
	s_add_u32 s60, s56, 0x4000
	s_addc_u32 s61, s57, 0
	s_and_b64 s[58:59], s[58:59], exec
	s_cselect_b32 s64, s50, s60
	s_cselect_b32 s65, s51, s61
	s_cselect_b32 s61, s53, s90
	s_cselect_b32 s60, s52, s89
	s_add_u32 s58, s64, 0x8000
	s_addc_u32 s59, s65, 0
	s_add_u32 s62, s60, 0x8000
	s_addc_u32 s63, s61, 0
	s_mov_b32 m0, s80
	ds_read_b128 v[176:179], v143
	ds_read_b128 v[180:183], v143 offset:1024
	ds_read_b128 v[184:187], v143 offset:2048
	ds_read_b128 v[188:191], v143 offset:3072
	ds_read_b128 v[194:197], v143 offset:4096
	ds_read_b128 v[198:201], v143 offset:5120
	ds_read_b128 v[202:205], v143 offset:6144
	ds_read_b128 v[206:209], v143 offset:7168
	s_nop 0
	global_load_lds_dwordx4 v137, s[56:57]
	s_mov_b32 m0, s81
	s_nop 0
	global_load_lds_dwordx4 v139, s[56:57]
	s_waitcnt vmcnt(8)
	s_waitcnt lgkmcnt(0)
	s_barrier
	s_waitcnt lgkmcnt(0)
	v_mfma_f32_16x16x32_bf16 v[118:121], v[144:147], v[176:179], v[118:121]
	v_mfma_f32_16x16x32_bf16 v[114:117], v[152:155], v[176:179], v[114:117]
	v_mfma_f32_16x16x32_bf16 v[102:105], v[144:147], v[184:187], v[102:105]
	v_mfma_f32_16x16x32_bf16 v[98:101], v[152:155], v[184:187], v[98:101]
	v_mfma_f32_16x16x32_bf16 v[86:89], v[144:147], v[194:197], v[86:89]
	v_mfma_f32_16x16x32_bf16 v[82:85], v[152:155], v[194:197], v[82:85]
	v_mfma_f32_16x16x32_bf16 v[62:65], v[144:147], v[202:205], v[62:65]
	v_mfma_f32_16x16x32_bf16 v[54:57], v[152:155], v[202:205], v[54:57]
	v_mfma_f32_16x16x32_bf16 v[118:121], v[148:151], v[180:183], v[118:121]
	v_mfma_f32_16x16x32_bf16 v[114:117], v[156:159], v[180:183], v[114:117]
	v_mfma_f32_16x16x32_bf16 v[102:105], v[148:151], v[188:191], v[102:105]
	v_mfma_f32_16x16x32_bf16 v[98:101], v[156:159], v[188:191], v[98:101]
	v_mfma_f32_16x16x32_bf16 v[86:89], v[148:151], v[198:201], v[86:89]
	v_mfma_f32_16x16x32_bf16 v[82:85], v[156:159], v[198:201], v[82:85]
	v_mfma_f32_16x16x32_bf16 v[62:65], v[148:151], v[206:209], v[62:65]
	v_mfma_f32_16x16x32_bf16 v[54:57], v[156:159], v[206:209], v[54:57]
	v_mfma_f32_16x16x32_bf16 v[126:129], v[160:163], v[176:179], v[126:129]
	v_mfma_f32_16x16x32_bf16 v[122:125], v[168:171], v[176:179], v[122:125]
	v_mfma_f32_16x16x32_bf16 v[110:113], v[160:163], v[184:187], v[110:113]
	v_mfma_f32_16x16x32_bf16 v[106:109], v[168:171], v[184:187], v[106:109]
	v_mfma_f32_16x16x32_bf16 v[94:97], v[160:163], v[194:197], v[94:97]
	v_mfma_f32_16x16x32_bf16 v[90:93], v[168:171], v[194:197], v[90:93]
	v_mfma_f32_16x16x32_bf16 v[78:81], v[160:163], v[202:205], v[78:81]
	v_mfma_f32_16x16x32_bf16 v[70:73], v[168:171], v[202:205], v[70:73]
	v_mfma_f32_16x16x32_bf16 v[126:129], v[164:167], v[180:183], v[126:129]
	v_mfma_f32_16x16x32_bf16 v[122:125], v[172:175], v[180:183], v[122:125]
	v_mfma_f32_16x16x32_bf16 v[110:113], v[164:167], v[188:191], v[110:113]
	v_mfma_f32_16x16x32_bf16 v[106:109], v[172:175], v[188:191], v[106:109]
	v_mfma_f32_16x16x32_bf16 v[94:97], v[164:167], v[198:201], v[94:97]
	v_mfma_f32_16x16x32_bf16 v[90:93], v[172:175], v[198:201], v[90:93]
	v_mfma_f32_16x16x32_bf16 v[78:81], v[164:167], v[206:209], v[78:81]
	v_mfma_f32_16x16x32_bf16 v[70:73], v[172:175], v[206:209], v[70:73]
	s_barrier
	s_mov_b32 m0, s82
	ds_read_b128 v[176:179], v143 offset:16384
	ds_read_b128 v[180:183], v143 offset:17408
	ds_read_b128 v[184:187], v143 offset:18432
	ds_read_b128 v[188:191], v143 offset:19456
	ds_read_b128 v[194:197], v143 offset:20480
	ds_read_b128 v[198:201], v143 offset:21504
	ds_read_b128 v[202:205], v143 offset:22528
	ds_read_b128 v[206:209], v143 offset:23552
	s_add_u32 s92, s60, 0x4000
	global_load_lds_dwordx4 v138, s[60:61]
	s_mov_b32 m0, s83
	s_addc_u32 s93, s61, 0
	global_load_lds_dwordx4 v140, s[60:61]
	s_mov_b32 m0, s84
	s_nop 0
	global_load_lds_dwordx4 v138, s[92:93]
	s_mov_b32 m0, s85
	s_nop 0
	global_load_lds_dwordx4 v140, s[92:93]
	s_mov_b32 m0, s15
	s_nop 0
	global_load_lds_dwordx4 v137, s[64:65]
	s_mov_b32 m0, s18
	s_nop 0
	global_load_lds_dwordx4 v139, s[64:65]
	s_waitcnt vmcnt(8)
	s_waitcnt lgkmcnt(0)
	s_barrier
	s_waitcnt lgkmcnt(0)
	v_mfma_f32_16x16x32_bf16 v[58:61], v[144:147], v[176:179], v[58:61]
	v_mfma_f32_16x16x32_bf16 v[50:53], v[152:155], v[176:179], v[50:53]
	v_mfma_f32_16x16x32_bf16 v[38:41], v[144:147], v[184:187], v[38:41]
	v_mfma_f32_16x16x32_bf16 v[34:37], v[152:155], v[184:187], v[34:37]
	v_mfma_f32_16x16x32_bf16 v[22:25], v[144:147], v[194:197], v[22:25]
	v_mfma_f32_16x16x32_bf16 v[18:21], v[152:155], v[194:197], v[18:21]
	v_mfma_f32_16x16x32_bf16 v[6:9], v[144:147], v[202:205], v[6:9]
	v_mfma_f32_16x16x32_bf16 v[2:5], v[152:155], v[202:205], v[2:5]
	v_mfma_f32_16x16x32_bf16 v[58:61], v[148:151], v[180:183], v[58:61]
	v_mfma_f32_16x16x32_bf16 v[50:53], v[156:159], v[180:183], v[50:53]
	v_mfma_f32_16x16x32_bf16 v[38:41], v[148:151], v[188:191], v[38:41]
	v_mfma_f32_16x16x32_bf16 v[34:37], v[156:159], v[188:191], v[34:37]
	v_mfma_f32_16x16x32_bf16 v[22:25], v[148:151], v[198:201], v[22:25]
	v_mfma_f32_16x16x32_bf16 v[18:21], v[156:159], v[198:201], v[18:21]
	v_mfma_f32_16x16x32_bf16 v[6:9], v[148:151], v[206:209], v[6:9]
	v_mfma_f32_16x16x32_bf16 v[2:5], v[156:159], v[206:209], v[2:5]
	v_mfma_f32_16x16x32_bf16 v[74:77], v[160:163], v[176:179], v[74:77]
	v_mfma_f32_16x16x32_bf16 v[66:69], v[168:171], v[176:179], v[66:69]
	v_mfma_f32_16x16x32_bf16 v[46:49], v[160:163], v[184:187], v[46:49]
	v_mfma_f32_16x16x32_bf16 v[42:45], v[168:171], v[184:187], v[42:45]
	v_mfma_f32_16x16x32_bf16 v[30:33], v[160:163], v[194:197], v[30:33]
	v_mfma_f32_16x16x32_bf16 v[26:29], v[168:171], v[194:197], v[26:29]
	v_mfma_f32_16x16x32_bf16 v[14:17], v[160:163], v[202:205], v[14:17]
	v_mfma_f32_16x16x32_bf16 v[10:13], v[168:171], v[202:205], v[10:13]
	v_mfma_f32_16x16x32_bf16 v[74:77], v[164:167], v[180:183], v[74:77]
	v_mfma_f32_16x16x32_bf16 v[66:69], v[172:175], v[180:183], v[66:69]
	v_mfma_f32_16x16x32_bf16 v[46:49], v[164:167], v[188:191], v[46:49]
	v_mfma_f32_16x16x32_bf16 v[42:45], v[172:175], v[188:191], v[42:45]
	v_mfma_f32_16x16x32_bf16 v[30:33], v[164:167], v[198:201], v[30:33]
	v_mfma_f32_16x16x32_bf16 v[26:29], v[172:175], v[198:201], v[26:29]
	v_mfma_f32_16x16x32_bf16 v[14:17], v[164:167], v[206:209], v[14:17]
	v_mfma_f32_16x16x32_bf16 v[10:13], v[172:175], v[206:209], v[10:13]
	s_barrier
	ds_read_b128 v[144:147], v134
	ds_read_b128 v[148:151], v134 offset:1024
	ds_read_b128 v[152:155], v134 offset:2048
	ds_read_b128 v[156:159], v134 offset:3072
	ds_read_b128 v[160:163], v135
	ds_read_b128 v[164:167], v135 offset:1024
	ds_read_b128 v[168:171], v135 offset:2048
	ds_read_b128 v[172:175], v135 offset:3072
	s_add_u32 s64, s64, 0x4000
	s_addc_u32 s65, s65, 0
	s_mov_b32 m0, s20
	ds_read_b128 v[176:179], v143 offset:32768
	ds_read_b128 v[180:183], v143 offset:33792
	ds_read_b128 v[184:187], v143 offset:34816
	ds_read_b128 v[188:191], v143 offset:35840
	ds_read_b128 v[194:197], v143 offset:36864
	ds_read_b128 v[198:201], v143 offset:37888
	ds_read_b128 v[202:205], v143 offset:38912
	ds_read_b128 v[206:209], v143 offset:39936
	s_nop 0
	global_load_lds_dwordx4 v137, s[64:65]
	s_mov_b32 m0, s21
	s_nop 0
	global_load_lds_dwordx4 v139, s[64:65]
	s_waitcnt vmcnt(8)
	s_waitcnt lgkmcnt(0)
	s_barrier
	s_waitcnt lgkmcnt(0)
	v_mfma_f32_16x16x32_bf16 v[118:121], v[144:147], v[176:179], v[118:121]
	v_mfma_f32_16x16x32_bf16 v[114:117], v[152:155], v[176:179], v[114:117]
	v_mfma_f32_16x16x32_bf16 v[102:105], v[144:147], v[184:187], v[102:105]
	v_mfma_f32_16x16x32_bf16 v[98:101], v[152:155], v[184:187], v[98:101]
	v_mfma_f32_16x16x32_bf16 v[86:89], v[144:147], v[194:197], v[86:89]
	v_mfma_f32_16x16x32_bf16 v[82:85], v[152:155], v[194:197], v[82:85]
	v_mfma_f32_16x16x32_bf16 v[62:65], v[144:147], v[202:205], v[62:65]
	v_mfma_f32_16x16x32_bf16 v[54:57], v[152:155], v[202:205], v[54:57]
	v_mfma_f32_16x16x32_bf16 v[118:121], v[148:151], v[180:183], v[118:121]
	v_mfma_f32_16x16x32_bf16 v[114:117], v[156:159], v[180:183], v[114:117]
	v_mfma_f32_16x16x32_bf16 v[102:105], v[148:151], v[188:191], v[102:105]
	v_mfma_f32_16x16x32_bf16 v[98:101], v[156:159], v[188:191], v[98:101]
	v_mfma_f32_16x16x32_bf16 v[86:89], v[148:151], v[198:201], v[86:89]
	v_mfma_f32_16x16x32_bf16 v[82:85], v[156:159], v[198:201], v[82:85]
	v_mfma_f32_16x16x32_bf16 v[62:65], v[148:151], v[206:209], v[62:65]
	v_mfma_f32_16x16x32_bf16 v[54:57], v[156:159], v[206:209], v[54:57]
	v_mfma_f32_16x16x32_bf16 v[126:129], v[160:163], v[176:179], v[126:129]
	v_mfma_f32_16x16x32_bf16 v[122:125], v[168:171], v[176:179], v[122:125]
	v_mfma_f32_16x16x32_bf16 v[110:113], v[160:163], v[184:187], v[110:113]
	v_mfma_f32_16x16x32_bf16 v[106:109], v[168:171], v[184:187], v[106:109]
	v_mfma_f32_16x16x32_bf16 v[94:97], v[160:163], v[194:197], v[94:97]
	v_mfma_f32_16x16x32_bf16 v[90:93], v[168:171], v[194:197], v[90:93]
	v_mfma_f32_16x16x32_bf16 v[78:81], v[160:163], v[202:205], v[78:81]
	v_mfma_f32_16x16x32_bf16 v[70:73], v[168:171], v[202:205], v[70:73]
	v_mfma_f32_16x16x32_bf16 v[126:129], v[164:167], v[180:183], v[126:129]
	v_mfma_f32_16x16x32_bf16 v[122:125], v[172:175], v[180:183], v[122:125]
	v_mfma_f32_16x16x32_bf16 v[110:113], v[164:167], v[188:191], v[110:113]
	v_mfma_f32_16x16x32_bf16 v[106:109], v[172:175], v[188:191], v[106:109]
	v_mfma_f32_16x16x32_bf16 v[94:97], v[164:167], v[198:201], v[94:97]
	v_mfma_f32_16x16x32_bf16 v[90:93], v[172:175], v[198:201], v[90:93]
	v_mfma_f32_16x16x32_bf16 v[78:81], v[164:167], v[206:209], v[78:81]
	v_mfma_f32_16x16x32_bf16 v[70:73], v[172:175], v[206:209], v[70:73]
	s_barrier
	s_mov_b32 m0, s66
	ds_read_b128 v[176:179], v143 offset:49152
	ds_read_b128 v[180:183], v143 offset:50176
	ds_read_b128 v[184:187], v143 offset:51200
	ds_read_b128 v[188:191], v143 offset:52224
	ds_read_b128 v[194:197], v143 offset:53248
	ds_read_b128 v[198:201], v143 offset:54272
	ds_read_b128 v[202:205], v143 offset:55296
	ds_read_b128 v[206:209], v143 offset:56320
	s_add_u32 s60, s60, 0xc000
	global_load_lds_dwordx4 v138, s[62:63]
	s_mov_b32 m0, s67
	s_addc_u32 s61, s61, 0
	global_load_lds_dwordx4 v140, s[62:63]
	s_mov_b32 m0, s86
	s_nop 0
	global_load_lds_dwordx4 v138, s[60:61]
	s_mov_b32 m0, s87
	s_nop 0
	global_load_lds_dwordx4 v140, s[60:61]
	s_mov_b32 m0, s69
	s_nop 0
	global_load_lds_dwordx4 v137, s[58:59]
	s_mov_b32 m0, s70
	s_nop 0
	global_load_lds_dwordx4 v139, s[58:59]
	s_waitcnt vmcnt(8)
	s_waitcnt lgkmcnt(0)
	s_barrier
	s_waitcnt lgkmcnt(0)
	v_mfma_f32_16x16x32_bf16 v[58:61], v[144:147], v[176:179], v[58:61]
	v_mfma_f32_16x16x32_bf16 v[50:53], v[152:155], v[176:179], v[50:53]
	v_mfma_f32_16x16x32_bf16 v[38:41], v[144:147], v[184:187], v[38:41]
	v_mfma_f32_16x16x32_bf16 v[34:37], v[152:155], v[184:187], v[34:37]
	v_mfma_f32_16x16x32_bf16 v[22:25], v[144:147], v[194:197], v[22:25]
	v_mfma_f32_16x16x32_bf16 v[18:21], v[152:155], v[194:197], v[18:21]
	v_mfma_f32_16x16x32_bf16 v[6:9], v[144:147], v[202:205], v[6:9]
	v_mfma_f32_16x16x32_bf16 v[2:5], v[152:155], v[202:205], v[2:5]
	v_mfma_f32_16x16x32_bf16 v[58:61], v[148:151], v[180:183], v[58:61]
	v_mfma_f32_16x16x32_bf16 v[50:53], v[156:159], v[180:183], v[50:53]
	v_mfma_f32_16x16x32_bf16 v[38:41], v[148:151], v[188:191], v[38:41]
	v_mfma_f32_16x16x32_bf16 v[34:37], v[156:159], v[188:191], v[34:37]
	v_mfma_f32_16x16x32_bf16 v[22:25], v[148:151], v[198:201], v[22:25]
	v_mfma_f32_16x16x32_bf16 v[18:21], v[156:159], v[198:201], v[18:21]
	v_mfma_f32_16x16x32_bf16 v[6:9], v[148:151], v[206:209], v[6:9]
	v_mfma_f32_16x16x32_bf16 v[2:5], v[156:159], v[206:209], v[2:5]
	v_mfma_f32_16x16x32_bf16 v[74:77], v[160:163], v[176:179], v[74:77]
	v_mfma_f32_16x16x32_bf16 v[66:69], v[168:171], v[176:179], v[66:69]
	v_mfma_f32_16x16x32_bf16 v[46:49], v[160:163], v[184:187], v[46:49]
	v_mfma_f32_16x16x32_bf16 v[42:45], v[168:171], v[184:187], v[42:45]
	v_mfma_f32_16x16x32_bf16 v[30:33], v[160:163], v[194:197], v[30:33]
	v_mfma_f32_16x16x32_bf16 v[26:29], v[168:171], v[194:197], v[26:29]
	v_mfma_f32_16x16x32_bf16 v[14:17], v[160:163], v[202:205], v[14:17]
	v_mfma_f32_16x16x32_bf16 v[10:13], v[168:171], v[202:205], v[10:13]
	v_mfma_f32_16x16x32_bf16 v[74:77], v[164:167], v[180:183], v[74:77]
	v_mfma_f32_16x16x32_bf16 v[66:69], v[172:175], v[180:183], v[66:69]
	v_mfma_f32_16x16x32_bf16 v[46:49], v[164:167], v[188:191], v[46:49]
	v_mfma_f32_16x16x32_bf16 v[42:45], v[172:175], v[188:191], v[42:45]
	v_mfma_f32_16x16x32_bf16 v[30:33], v[164:167], v[198:201], v[30:33]
	v_mfma_f32_16x16x32_bf16 v[26:29], v[172:175], v[198:201], v[26:29]
	v_mfma_f32_16x16x32_bf16 v[14:17], v[164:167], v[206:209], v[14:17]
	v_mfma_f32_16x16x32_bf16 v[10:13], v[172:175], v[206:209], v[10:13]
	s_barrier
	s_add_i32 s58, s91, 2
	s_add_u32 s89, s89, 0x10000
	s_addc_u32 s90, s90, 0
	s_add_u32 s56, s56, 0x10000
	s_addc_u32 s57, s57, 0
	s_cmp_lt_i32 s91, s25
	s_cbranch_scc0 .LBB0_282
	s_mov_b32 s91, s58
	s_branch .LBB0_278

.LBB0_306:
	s_add_i32 s68, s50, 2
	s_add_u32 s48, s46, 0x100
	s_addc_u32 s49, s47, 0
	s_add_i32 s69, 0, 0x10000
	s_cmp_eq_u32 s60, s50
	s_cselect_b32 s51, s41, s49
	s_cselect_b32 s50, s40, s48
	v_add_u32_e32 v131, s69, v133
	s_cselect_b32 s53, s43, s67
	s_cselect_b32 s52, s42, s45
	s_add_i32 s70, 0, 0x14000
	ds_read_b128 v[138:141], v131
	ds_read_b128 v[142:145], v131 offset:1024
	ds_read_b128 v[146:149], v131 offset:2048
	ds_read_b128 v[150:153], v131 offset:3072
	v_add_u32_e32 v131, s70, v133
	ds_read_b128 v[154:157], v131
	ds_read_b128 v[158:161], v131 offset:1024
	ds_read_b128 v[162:165], v131 offset:2048
	ds_read_b128 v[166:169], v131 offset:3072
	s_add_u32 s46, s46, s61
	s_addc_u32 s47, s47, s62
	s_add_i32 m0, s15, 0xc000
	ds_read_b128 v[170:173], v136
	ds_read_b128 v[174:177], v136 offset:1024
	ds_read_b128 v[178:181], v136 offset:2048
	ds_read_b128 v[182:185], v136 offset:3072
	ds_read_b128 v[186:189], v136 offset:4096
	ds_read_b128 v[194:197], v136 offset:5120
	ds_read_b128 v[198:201], v136 offset:6144
	ds_read_b128 v[202:205], v136 offset:7168
	s_nop 0
	global_load_lds_dwordx4 v0, s[46:47]
	s_add_i32 m0, s15, 0xe000
	s_nop 0
	global_load_lds_dwordx4 v130, s[46:47]
	s_waitcnt vmcnt(8)
	s_waitcnt lgkmcnt(0)
	s_barrier
	s_waitcnt lgkmcnt(0)
	v_mfma_f32_16x16x32_bf16 v[126:129], v[138:141], v[170:173], v[126:129]
	v_mfma_f32_16x16x32_bf16 v[118:121], v[146:149], v[170:173], v[118:121]
	v_mfma_f32_16x16x32_bf16 v[110:113], v[138:141], v[178:181], v[110:113]
	v_mfma_f32_16x16x32_bf16 v[102:105], v[146:149], v[178:181], v[102:105]
	v_mfma_f32_16x16x32_bf16 v[94:97], v[138:141], v[186:189], v[94:97]
	v_mfma_f32_16x16x32_bf16 v[86:89], v[146:149], v[186:189], v[86:89]
	v_mfma_f32_16x16x32_bf16 v[78:81], v[138:141], v[198:201], v[78:81]
	v_mfma_f32_16x16x32_bf16 v[70:73], v[146:149], v[198:201], v[70:73]
	v_mfma_f32_16x16x32_bf16 v[126:129], v[142:145], v[174:177], v[126:129]
	v_mfma_f32_16x16x32_bf16 v[118:121], v[150:153], v[174:177], v[118:121]
	v_mfma_f32_16x16x32_bf16 v[110:113], v[142:145], v[182:185], v[110:113]
	v_mfma_f32_16x16x32_bf16 v[102:105], v[150:153], v[182:185], v[102:105]
	v_mfma_f32_16x16x32_bf16 v[94:97], v[142:145], v[194:197], v[94:97]
	v_mfma_f32_16x16x32_bf16 v[86:89], v[150:153], v[194:197], v[86:89]
	v_mfma_f32_16x16x32_bf16 v[78:81], v[142:145], v[202:205], v[78:81]
	v_mfma_f32_16x16x32_bf16 v[70:73], v[150:153], v[202:205], v[70:73]
	v_mfma_f32_16x16x32_bf16 v[54:57], v[154:157], v[170:173], v[54:57]
	v_mfma_f32_16x16x32_bf16 v[46:49], v[162:165], v[170:173], v[46:49]
	v_mfma_f32_16x16x32_bf16 v[38:41], v[154:157], v[178:181], v[38:41]
	v_mfma_f32_16x16x32_bf16 v[30:33], v[162:165], v[178:181], v[30:33]
	v_mfma_f32_16x16x32_bf16 v[22:25], v[154:157], v[186:189], v[22:25]
	v_mfma_f32_16x16x32_bf16 v[14:17], v[162:165], v[186:189], v[14:17]
	v_mfma_f32_16x16x32_bf16 v[6:9], v[154:157], v[198:201], v[6:9]
	v_mfma_f32_16x16x32_bf16 v[2:5], v[162:165], v[198:201], v[2:5]
	v_mfma_f32_16x16x32_bf16 v[54:57], v[158:161], v[174:177], v[54:57]
	v_mfma_f32_16x16x32_bf16 v[46:49], v[166:169], v[174:177], v[46:49]
	v_mfma_f32_16x16x32_bf16 v[38:41], v[158:161], v[182:185], v[38:41]
	v_mfma_f32_16x16x32_bf16 v[30:33], v[166:169], v[182:185], v[30:33]
	v_mfma_f32_16x16x32_bf16 v[22:25], v[158:161], v[194:197], v[22:25]
	v_mfma_f32_16x16x32_bf16 v[14:17], v[166:169], v[194:197], v[14:17]
	v_mfma_f32_16x16x32_bf16 v[6:9], v[158:161], v[202:205], v[6:9]
	v_mfma_f32_16x16x32_bf16 v[2:5], v[166:169], v[202:205], v[2:5]
	s_barrier
	s_add_i32 s46, s69, s14
	s_mov_b32 m0, s46
	ds_read_b128 v[170:173], v136 offset:16384
	ds_read_b128 v[174:177], v136 offset:17408
	ds_read_b128 v[178:181], v136 offset:18432
	ds_read_b128 v[182:185], v136 offset:19456
	ds_read_b128 v[186:189], v136 offset:20480
	ds_read_b128 v[194:197], v136 offset:21504
	ds_read_b128 v[198:201], v136 offset:22528
	ds_read_b128 v[202:205], v136 offset:23552
	s_nop 0
	global_load_lds_dwordx4 v135, s[52:53]
	s_add_i32 m0, s46, 0x2000
	s_add_u32 s46, s52, 0x4000
	s_addc_u32 s47, s53, 0
	s_add_i32 s69, s70, s14
	s_nop 0
	global_load_lds_dwordx4 v134, s[52:53]
	s_mov_b32 m0, s69
	s_nop 0
	global_load_lds_dwordx4 v135, s[46:47]
	s_add_i32 m0, s69, 0x2000
	s_nop 0
	global_load_lds_dwordx4 v134, s[46:47]
	s_mov_b32 m0, s15
	s_nop 0
	global_load_lds_dwordx4 v0, s[50:51]
	s_mov_b32 m0, s18
	s_nop 0
	global_load_lds_dwordx4 v130, s[50:51]
	s_waitcnt vmcnt(8)
	s_waitcnt lgkmcnt(0)
	s_barrier
	s_waitcnt lgkmcnt(0)
	v_mfma_f32_16x16x32_bf16 v[122:125], v[138:141], v[170:173], v[122:125]
	v_mfma_f32_16x16x32_bf16 v[114:117], v[146:149], v[170:173], v[114:117]
	v_mfma_f32_16x16x32_bf16 v[106:109], v[138:141], v[178:181], v[106:109]
	v_mfma_f32_16x16x32_bf16 v[98:101], v[146:149], v[178:181], v[98:101]
	v_mfma_f32_16x16x32_bf16 v[90:93], v[138:141], v[186:189], v[90:93]
	v_mfma_f32_16x16x32_bf16 v[82:85], v[146:149], v[186:189], v[82:85]
	v_mfma_f32_16x16x32_bf16 v[74:77], v[138:141], v[198:201], v[74:77]
	v_mfma_f32_16x16x32_bf16 v[66:69], v[146:149], v[198:201], v[66:69]
	v_mfma_f32_16x16x32_bf16 v[122:125], v[142:145], v[174:177], v[122:125]
	v_mfma_f32_16x16x32_bf16 v[114:117], v[150:153], v[174:177], v[114:117]
	v_mfma_f32_16x16x32_bf16 v[106:109], v[142:145], v[182:185], v[106:109]
	v_mfma_f32_16x16x32_bf16 v[98:101], v[150:153], v[182:185], v[98:101]
	v_mfma_f32_16x16x32_bf16 v[90:93], v[142:145], v[194:197], v[90:93]
	v_mfma_f32_16x16x32_bf16 v[82:85], v[150:153], v[194:197], v[82:85]
	v_mfma_f32_16x16x32_bf16 v[74:77], v[142:145], v[202:205], v[74:77]
	v_mfma_f32_16x16x32_bf16 v[66:69], v[150:153], v[202:205], v[66:69]
	v_mfma_f32_16x16x32_bf16 v[50:53], v[154:157], v[170:173], v[50:53]
	v_mfma_f32_16x16x32_bf16 v[42:45], v[162:165], v[170:173], v[42:45]
	v_mfma_f32_16x16x32_bf16 v[34:37], v[154:157], v[178:181], v[34:37]
	v_mfma_f32_16x16x32_bf16 v[26:29], v[162:165], v[178:181], v[26:29]
	v_mfma_f32_16x16x32_bf16 v[18:21], v[154:157], v[186:189], v[18:21]
	v_mfma_f32_16x16x32_bf16 v[10:13], v[162:165], v[186:189], v[10:13]
	v_mfma_f32_16x16x32_bf16 v[58:61], v[154:157], v[198:201], v[58:61]
	v_mfma_f32_16x16x32_bf16 v[62:65], v[162:165], v[198:201], v[62:65]
	v_mfma_f32_16x16x32_bf16 v[50:53], v[158:161], v[174:177], v[50:53]
	v_mfma_f32_16x16x32_bf16 v[42:45], v[166:169], v[174:177], v[42:45]
	v_mfma_f32_16x16x32_bf16 v[34:37], v[158:161], v[182:185], v[34:37]
	v_mfma_f32_16x16x32_bf16 v[26:29], v[166:169], v[182:185], v[26:29]
	v_mfma_f32_16x16x32_bf16 v[18:21], v[158:161], v[194:197], v[18:21]
	v_mfma_f32_16x16x32_bf16 v[10:13], v[166:169], v[194:197], v[10:13]
	v_mfma_f32_16x16x32_bf16 v[58:61], v[158:161], v[202:205], v[58:61]
	v_mfma_f32_16x16x32_bf16 v[62:65], v[166:169], v[202:205], v[62:65]
	s_barrier
	s_add_i32 s69, 0, 0x18000
	v_add_u32_e32 v131, s69, v133
	s_add_i32 s70, 0, 0x1c000
	ds_read_b128 v[138:141], v131
	ds_read_b128 v[142:145], v131 offset:1024
	ds_read_b128 v[146:149], v131 offset:2048
	ds_read_b128 v[150:153], v131 offset:3072
	v_add_u32_e32 v131, s70, v133
	ds_read_b128 v[154:157], v131
	ds_read_b128 v[158:161], v131 offset:1024
	ds_read_b128 v[162:165], v131 offset:2048
	ds_read_b128 v[166:169], v131 offset:3072
	s_add_u32 s46, s50, s26
	s_addc_u32 s47, s51, s27
	s_mov_b32 m0, s20
	ds_read_b128 v[170:173], v136 offset:32768
	ds_read_b128 v[174:177], v136 offset:33792
	ds_read_b128 v[178:181], v136 offset:34816
	ds_read_b128 v[182:185], v136 offset:35840
	ds_read_b128 v[186:189], v136 offset:36864
	ds_read_b128 v[194:197], v136 offset:37888
	ds_read_b128 v[198:201], v136 offset:38912
	ds_read_b128 v[202:205], v136 offset:39936
	s_nop 0
	global_load_lds_dwordx4 v0, s[46:47]
	s_mov_b32 m0, s21
	s_nop 0
	global_load_lds_dwordx4 v130, s[46:47]
	s_waitcnt vmcnt(8)
	s_waitcnt lgkmcnt(0)
	s_barrier
	s_waitcnt lgkmcnt(0)
	v_mfma_f32_16x16x32_bf16 v[126:129], v[138:141], v[170:173], v[126:129]
	v_mfma_f32_16x16x32_bf16 v[118:121], v[146:149], v[170:173], v[118:121]
	v_mfma_f32_16x16x32_bf16 v[110:113], v[138:141], v[178:181], v[110:113]
	v_mfma_f32_16x16x32_bf16 v[102:105], v[146:149], v[178:181], v[102:105]
	v_mfma_f32_16x16x32_bf16 v[94:97], v[138:141], v[186:189], v[94:97]
	v_mfma_f32_16x16x32_bf16 v[86:89], v[146:149], v[186:189], v[86:89]
	v_mfma_f32_16x16x32_bf16 v[78:81], v[138:141], v[198:201], v[78:81]
	v_mfma_f32_16x16x32_bf16 v[70:73], v[146:149], v[198:201], v[70:73]
	v_mfma_f32_16x16x32_bf16 v[126:129], v[142:145], v[174:177], v[126:129]
	v_mfma_f32_16x16x32_bf16 v[118:121], v[150:153], v[174:177], v[118:121]
	v_mfma_f32_16x16x32_bf16 v[110:113], v[142:145], v[182:185], v[110:113]
	v_mfma_f32_16x16x32_bf16 v[102:105], v[150:153], v[182:185], v[102:105]
	v_mfma_f32_16x16x32_bf16 v[94:97], v[142:145], v[194:197], v[94:97]
	v_mfma_f32_16x16x32_bf16 v[86:89], v[150:153], v[194:197], v[86:89]
	v_mfma_f32_16x16x32_bf16 v[78:81], v[142:145], v[202:205], v[78:81]
	v_mfma_f32_16x16x32_bf16 v[70:73], v[150:153], v[202:205], v[70:73]
	v_mfma_f32_16x16x32_bf16 v[54:57], v[154:157], v[170:173], v[54:57]
	v_mfma_f32_16x16x32_bf16 v[46:49], v[162:165], v[170:173], v[46:49]
	v_mfma_f32_16x16x32_bf16 v[38:41], v[154:157], v[178:181], v[38:41]
	v_mfma_f32_16x16x32_bf16 v[30:33], v[162:165], v[178:181], v[30:33]
	v_mfma_f32_16x16x32_bf16 v[22:25], v[154:157], v[186:189], v[22:25]
	v_mfma_f32_16x16x32_bf16 v[14:17], v[162:165], v[186:189], v[14:17]
	v_mfma_f32_16x16x32_bf16 v[6:9], v[154:157], v[198:201], v[6:9]
	v_mfma_f32_16x16x32_bf16 v[2:5], v[162:165], v[198:201], v[2:5]
	v_mfma_f32_16x16x32_bf16 v[54:57], v[158:161], v[174:177], v[54:57]
	v_mfma_f32_16x16x32_bf16 v[46:49], v[166:169], v[174:177], v[46:49]
	v_mfma_f32_16x16x32_bf16 v[38:41], v[158:161], v[182:185], v[38:41]
	v_mfma_f32_16x16x32_bf16 v[30:33], v[166:169], v[182:185], v[30:33]
	v_mfma_f32_16x16x32_bf16 v[22:25], v[158:161], v[194:197], v[22:25]
	v_mfma_f32_16x16x32_bf16 v[14:17], v[166:169], v[194:197], v[14:17]
	v_mfma_f32_16x16x32_bf16 v[6:9], v[158:161], v[202:205], v[6:9]
	v_mfma_f32_16x16x32_bf16 v[2:5], v[166:169], v[202:205], v[2:5]
	s_barrier
	s_add_u32 s46, s52, 0x8000
	s_addc_u32 s47, s53, 0
	s_add_i32 s69, s69, s14
	s_mov_b32 m0, s69
	ds_read_b128 v[170:173], v136 offset:49152
	ds_read_b128 v[174:177], v136 offset:50176
	ds_read_b128 v[178:181], v136 offset:51200
	ds_read_b128 v[182:185], v136 offset:52224
	ds_read_b128 v[186:189], v136 offset:53248
	ds_read_b128 v[194:197], v136 offset:54272
	ds_read_b128 v[198:201], v136 offset:55296
	ds_read_b128 v[202:205], v136 offset:56320
	v_mov_b32_e32 v131, v1
	global_load_lds_dwordx4 v135, s[46:47]
	s_add_i32 m0, s69, 0x2000
	s_nop 0
	global_load_lds_dwordx4 v134, s[46:47]
	s_add_u32 s46, s52, 0xc000
	s_addc_u32 s47, s53, 0
	s_add_i32 s52, s70, s14
	s_mov_b32 m0, s52
	s_nop 0
	global_load_lds_dwordx4 v135, s[46:47]
	s_add_i32 m0, s52, 0x2000
	s_nop 0
	global_load_lds_dwordx4 v134, s[46:47]
	s_mov_b32 m0, s58
	v_lshl_add_u64 v[190:191], s[50:51], 0, v[0:1]
	v_lshl_add_u64 v[190:191], v[190:191], 0, s[16:17]
	global_load_lds_dwordx4 v[190:191], off
	s_mov_b32 m0, s59
	v_lshl_add_u64 v[190:191], s[50:51], 0, v[130:131]
	v_lshl_add_u64 v[190:191], v[190:191], 0, s[16:17]
	global_load_lds_dwordx4 v[190:191], off
	s_waitcnt vmcnt(8)
	s_waitcnt lgkmcnt(0)
	s_barrier
	s_waitcnt lgkmcnt(0)
	v_mfma_f32_16x16x32_bf16 v[122:125], v[138:141], v[170:173], v[122:125]
	v_mfma_f32_16x16x32_bf16 v[114:117], v[146:149], v[170:173], v[114:117]
	v_mfma_f32_16x16x32_bf16 v[106:109], v[138:141], v[178:181], v[106:109]
	v_mfma_f32_16x16x32_bf16 v[98:101], v[146:149], v[178:181], v[98:101]
	v_mfma_f32_16x16x32_bf16 v[90:93], v[138:141], v[186:189], v[90:93]
	v_mfma_f32_16x16x32_bf16 v[82:85], v[146:149], v[186:189], v[82:85]
	v_mfma_f32_16x16x32_bf16 v[74:77], v[138:141], v[198:201], v[74:77]
	v_mfma_f32_16x16x32_bf16 v[66:69], v[146:149], v[198:201], v[66:69]
	v_mfma_f32_16x16x32_bf16 v[122:125], v[142:145], v[174:177], v[122:125]
	v_mfma_f32_16x16x32_bf16 v[114:117], v[150:153], v[174:177], v[114:117]
	v_mfma_f32_16x16x32_bf16 v[106:109], v[142:145], v[182:185], v[106:109]
	v_mfma_f32_16x16x32_bf16 v[98:101], v[150:153], v[182:185], v[98:101]
	v_mfma_f32_16x16x32_bf16 v[90:93], v[142:145], v[194:197], v[90:93]
	v_mfma_f32_16x16x32_bf16 v[82:85], v[150:153], v[194:197], v[82:85]
	v_mfma_f32_16x16x32_bf16 v[74:77], v[142:145], v[202:205], v[74:77]
	v_mfma_f32_16x16x32_bf16 v[66:69], v[150:153], v[202:205], v[66:69]
	v_mfma_f32_16x16x32_bf16 v[50:53], v[154:157], v[170:173], v[50:53]
	v_mfma_f32_16x16x32_bf16 v[42:45], v[162:165], v[170:173], v[42:45]
	v_mfma_f32_16x16x32_bf16 v[34:37], v[154:157], v[178:181], v[34:37]
	v_mfma_f32_16x16x32_bf16 v[26:29], v[162:165], v[178:181], v[26:29]
	v_mfma_f32_16x16x32_bf16 v[18:21], v[154:157], v[186:189], v[18:21]
	v_mfma_f32_16x16x32_bf16 v[10:13], v[162:165], v[186:189], v[10:13]
	v_mfma_f32_16x16x32_bf16 v[58:61], v[154:157], v[198:201], v[58:61]
	v_mfma_f32_16x16x32_bf16 v[62:65], v[162:165], v[198:201], v[62:65]
	v_mfma_f32_16x16x32_bf16 v[50:53], v[158:161], v[174:177], v[50:53]
	v_mfma_f32_16x16x32_bf16 v[42:45], v[166:169], v[174:177], v[42:45]
	v_mfma_f32_16x16x32_bf16 v[34:37], v[158:161], v[182:185], v[34:37]
	v_mfma_f32_16x16x32_bf16 v[26:29], v[166:169], v[182:185], v[26:29]
	v_mfma_f32_16x16x32_bf16 v[18:21], v[158:161], v[194:197], v[18:21]
	v_mfma_f32_16x16x32_bf16 v[10:13], v[166:169], v[194:197], v[10:13]
	v_mfma_f32_16x16x32_bf16 v[58:61], v[158:161], v[202:205], v[58:61]
	v_mfma_f32_16x16x32_bf16 v[62:65], v[166:169], v[202:205], v[62:65]
	s_barrier
	s_add_u32 s45, s45, 0x10000
	s_addc_u32 s67, s67, 0
	s_cmp_ge_i32 s68, s55
	s_mov_b64 s[46:47], s[48:49]
	s_mov_b32 s50, s68
	s_cbranch_scc0 .LBB0_306

.LBB0_379:
	s_add_u32 s34, s26, 0x10000
	s_addc_u32 s35, s27, 0
	s_and_b64 s[30:31], s[46:47], exec
	s_cselect_b32 s53, s43, s35
	s_cselect_b32 s52, s42, s34
	s_add_u32 s65, s28, 0x10000
	s_addc_u32 s66, s29, 0
	s_add_u32 s30, s52, 0x8000
	s_addc_u32 s31, s53, 0
	s_add_i32 s67, 0, 0x10000
	s_and_b64 s[34:35], s[46:47], exec
	s_cselect_b32 s35, s45, s66
	s_cselect_b32 s34, s44, s65
	s_add_i32 s70, 0, 0x14000
	v_add_u32_e32 v114, s67, v236
	v_add_u32_e32 v115, s70, v236
	ds_read_b128 v[2:5], v114
	s_waitcnt lgkmcnt(0)
	ds_read_b128 v[6:9], v114 offset:1024
	ds_read_b128 v[10:13], v114 offset:2048
	ds_read_b128 v[14:17], v114 offset:3072
	ds_read_b128 v[18:21], v115
	ds_read_b128 v[22:25], v115 offset:1024
	ds_read_b128 v[26:29], v115 offset:2048
	ds_read_b128 v[30:33], v115 offset:3072
	s_add_u32 s68, s26, 0xc000
	s_addc_u32 s69, s27, 0
	s_add_i32 s65, s20, 0xc000
	s_mov_b32 m0, s65
	s_add_i32 s66, s20, 0xe000
	ds_read_b128 v[34:37], v237
	ds_read_b128 v[38:41], v237 offset:1024
	ds_read_b128 v[42:45], v237 offset:2048
	ds_read_b128 v[46:49], v237 offset:3072
	ds_read_b128 v[50:53], v237 offset:4096
	ds_read_b128 v[54:57], v237 offset:5120
	ds_read_b128 v[58:61], v237 offset:6144
	ds_read_b128 v[62:65], v237 offset:7168
	s_nop 0
	global_load_lds_dwordx4 v235, s[68:69]
	s_mov_b32 m0, s66
	s_nop 0
	global_load_lds_dwordx4 v226, s[68:69]
	s_waitcnt vmcnt(8)
	s_waitcnt lgkmcnt(0)
	s_barrier
	s_waitcnt lgkmcnt(0)
	v_mfma_f32_16x16x32_bf16 v[90:93], v[2:5], v[58:61], 0
	v_mfma_f32_16x16x32_bf16 v[66:69], v[2:5], v[34:37], 0
	v_mfma_f32_16x16x32_bf16 v[70:73], v[10:13], v[34:37], 0
	v_mfma_f32_16x16x32_bf16 v[74:77], v[2:5], v[42:45], 0
	v_mfma_f32_16x16x32_bf16 v[78:81], v[10:13], v[42:45], 0
	v_mfma_f32_16x16x32_bf16 v[82:85], v[2:5], v[50:53], 0
	v_mfma_f32_16x16x32_bf16 v[86:89], v[10:13], v[50:53], 0
	v_mfma_f32_16x16x32_bf16 v[98:101], v[6:9], v[62:65], v[90:93]
	v_mfma_f32_16x16x32_bf16 v[90:93], v[10:13], v[58:61], 0
	v_mfma_f32_16x16x32_bf16 v[66:69], v[6:9], v[38:41], v[66:69]
	v_mfma_f32_16x16x32_bf16 v[70:73], v[14:17], v[38:41], v[70:73]
	v_mfma_f32_16x16x32_bf16 v[74:77], v[6:9], v[46:49], v[74:77]
	v_mfma_f32_16x16x32_bf16 v[78:81], v[14:17], v[46:49], v[78:81]
	v_mfma_f32_16x16x32_bf16 v[82:85], v[6:9], v[54:57], v[82:85]
	v_mfma_f32_16x16x32_bf16 v[86:89], v[14:17], v[54:57], v[86:89]
	v_mfma_f32_16x16x32_bf16 v[102:105], v[14:17], v[62:65], v[90:93]
	v_mfma_f32_16x16x32_bf16 v[90:93], v[18:21], v[34:37], 0
	v_mfma_f32_16x16x32_bf16 v[34:37], v[26:29], v[34:37], 0
	v_mfma_f32_16x16x32_bf16 v[118:121], v[22:25], v[38:41], v[90:93]
	v_mfma_f32_16x16x32_bf16 v[34:37], v[30:33], v[38:41], v[34:37]
	v_mfma_f32_16x16x32_bf16 v[38:41], v[18:21], v[42:45], 0
	v_mfma_f32_16x16x32_bf16 v[42:45], v[26:29], v[42:45], 0
	v_mfma_f32_16x16x32_bf16 v[38:41], v[22:25], v[46:49], v[38:41]
	v_mfma_f32_16x16x32_bf16 v[42:45], v[30:33], v[46:49], v[42:45]
	v_mfma_f32_16x16x32_bf16 v[46:49], v[18:21], v[50:53], 0
	v_mfma_f32_16x16x32_bf16 v[50:53], v[26:29], v[50:53], 0
	v_mfma_f32_16x16x32_bf16 v[46:49], v[22:25], v[54:57], v[46:49]
	v_mfma_f32_16x16x32_bf16 v[50:53], v[30:33], v[54:57], v[50:53]
	v_mfma_f32_16x16x32_bf16 v[54:57], v[18:21], v[58:61], 0
	v_mfma_f32_16x16x32_bf16 v[58:61], v[26:29], v[58:61], 0
	v_mfma_f32_16x16x32_bf16 v[54:57], v[22:25], v[62:65], v[54:57]
	v_mfma_f32_16x16x32_bf16 v[58:61], v[30:33], v[62:65], v[58:61]
	s_barrier
	s_add_i32 s67, s67, s18
	s_add_i32 s68, s67, 0x2000
	s_mov_b32 m0, s67
	s_add_u32 s72, s34, 0x4000
	ds_read_b128 v[62:65], v237 offset:16384
	ds_read_b128 v[90:93], v237 offset:17408
	ds_read_b128 v[94:97], v237 offset:18432
	ds_read_b128 v[106:109], v237 offset:19456
	ds_read_b128 v[110:113], v237 offset:20480
	ds_read_b128 v[122:125], v237 offset:21504
	ds_read_b128 v[126:129], v237 offset:22528
	ds_read_b128 v[130:133], v237 offset:23552
	s_addc_u32 s73, s35, 0
	global_load_lds_dwordx4 v227, s[34:35]
	s_mov_b32 m0, s68
	s_add_i32 s69, s70, s18
	s_add_i32 s70, s69, 0x2000
	global_load_lds_dwordx4 v0, s[34:35]
	s_mov_b32 m0, s69
	s_nop 0
	global_load_lds_dwordx4 v227, s[72:73]
	s_mov_b32 m0, s70
	s_nop 0
	global_load_lds_dwordx4 v0, s[72:73]
	s_mov_b32 m0, s20
	s_nop 0
	global_load_lds_dwordx4 v235, s[52:53]
	s_mov_b32 m0, s25
	s_nop 0
	global_load_lds_dwordx4 v226, s[52:53]
	s_waitcnt vmcnt(8)
	s_waitcnt lgkmcnt(0)
	s_barrier
	s_waitcnt lgkmcnt(0)
	v_mfma_f32_16x16x32_bf16 v[134:137], v[2:5], v[62:65], 0
	v_mfma_f32_16x16x32_bf16 v[142:145], v[2:5], v[94:97], 0
	v_mfma_f32_16x16x32_bf16 v[150:153], v[2:5], v[110:113], 0
	v_mfma_f32_16x16x32_bf16 v[2:5], v[2:5], v[126:129], 0
	v_mfma_f32_16x16x32_bf16 v[134:137], v[6:9], v[90:93], v[134:137]
	v_mfma_f32_16x16x32_bf16 v[142:145], v[6:9], v[106:109], v[142:145]
	v_mfma_f32_16x16x32_bf16 v[150:153], v[6:9], v[122:125], v[150:153]
	v_mfma_f32_16x16x32_bf16 v[2:5], v[6:9], v[130:133], v[2:5]
	v_mfma_f32_16x16x32_bf16 v[6:9], v[10:13], v[126:129], 0
	v_mfma_f32_16x16x32_bf16 v[138:141], v[10:13], v[62:65], 0
	v_mfma_f32_16x16x32_bf16 v[146:149], v[10:13], v[94:97], 0
	v_mfma_f32_16x16x32_bf16 v[154:157], v[10:13], v[110:113], 0
	v_mfma_f32_16x16x32_bf16 v[6:9], v[14:17], v[130:133], v[6:9]
	v_mfma_f32_16x16x32_bf16 v[138:141], v[14:17], v[90:93], v[138:141]
	v_mfma_f32_16x16x32_bf16 v[146:149], v[14:17], v[106:109], v[146:149]
	v_mfma_f32_16x16x32_bf16 v[154:157], v[14:17], v[122:125], v[154:157]
	v_mfma_f32_16x16x32_bf16 v[10:13], v[18:21], v[62:65], 0
	v_mfma_f32_16x16x32_bf16 v[158:161], v[22:25], v[90:93], v[10:13]
	v_mfma_f32_16x16x32_bf16 v[10:13], v[26:29], v[62:65], 0
	v_mfma_f32_16x16x32_bf16 v[162:165], v[30:33], v[90:93], v[10:13]
	v_mfma_f32_16x16x32_bf16 v[10:13], v[18:21], v[94:97], 0
	v_mfma_f32_16x16x32_bf16 v[174:177], v[22:25], v[106:109], v[10:13]
	v_mfma_f32_16x16x32_bf16 v[10:13], v[26:29], v[94:97], 0
	v_mfma_f32_16x16x32_bf16 v[178:181], v[30:33], v[106:109], v[10:13]
	v_mfma_f32_16x16x32_bf16 v[10:13], v[18:21], v[110:113], 0
	v_mfma_f32_16x16x32_bf16 v[182:185], v[22:25], v[122:125], v[10:13]
	v_mfma_f32_16x16x32_bf16 v[10:13], v[26:29], v[110:113], 0
	v_mfma_f32_16x16x32_bf16 v[122:125], v[30:33], v[122:125], v[10:13]
	v_mfma_f32_16x16x32_bf16 v[10:13], v[18:21], v[126:129], 0
	v_mfma_f32_16x16x32_bf16 v[186:189], v[22:25], v[130:133], v[10:13]
	v_mfma_f32_16x16x32_bf16 v[10:13], v[26:29], v[126:129], 0
	v_mfma_f32_16x16x32_bf16 v[130:133], v[30:33], v[130:133], v[10:13]
	s_barrier
	s_add_i32 s71, 0, 0x18000
	s_add_i32 s74, 0, 0x1c000
	v_add_u32_e32 v116, s71, v236
	v_add_u32_e32 v117, s74, v236
	s_nop 0
	ds_read_b128 v[10:13], v116
	ds_read_b128 v[14:17], v116 offset:1024
	ds_read_b128 v[18:21], v116 offset:2048
	ds_read_b128 v[22:25], v116 offset:3072
	ds_read_b128 v[194:197], v117
	ds_read_b128 v[198:201], v117 offset:1024
	ds_read_b128 v[202:205], v117 offset:2048
	ds_read_b128 v[206:209], v117 offset:3072
	s_add_u32 s52, s52, 0x4000
	s_addc_u32 s53, s53, 0
	s_mov_b32 m0, s54
	ds_read_b128 v[26:29], v237 offset:32768
	ds_read_b128 v[30:33], v237 offset:33792
	ds_read_b128 v[62:65], v237 offset:34816
	ds_read_b128 v[210:213], v237 offset:35840
	ds_read_b128 v[214:217], v237 offset:36864
	ds_read_b128 v[218:221], v237 offset:37888
	ds_read_b128 v[222:225], v237 offset:38912
	ds_read_b128 v[238:241], v237 offset:39936
	s_nop 0
	global_load_lds_dwordx4 v235, s[52:53]
	s_mov_b32 m0, s55
	s_nop 0
	global_load_lds_dwordx4 v226, s[52:53]
	s_waitcnt vmcnt(8)
	s_waitcnt lgkmcnt(0)
	s_barrier
	s_waitcnt lgkmcnt(0)
	v_mfma_f32_16x16x32_bf16 v[66:69], v[10:13], v[26:29], v[66:69]
	v_mfma_f32_16x16x32_bf16 v[166:169], v[14:17], v[30:33], v[66:69]
	v_mfma_f32_16x16x32_bf16 v[66:69], v[18:21], v[26:29], v[70:73]
	v_mfma_f32_16x16x32_bf16 v[170:173], v[22:25], v[30:33], v[66:69]
	v_mfma_f32_16x16x32_bf16 v[66:69], v[10:13], v[62:65], v[74:77]
	v_mfma_f32_16x16x32_bf16 v[110:113], v[14:17], v[210:213], v[66:69]
	v_mfma_f32_16x16x32_bf16 v[66:69], v[18:21], v[62:65], v[78:81]
	v_mfma_f32_16x16x32_bf16 v[106:109], v[22:25], v[210:213], v[66:69]
	v_mfma_f32_16x16x32_bf16 v[66:69], v[10:13], v[214:217], v[82:85]
	v_mfma_f32_16x16x32_bf16 v[94:97], v[14:17], v[218:221], v[66:69]
	v_mfma_f32_16x16x32_bf16 v[66:69], v[18:21], v[214:217], v[86:89]
	v_mfma_f32_16x16x32_bf16 v[90:93], v[22:25], v[218:221], v[66:69]
	v_mfma_f32_16x16x32_bf16 v[66:69], v[10:13], v[222:225], v[98:101]
	v_mfma_f32_16x16x32_bf16 v[78:81], v[14:17], v[238:241], v[66:69]
	v_mfma_f32_16x16x32_bf16 v[66:69], v[18:21], v[222:225], v[102:105]
	v_mfma_f32_16x16x32_bf16 v[70:73], v[22:25], v[238:241], v[66:69]
	v_mfma_f32_16x16x32_bf16 v[66:69], v[194:197], v[26:29], v[118:121]
	v_mfma_f32_16x16x32_bf16 v[26:29], v[202:205], v[26:29], v[34:37]
	v_mfma_f32_16x16x32_bf16 v[118:121], v[206:209], v[30:33], v[26:29]
	v_mfma_f32_16x16x32_bf16 v[26:29], v[194:197], v[62:65], v[38:41]
	v_mfma_f32_16x16x32_bf16 v[102:105], v[198:201], v[210:213], v[26:29]
	v_mfma_f32_16x16x32_bf16 v[26:29], v[202:205], v[62:65], v[42:45]
	v_mfma_f32_16x16x32_bf16 v[98:101], v[206:209], v[210:213], v[26:29]
	v_mfma_f32_16x16x32_bf16 v[26:29], v[194:197], v[214:217], v[46:49]
	v_mfma_f32_16x16x32_bf16 v[86:89], v[198:201], v[218:221], v[26:29]
	v_mfma_f32_16x16x32_bf16 v[26:29], v[202:205], v[214:217], v[50:53]
	v_mfma_f32_16x16x32_bf16 v[82:85], v[206:209], v[218:221], v[26:29]
	v_mfma_f32_16x16x32_bf16 v[26:29], v[194:197], v[222:225], v[54:57]
	v_mfma_f32_16x16x32_bf16 v[62:65], v[198:201], v[238:241], v[26:29]
	v_mfma_f32_16x16x32_bf16 v[26:29], v[202:205], v[222:225], v[58:61]
	v_mfma_f32_16x16x32_bf16 v[126:129], v[198:201], v[30:33], v[66:69]
	v_mfma_f32_16x16x32_bf16 v[54:57], v[206:209], v[238:241], v[26:29]
	s_barrier
	s_add_u32 s72, s34, 0x8000
	s_addc_u32 s73, s35, 0
	s_add_i32 s52, s71, s18
	s_add_i32 s53, s52, 0x2000
	s_mov_b32 m0, s52
	s_add_u32 s34, s34, 0xc000
	ds_read_b128 v[34:37], v237 offset:49152
	ds_read_b128 v[38:41], v237 offset:50176
	ds_read_b128 v[210:213], v237 offset:51200
	ds_read_b128 v[214:217], v237 offset:52224
	ds_read_b128 v[218:221], v237 offset:53248
	ds_read_b128 v[222:225], v237 offset:54272
	ds_read_b128 v[238:241], v237 offset:55296
	ds_read_b128 v[242:245], v237 offset:56320
	s_addc_u32 s35, s35, 0
	global_load_lds_dwordx4 v227, s[72:73]
	s_mov_b32 m0, s53
	s_add_i32 s71, s74, s18
	s_nop 0
	global_load_lds_dwordx4 v0, s[72:73]
	s_mov_b32 m0, s71
	s_add_i32 s72, s71, 0x2000
	s_nop 0
	global_load_lds_dwordx4 v227, s[34:35]
	s_mov_b32 m0, s72
	s_nop 0
	global_load_lds_dwordx4 v0, s[34:35]
	s_mov_b32 m0, s58
	s_nop 0
	global_load_lds_dwordx4 v235, s[30:31]
	s_mov_b32 m0, s59
	s_nop 0
	global_load_lds_dwordx4 v226, s[30:31]
	s_waitcnt vmcnt(8)
	s_waitcnt lgkmcnt(0)
	s_barrier
	s_waitcnt lgkmcnt(0)
	v_mfma_f32_16x16x32_bf16 v[26:29], v[10:13], v[34:37], v[134:137]
	v_mfma_f32_16x16x32_bf16 v[74:77], v[14:17], v[38:41], v[26:29]
	v_mfma_f32_16x16x32_bf16 v[26:29], v[18:21], v[34:37], v[138:141]
	v_mfma_f32_16x16x32_bf16 v[66:69], v[22:25], v[38:41], v[26:29]
	v_mfma_f32_16x16x32_bf16 v[26:29], v[10:13], v[210:213], v[142:145]
	v_mfma_f32_16x16x32_bf16 v[46:49], v[14:17], v[214:217], v[26:29]
	v_mfma_f32_16x16x32_bf16 v[26:29], v[18:21], v[210:213], v[146:149]
	v_mfma_f32_16x16x32_bf16 v[42:45], v[22:25], v[214:217], v[26:29]
	v_mfma_f32_16x16x32_bf16 v[26:29], v[10:13], v[218:221], v[150:153]
	v_mfma_f32_16x16x32_bf16 v[2:5], v[10:13], v[238:241], v[2:5]
	v_mfma_f32_16x16x32_bf16 v[30:33], v[14:17], v[222:225], v[26:29]
	v_mfma_f32_16x16x32_bf16 v[26:29], v[18:21], v[218:221], v[154:157]
	v_mfma_f32_16x16x32_bf16 v[14:17], v[14:17], v[242:245], v[2:5]
	v_mfma_f32_16x16x32_bf16 v[2:5], v[18:21], v[238:241], v[6:9]
	v_mfma_f32_16x16x32_bf16 v[26:29], v[22:25], v[222:225], v[26:29]
	v_mfma_f32_16x16x32_bf16 v[10:13], v[22:25], v[242:245], v[2:5]
	v_mfma_f32_16x16x32_bf16 v[2:5], v[194:197], v[34:37], v[158:161]
	v_mfma_f32_16x16x32_bf16 v[58:61], v[198:201], v[38:41], v[2:5]
	v_mfma_f32_16x16x32_bf16 v[2:5], v[202:205], v[34:37], v[162:165]
	v_mfma_f32_16x16x32_bf16 v[50:53], v[206:209], v[38:41], v[2:5]
	v_mfma_f32_16x16x32_bf16 v[2:5], v[194:197], v[210:213], v[174:177]
	v_mfma_f32_16x16x32_bf16 v[38:41], v[198:201], v[214:217], v[2:5]
	v_mfma_f32_16x16x32_bf16 v[2:5], v[202:205], v[210:213], v[178:181]
	v_mfma_f32_16x16x32_bf16 v[34:37], v[206:209], v[214:217], v[2:5]
	v_mfma_f32_16x16x32_bf16 v[2:5], v[194:197], v[218:221], v[182:185]
	v_mfma_f32_16x16x32_bf16 v[22:25], v[198:201], v[222:225], v[2:5]
	v_mfma_f32_16x16x32_bf16 v[2:5], v[202:205], v[218:221], v[122:125]
	v_mfma_f32_16x16x32_bf16 v[18:21], v[206:209], v[222:225], v[2:5]
	v_mfma_f32_16x16x32_bf16 v[2:5], v[194:197], v[238:241], v[186:189]
	v_mfma_f32_16x16x32_bf16 v[6:9], v[198:201], v[242:245], v[2:5]
	v_mfma_f32_16x16x32_bf16 v[2:5], v[202:205], v[238:241], v[130:133]
	v_mfma_f32_16x16x32_bf16 v[2:5], v[206:209], v[242:245], v[2:5]
	s_barrier
	s_andn2_b64 vcc, exec, s[48:49]
	s_cbranch_vccnz .LBB0_382
	s_add_u32 s73, s28, 0x20000
	s_addc_u32 s74, s29, 0
	s_add_u32 s26, s26, 0x1c000
	s_addc_u32 s27, s27, 0
	s_mov_b32 s75, 4
.LBB0_381:
	ds_read_b128 v[122:125], v114
	ds_read_b128 v[130:133], v114 offset:1024
	ds_read_b128 v[134:137], v114 offset:2048
	ds_read_b128 v[138:141], v114 offset:3072
	ds_read_b128 v[142:145], v115
	ds_read_b128 v[146:149], v115 offset:1024
	ds_read_b128 v[150:153], v115 offset:2048
	ds_read_b128 v[154:157], v115 offset:3072
	s_add_u32 s28, s26, 0x4000
	s_addc_u32 s29, s27, 0
	s_cmp_eq_u32 s56, s75
	s_cselect_b32 s34, s42, s28
	s_cselect_b32 s35, s43, s29
	s_cselect_b32 s30, s44, s73
	s_cselect_b32 s31, s45, s74
	s_add_u32 s28, s34, 0x8000
	s_addc_u32 s29, s35, 0
	s_mov_b32 m0, s65
	ds_read_b128 v[158:161], v237
	ds_read_b128 v[162:165], v237 offset:1024
	ds_read_b128 v[174:177], v237 offset:2048
	ds_read_b128 v[178:181], v237 offset:3072
	ds_read_b128 v[182:185], v237 offset:4096
	ds_read_b128 v[186:189], v237 offset:5120
	ds_read_b128 v[194:197], v237 offset:6144
	ds_read_b128 v[198:201], v237 offset:7168
	s_nop 0
	global_load_lds_dwordx4 v235, s[26:27]
	s_mov_b32 m0, s66
	s_nop 0
	global_load_lds_dwordx4 v226, s[26:27]
	s_waitcnt vmcnt(8)
	s_waitcnt lgkmcnt(0)
	s_barrier
	s_waitcnt lgkmcnt(0)
	v_mfma_f32_16x16x32_bf16 v[166:169], v[122:125], v[158:161], v[166:169]
	v_mfma_f32_16x16x32_bf16 v[170:173], v[134:137], v[158:161], v[170:173]
	v_mfma_f32_16x16x32_bf16 v[110:113], v[122:125], v[174:177], v[110:113]
	v_mfma_f32_16x16x32_bf16 v[106:109], v[134:137], v[174:177], v[106:109]
	v_mfma_f32_16x16x32_bf16 v[94:97], v[122:125], v[182:185], v[94:97]
	v_mfma_f32_16x16x32_bf16 v[90:93], v[134:137], v[182:185], v[90:93]
	v_mfma_f32_16x16x32_bf16 v[78:81], v[122:125], v[194:197], v[78:81]
	v_mfma_f32_16x16x32_bf16 v[70:73], v[134:137], v[194:197], v[70:73]
	v_mfma_f32_16x16x32_bf16 v[166:169], v[130:133], v[162:165], v[166:169]
	v_mfma_f32_16x16x32_bf16 v[170:173], v[138:141], v[162:165], v[170:173]
	v_mfma_f32_16x16x32_bf16 v[110:113], v[130:133], v[178:181], v[110:113]
	v_mfma_f32_16x16x32_bf16 v[106:109], v[138:141], v[178:181], v[106:109]
	v_mfma_f32_16x16x32_bf16 v[94:97], v[130:133], v[186:189], v[94:97]
	v_mfma_f32_16x16x32_bf16 v[90:93], v[138:141], v[186:189], v[90:93]
	v_mfma_f32_16x16x32_bf16 v[78:81], v[130:133], v[198:201], v[78:81]
	v_mfma_f32_16x16x32_bf16 v[70:73], v[138:141], v[198:201], v[70:73]
	v_mfma_f32_16x16x32_bf16 v[126:129], v[142:145], v[158:161], v[126:129]
	v_mfma_f32_16x16x32_bf16 v[118:121], v[150:153], v[158:161], v[118:121]
	v_mfma_f32_16x16x32_bf16 v[102:105], v[142:145], v[174:177], v[102:105]
	v_mfma_f32_16x16x32_bf16 v[98:101], v[150:153], v[174:177], v[98:101]
	v_mfma_f32_16x16x32_bf16 v[86:89], v[142:145], v[182:185], v[86:89]
	v_mfma_f32_16x16x32_bf16 v[82:85], v[150:153], v[182:185], v[82:85]
	v_mfma_f32_16x16x32_bf16 v[62:65], v[142:145], v[194:197], v[62:65]
	v_mfma_f32_16x16x32_bf16 v[54:57], v[150:153], v[194:197], v[54:57]
	v_mfma_f32_16x16x32_bf16 v[126:129], v[146:149], v[162:165], v[126:129]
	v_mfma_f32_16x16x32_bf16 v[118:121], v[154:157], v[162:165], v[118:121]
	v_mfma_f32_16x16x32_bf16 v[102:105], v[146:149], v[178:181], v[102:105]
	v_mfma_f32_16x16x32_bf16 v[98:101], v[154:157], v[178:181], v[98:101]
	v_mfma_f32_16x16x32_bf16 v[86:89], v[146:149], v[186:189], v[86:89]
	v_mfma_f32_16x16x32_bf16 v[82:85], v[154:157], v[186:189], v[82:85]
	v_mfma_f32_16x16x32_bf16 v[62:65], v[146:149], v[198:201], v[62:65]
	v_mfma_f32_16x16x32_bf16 v[54:57], v[154:157], v[198:201], v[54:57]
	s_barrier
	s_mov_b32 m0, s67
	ds_read_b128 v[158:161], v237 offset:16384
	ds_read_b128 v[162:165], v237 offset:17408
	ds_read_b128 v[174:177], v237 offset:18432
	ds_read_b128 v[178:181], v237 offset:19456
	ds_read_b128 v[182:185], v237 offset:20480
	ds_read_b128 v[186:189], v237 offset:21504
	ds_read_b128 v[194:197], v237 offset:22528
	ds_read_b128 v[198:201], v237 offset:23552
	s_add_u32 s76, s30, 0x4000
	global_load_lds_dwordx4 v227, s[30:31]
	s_mov_b32 m0, s68
	s_addc_u32 s77, s31, 0
	global_load_lds_dwordx4 v0, s[30:31]
	s_mov_b32 m0, s69
	s_nop 0
	global_load_lds_dwordx4 v227, s[76:77]
	s_mov_b32 m0, s70
	s_nop 0
	global_load_lds_dwordx4 v0, s[76:77]
	s_mov_b32 m0, s20
	s_nop 0
	global_load_lds_dwordx4 v235, s[34:35]
	s_mov_b32 m0, s25
	s_nop 0
	global_load_lds_dwordx4 v226, s[34:35]
	s_waitcnt vmcnt(8)
	s_waitcnt lgkmcnt(0)
	s_barrier
	s_waitcnt lgkmcnt(0)
	v_mfma_f32_16x16x32_bf16 v[74:77], v[122:125], v[158:161], v[74:77]
	v_mfma_f32_16x16x32_bf16 v[66:69], v[134:137], v[158:161], v[66:69]
	v_mfma_f32_16x16x32_bf16 v[46:49], v[122:125], v[174:177], v[46:49]
	v_mfma_f32_16x16x32_bf16 v[42:45], v[134:137], v[174:177], v[42:45]
	v_mfma_f32_16x16x32_bf16 v[30:33], v[122:125], v[182:185], v[30:33]
	v_mfma_f32_16x16x32_bf16 v[26:29], v[134:137], v[182:185], v[26:29]
	v_mfma_f32_16x16x32_bf16 v[14:17], v[122:125], v[194:197], v[14:17]
	v_mfma_f32_16x16x32_bf16 v[10:13], v[134:137], v[194:197], v[10:13]
	v_mfma_f32_16x16x32_bf16 v[74:77], v[130:133], v[162:165], v[74:77]
	v_mfma_f32_16x16x32_bf16 v[66:69], v[138:141], v[162:165], v[66:69]
	v_mfma_f32_16x16x32_bf16 v[46:49], v[130:133], v[178:181], v[46:49]
	v_mfma_f32_16x16x32_bf16 v[42:45], v[138:141], v[178:181], v[42:45]
	v_mfma_f32_16x16x32_bf16 v[30:33], v[130:133], v[186:189], v[30:33]
	v_mfma_f32_16x16x32_bf16 v[26:29], v[138:141], v[186:189], v[26:29]
	v_mfma_f32_16x16x32_bf16 v[14:17], v[130:133], v[198:201], v[14:17]
	v_mfma_f32_16x16x32_bf16 v[10:13], v[138:141], v[198:201], v[10:13]
	v_mfma_f32_16x16x32_bf16 v[58:61], v[142:145], v[158:161], v[58:61]
	v_mfma_f32_16x16x32_bf16 v[50:53], v[150:153], v[158:161], v[50:53]
	v_mfma_f32_16x16x32_bf16 v[38:41], v[142:145], v[174:177], v[38:41]
	v_mfma_f32_16x16x32_bf16 v[34:37], v[150:153], v[174:177], v[34:37]
	v_mfma_f32_16x16x32_bf16 v[22:25], v[142:145], v[182:185], v[22:25]
	v_mfma_f32_16x16x32_bf16 v[18:21], v[150:153], v[182:185], v[18:21]
	v_mfma_f32_16x16x32_bf16 v[6:9], v[142:145], v[194:197], v[6:9]
	v_mfma_f32_16x16x32_bf16 v[2:5], v[150:153], v[194:197], v[2:5]
	v_mfma_f32_16x16x32_bf16 v[58:61], v[146:149], v[162:165], v[58:61]
	v_mfma_f32_16x16x32_bf16 v[50:53], v[154:157], v[162:165], v[50:53]
	v_mfma_f32_16x16x32_bf16 v[38:41], v[146:149], v[178:181], v[38:41]
	v_mfma_f32_16x16x32_bf16 v[34:37], v[154:157], v[178:181], v[34:37]
	v_mfma_f32_16x16x32_bf16 v[22:25], v[146:149], v[186:189], v[22:25]
	v_mfma_f32_16x16x32_bf16 v[18:21], v[154:157], v[186:189], v[18:21]
	v_mfma_f32_16x16x32_bf16 v[6:9], v[146:149], v[198:201], v[6:9]
	v_mfma_f32_16x16x32_bf16 v[2:5], v[154:157], v[198:201], v[2:5]
	s_barrier
	ds_read_b128 v[122:125], v116
	ds_read_b128 v[130:133], v116 offset:1024
	ds_read_b128 v[134:137], v116 offset:2048
	ds_read_b128 v[138:141], v116 offset:3072
	ds_read_b128 v[142:145], v117
	ds_read_b128 v[146:149], v117 offset:1024
	ds_read_b128 v[150:153], v117 offset:2048
	ds_read_b128 v[154:157], v117 offset:3072
	s_add_u32 s34, s34, 0x4000
	s_addc_u32 s35, s35, 0
	s_mov_b32 m0, s54
	ds_read_b128 v[158:161], v237 offset:32768
	ds_read_b128 v[162:165], v237 offset:33792
	ds_read_b128 v[174:177], v237 offset:34816
	ds_read_b128 v[178:181], v237 offset:35840
	ds_read_b128 v[182:185], v237 offset:36864
	ds_read_b128 v[186:189], v237 offset:37888
	ds_read_b128 v[194:197], v237 offset:38912
	ds_read_b128 v[198:201], v237 offset:39936
	s_nop 0
	global_load_lds_dwordx4 v235, s[34:35]
	s_mov_b32 m0, s55
	s_nop 0
	global_load_lds_dwordx4 v226, s[34:35]
	s_waitcnt vmcnt(8)
	s_waitcnt lgkmcnt(0)
	s_barrier
	s_waitcnt lgkmcnt(0)
	v_mfma_f32_16x16x32_bf16 v[166:169], v[122:125], v[158:161], v[166:169]
	v_mfma_f32_16x16x32_bf16 v[170:173], v[134:137], v[158:161], v[170:173]
	v_mfma_f32_16x16x32_bf16 v[110:113], v[122:125], v[174:177], v[110:113]
	v_mfma_f32_16x16x32_bf16 v[106:109], v[134:137], v[174:177], v[106:109]
	v_mfma_f32_16x16x32_bf16 v[94:97], v[122:125], v[182:185], v[94:97]
	v_mfma_f32_16x16x32_bf16 v[90:93], v[134:137], v[182:185], v[90:93]
	v_mfma_f32_16x16x32_bf16 v[78:81], v[122:125], v[194:197], v[78:81]
	v_mfma_f32_16x16x32_bf16 v[70:73], v[134:137], v[194:197], v[70:73]
	v_mfma_f32_16x16x32_bf16 v[166:169], v[130:133], v[162:165], v[166:169]
	v_mfma_f32_16x16x32_bf16 v[170:173], v[138:141], v[162:165], v[170:173]
	v_mfma_f32_16x16x32_bf16 v[110:113], v[130:133], v[178:181], v[110:113]
	v_mfma_f32_16x16x32_bf16 v[106:109], v[138:141], v[178:181], v[106:109]
	v_mfma_f32_16x16x32_bf16 v[94:97], v[130:133], v[186:189], v[94:97]
	v_mfma_f32_16x16x32_bf16 v[90:93], v[138:141], v[186:189], v[90:93]
	v_mfma_f32_16x16x32_bf16 v[78:81], v[130:133], v[198:201], v[78:81]
	v_mfma_f32_16x16x32_bf16 v[70:73], v[138:141], v[198:201], v[70:73]
	v_mfma_f32_16x16x32_bf16 v[126:129], v[142:145], v[158:161], v[126:129]
	v_mfma_f32_16x16x32_bf16 v[118:121], v[150:153], v[158:161], v[118:121]
	v_mfma_f32_16x16x32_bf16 v[102:105], v[142:145], v[174:177], v[102:105]
	v_mfma_f32_16x16x32_bf16 v[98:101], v[150:153], v[174:177], v[98:101]
	v_mfma_f32_16x16x32_bf16 v[86:89], v[142:145], v[182:185], v[86:89]
	v_mfma_f32_16x16x32_bf16 v[82:85], v[150:153], v[182:185], v[82:85]
	v_mfma_f32_16x16x32_bf16 v[62:65], v[142:145], v[194:197], v[62:65]
	v_mfma_f32_16x16x32_bf16 v[54:57], v[150:153], v[194:197], v[54:57]
	v_mfma_f32_16x16x32_bf16 v[126:129], v[146:149], v[162:165], v[126:129]
	v_mfma_f32_16x16x32_bf16 v[118:121], v[154:157], v[162:165], v[118:121]
	v_mfma_f32_16x16x32_bf16 v[102:105], v[146:149], v[178:181], v[102:105]
	v_mfma_f32_16x16x32_bf16 v[98:101], v[154:157], v[178:181], v[98:101]
	v_mfma_f32_16x16x32_bf16 v[86:89], v[146:149], v[186:189], v[86:89]
	v_mfma_f32_16x16x32_bf16 v[82:85], v[154:157], v[186:189], v[82:85]
	v_mfma_f32_16x16x32_bf16 v[62:65], v[146:149], v[198:201], v[62:65]
	v_mfma_f32_16x16x32_bf16 v[54:57], v[154:157], v[198:201], v[54:57]
	s_barrier
	s_add_u32 s34, s30, 0x8000
	s_mov_b32 m0, s52
	s_addc_u32 s35, s31, 0
	ds_read_b128 v[158:161], v237 offset:49152
	ds_read_b128 v[162:165], v237 offset:50176
	ds_read_b128 v[174:177], v237 offset:51200
	ds_read_b128 v[178:181], v237 offset:52224
	ds_read_b128 v[182:185], v237 offset:53248
	ds_read_b128 v[186:189], v237 offset:54272
	ds_read_b128 v[194:197], v237 offset:55296
	ds_read_b128 v[198:201], v237 offset:56320
	s_add_u32 s30, s30, 0xc000
	global_load_lds_dwordx4 v227, s[34:35]
	s_mov_b32 m0, s53
	s_addc_u32 s31, s31, 0
	global_load_lds_dwordx4 v0, s[34:35]
	s_mov_b32 m0, s71
	s_nop 0
	global_load_lds_dwordx4 v227, s[30:31]
	s_mov_b32 m0, s72
	s_nop 0
	global_load_lds_dwordx4 v0, s[30:31]
	s_mov_b32 m0, s58
	s_nop 0
	global_load_lds_dwordx4 v235, s[28:29]
	s_mov_b32 m0, s59
	s_nop 0
	global_load_lds_dwordx4 v226, s[28:29]
	s_waitcnt vmcnt(8)
	s_waitcnt lgkmcnt(0)
	s_barrier
	s_waitcnt lgkmcnt(0)
	v_mfma_f32_16x16x32_bf16 v[74:77], v[122:125], v[158:161], v[74:77]
	v_mfma_f32_16x16x32_bf16 v[66:69], v[134:137], v[158:161], v[66:69]
	v_mfma_f32_16x16x32_bf16 v[46:49], v[122:125], v[174:177], v[46:49]
	v_mfma_f32_16x16x32_bf16 v[42:45], v[134:137], v[174:177], v[42:45]
	v_mfma_f32_16x16x32_bf16 v[30:33], v[122:125], v[182:185], v[30:33]
	v_mfma_f32_16x16x32_bf16 v[26:29], v[134:137], v[182:185], v[26:29]
	v_mfma_f32_16x16x32_bf16 v[14:17], v[122:125], v[194:197], v[14:17]
	v_mfma_f32_16x16x32_bf16 v[10:13], v[134:137], v[194:197], v[10:13]
	v_mfma_f32_16x16x32_bf16 v[74:77], v[130:133], v[162:165], v[74:77]
	v_mfma_f32_16x16x32_bf16 v[66:69], v[138:141], v[162:165], v[66:69]
	v_mfma_f32_16x16x32_bf16 v[46:49], v[130:133], v[178:181], v[46:49]
	v_mfma_f32_16x16x32_bf16 v[42:45], v[138:141], v[178:181], v[42:45]
	v_mfma_f32_16x16x32_bf16 v[30:33], v[130:133], v[186:189], v[30:33]
	v_mfma_f32_16x16x32_bf16 v[26:29], v[138:141], v[186:189], v[26:29]
	v_mfma_f32_16x16x32_bf16 v[14:17], v[130:133], v[198:201], v[14:17]
	v_mfma_f32_16x16x32_bf16 v[10:13], v[138:141], v[198:201], v[10:13]
	v_mfma_f32_16x16x32_bf16 v[58:61], v[142:145], v[158:161], v[58:61]
	v_mfma_f32_16x16x32_bf16 v[50:53], v[150:153], v[158:161], v[50:53]
	v_mfma_f32_16x16x32_bf16 v[38:41], v[142:145], v[174:177], v[38:41]
	v_mfma_f32_16x16x32_bf16 v[34:37], v[150:153], v[174:177], v[34:37]
	v_mfma_f32_16x16x32_bf16 v[22:25], v[142:145], v[182:185], v[22:25]
	v_mfma_f32_16x16x32_bf16 v[18:21], v[150:153], v[182:185], v[18:21]
	v_mfma_f32_16x16x32_bf16 v[6:9], v[142:145], v[194:197], v[6:9]
	v_mfma_f32_16x16x32_bf16 v[2:5], v[150:153], v[194:197], v[2:5]
	v_mfma_f32_16x16x32_bf16 v[58:61], v[146:149], v[162:165], v[58:61]
	v_mfma_f32_16x16x32_bf16 v[50:53], v[154:157], v[162:165], v[50:53]
	v_mfma_f32_16x16x32_bf16 v[38:41], v[146:149], v[178:181], v[38:41]
	v_mfma_f32_16x16x32_bf16 v[34:37], v[154:157], v[178:181], v[34:37]
	v_mfma_f32_16x16x32_bf16 v[22:25], v[146:149], v[186:189], v[22:25]
	v_mfma_f32_16x16x32_bf16 v[18:21], v[154:157], v[186:189], v[18:21]
	v_mfma_f32_16x16x32_bf16 v[6:9], v[146:149], v[198:201], v[6:9]
	v_mfma_f32_16x16x32_bf16 v[2:5], v[154:157], v[198:201], v[2:5]
	s_barrier
	s_add_i32 s28, s75, 2
	s_add_u32 s73, s73, 0x10000
	s_addc_u32 s74, s74, 0
	s_add_u32 s26, s26, 0x10000
	s_addc_u32 s27, s27, 0
	s_cmp_lt_i32 s75, s56
	s_mov_b32 s75, s28
	s_cbranch_scc1 .LBB0_381

.LBB0_454:
	s_or_b64 exec, exec, s[34:35]
	s_add_i32 s11, s11, 2
	s_add_u32 s18, s28, 0x4000
	s_addc_u32 s20, s29, 0
	s_and_b64 s[14:15], s[30:31], exec
	s_cselect_b32 s64, s18, s46
	s_cselect_b32 s65, s20, s47
	s_cselect_b32 s35, s2, s63
	s_cselect_b32 s34, s1, s62
	s_add_u32 s30, s64, 0x8000
	s_addc_u32 s31, s65, 0
	s_add_u32 s38, s34, 0x8000
	s_addc_u32 s39, s35, 0
	s_add_i32 s14, 0, 0x10000
	v_add_u32_e32 v149, s14, v146
	s_add_i32 s18, 0, 0x14000
	ds_read_b128 v[132:135], v149
	ds_read_b128 v[136:139], v149 offset:1024
	ds_read_b128 v[150:153], v149 offset:2048
	ds_read_b128 v[154:157], v149 offset:3072
	v_add_u32_e32 v149, s18, v146
	ds_read_b128 v[158:161], v149
	ds_read_b128 v[162:165], v149 offset:1024
	ds_read_b128 v[166:169], v149 offset:2048
	ds_read_b128 v[170:173], v149 offset:3072
	s_add_i32 m0, s71, 0xc000
	ds_read_b128 v[174:177], v148
	ds_read_b128 v[178:181], v148 offset:1024
	ds_read_b128 v[182:185], v148 offset:2048
	ds_read_b128 v[186:189], v148 offset:3072
	ds_read_b128 v[194:197], v148 offset:4096
	ds_read_b128 v[198:201], v148 offset:5120
	ds_read_b128 v[202:205], v148 offset:6144
	ds_read_b128 v[206:209], v148 offset:7168
	s_nop 0
	global_load_lds_dwordx4 v142, s[28:29]
	s_add_i32 m0, s71, 0xe000
	s_nop 0
	global_load_lds_dwordx4 v144, s[28:29]
	s_waitcnt vmcnt(8)
	s_waitcnt lgkmcnt(0)
	s_barrier
	s_waitcnt lgkmcnt(0)
	v_mfma_f32_16x16x32_bf16 v[66:69], v[132:135], v[174:177], v[66:69]
	v_mfma_f32_16x16x32_bf16 v[70:73], v[150:153], v[174:177], v[70:73]
	v_mfma_f32_16x16x32_bf16 v[58:61], v[132:135], v[182:185], v[58:61]
	v_mfma_f32_16x16x32_bf16 v[62:65], v[150:153], v[182:185], v[62:65]
	v_mfma_f32_16x16x32_bf16 v[50:53], v[132:135], v[194:197], v[50:53]
	v_mfma_f32_16x16x32_bf16 v[54:57], v[150:153], v[194:197], v[54:57]
	v_mfma_f32_16x16x32_bf16 v[42:45], v[132:135], v[202:205], v[42:45]
	v_mfma_f32_16x16x32_bf16 v[46:49], v[150:153], v[202:205], v[46:49]
	v_mfma_f32_16x16x32_bf16 v[66:69], v[136:139], v[178:181], v[66:69]
	v_mfma_f32_16x16x32_bf16 v[70:73], v[154:157], v[178:181], v[70:73]
	v_mfma_f32_16x16x32_bf16 v[58:61], v[136:139], v[186:189], v[58:61]
	v_mfma_f32_16x16x32_bf16 v[62:65], v[154:157], v[186:189], v[62:65]
	v_mfma_f32_16x16x32_bf16 v[50:53], v[136:139], v[198:201], v[50:53]
	v_mfma_f32_16x16x32_bf16 v[54:57], v[154:157], v[198:201], v[54:57]
	v_mfma_f32_16x16x32_bf16 v[42:45], v[136:139], v[206:209], v[42:45]
	v_mfma_f32_16x16x32_bf16 v[46:49], v[154:157], v[206:209], v[46:49]
	v_mfma_f32_16x16x32_bf16 v[126:129], v[158:161], v[174:177], v[126:129]
	v_mfma_f32_16x16x32_bf16 v[122:125], v[166:169], v[174:177], v[122:125]
	v_mfma_f32_16x16x32_bf16 v[118:121], v[158:161], v[182:185], v[118:121]
	v_mfma_f32_16x16x32_bf16 v[114:117], v[166:169], v[182:185], v[114:117]
	v_mfma_f32_16x16x32_bf16 v[110:113], v[158:161], v[194:197], v[110:113]
	v_mfma_f32_16x16x32_bf16 v[106:109], v[166:169], v[194:197], v[106:109]
	v_mfma_f32_16x16x32_bf16 v[94:97], v[158:161], v[202:205], v[94:97]
	v_mfma_f32_16x16x32_bf16 v[90:93], v[166:169], v[202:205], v[90:93]
	v_mfma_f32_16x16x32_bf16 v[126:129], v[162:165], v[178:181], v[126:129]
	v_mfma_f32_16x16x32_bf16 v[122:125], v[170:173], v[178:181], v[122:125]
	v_mfma_f32_16x16x32_bf16 v[118:121], v[162:165], v[186:189], v[118:121]
	v_mfma_f32_16x16x32_bf16 v[114:117], v[170:173], v[186:189], v[114:117]
	v_mfma_f32_16x16x32_bf16 v[110:113], v[162:165], v[198:201], v[110:113]
	v_mfma_f32_16x16x32_bf16 v[106:109], v[170:173], v[198:201], v[106:109]
	v_mfma_f32_16x16x32_bf16 v[94:97], v[162:165], v[206:209], v[94:97]
	v_mfma_f32_16x16x32_bf16 v[90:93], v[170:173], v[206:209], v[90:93]
	s_barrier
	s_add_i32 s14, s14, s70
	s_mov_b32 m0, s14
	ds_read_b128 v[174:177], v148 offset:16384
	ds_read_b128 v[178:181], v148 offset:17408
	ds_read_b128 v[182:185], v148 offset:18432
	ds_read_b128 v[186:189], v148 offset:19456
	ds_read_b128 v[194:197], v148 offset:20480
	ds_read_b128 v[198:201], v148 offset:21504
	ds_read_b128 v[202:205], v148 offset:22528
	ds_read_b128 v[206:209], v148 offset:23552
	s_nop 0
	global_load_lds_dwordx4 v143, s[34:35]
	s_add_i32 m0, s14, 0x2000
	s_add_u32 s14, s34, 0x4000
	s_addc_u32 s15, s35, 0
	s_add_i32 s18, s18, s70
	s_nop 0
	global_load_lds_dwordx4 v145, s[34:35]
	s_mov_b32 m0, s18
	s_nop 0
	global_load_lds_dwordx4 v143, s[14:15]
	s_add_i32 m0, s18, 0x2000
	s_nop 0
	global_load_lds_dwordx4 v145, s[14:15]
	s_mov_b32 m0, s71
	s_nop 0
	global_load_lds_dwordx4 v142, s[64:65]
	s_mov_b32 m0, s72
	s_nop 0
	global_load_lds_dwordx4 v144, s[64:65]
	s_waitcnt vmcnt(8)
	s_waitcnt lgkmcnt(0)
	s_barrier
	s_waitcnt lgkmcnt(0)
	v_mfma_f32_16x16x32_bf16 v[26:29], v[132:135], v[174:177], v[26:29]
	v_mfma_f32_16x16x32_bf16 v[30:33], v[150:153], v[174:177], v[30:33]
	v_mfma_f32_16x16x32_bf16 v[18:21], v[132:135], v[182:185], v[18:21]
	v_mfma_f32_16x16x32_bf16 v[22:25], v[150:153], v[182:185], v[22:25]
	v_mfma_f32_16x16x32_bf16 v[10:13], v[132:135], v[194:197], v[10:13]
	v_mfma_f32_16x16x32_bf16 v[14:17], v[150:153], v[194:197], v[14:17]
	v_mfma_f32_16x16x32_bf16 v[2:5], v[132:135], v[202:205], v[2:5]
	v_mfma_f32_16x16x32_bf16 v[6:9], v[150:153], v[202:205], v[6:9]
	v_mfma_f32_16x16x32_bf16 v[26:29], v[136:139], v[178:181], v[26:29]
	v_mfma_f32_16x16x32_bf16 v[30:33], v[154:157], v[178:181], v[30:33]
	v_mfma_f32_16x16x32_bf16 v[18:21], v[136:139], v[186:189], v[18:21]
	v_mfma_f32_16x16x32_bf16 v[22:25], v[154:157], v[186:189], v[22:25]
	v_mfma_f32_16x16x32_bf16 v[10:13], v[136:139], v[198:201], v[10:13]
	v_mfma_f32_16x16x32_bf16 v[14:17], v[154:157], v[198:201], v[14:17]
	v_mfma_f32_16x16x32_bf16 v[2:5], v[136:139], v[206:209], v[2:5]
	v_mfma_f32_16x16x32_bf16 v[6:9], v[154:157], v[206:209], v[6:9]
	v_mfma_f32_16x16x32_bf16 v[102:105], v[158:161], v[174:177], v[102:105]
	v_mfma_f32_16x16x32_bf16 v[98:101], v[166:169], v[174:177], v[98:101]
	v_mfma_f32_16x16x32_bf16 v[82:85], v[158:161], v[182:185], v[82:85]
	v_mfma_f32_16x16x32_bf16 v[86:89], v[166:169], v[182:185], v[86:89]
	v_mfma_f32_16x16x32_bf16 v[78:81], v[158:161], v[194:197], v[78:81]
	v_mfma_f32_16x16x32_bf16 v[74:77], v[166:169], v[194:197], v[74:77]
	v_mfma_f32_16x16x32_bf16 v[34:37], v[158:161], v[202:205], v[34:37]
	v_mfma_f32_16x16x32_bf16 v[38:41], v[166:169], v[202:205], v[38:41]
	v_mfma_f32_16x16x32_bf16 v[102:105], v[162:165], v[178:181], v[102:105]
	v_mfma_f32_16x16x32_bf16 v[98:101], v[170:173], v[178:181], v[98:101]
	v_mfma_f32_16x16x32_bf16 v[82:85], v[162:165], v[186:189], v[82:85]
	v_mfma_f32_16x16x32_bf16 v[86:89], v[170:173], v[186:189], v[86:89]
	v_mfma_f32_16x16x32_bf16 v[78:81], v[162:165], v[198:201], v[78:81]
	v_mfma_f32_16x16x32_bf16 v[74:77], v[170:173], v[198:201], v[74:77]
	v_mfma_f32_16x16x32_bf16 v[34:37], v[162:165], v[206:209], v[34:37]
	v_mfma_f32_16x16x32_bf16 v[38:41], v[170:173], v[206:209], v[38:41]
	s_barrier
	s_add_i32 s18, 0, 0x18000
	v_add_u32_e32 v149, s18, v146
	s_add_i32 s20, 0, 0x1c000
	ds_read_b128 v[132:135], v149
	ds_read_b128 v[136:139], v149 offset:1024
	ds_read_b128 v[150:153], v149 offset:2048
	ds_read_b128 v[154:157], v149 offset:3072
	v_add_u32_e32 v149, s20, v146
	ds_read_b128 v[158:161], v149
	ds_read_b128 v[162:165], v149 offset:1024
	ds_read_b128 v[166:169], v149 offset:2048
	ds_read_b128 v[170:173], v149 offset:3072
	s_add_u32 s14, s64, 0x4000
	s_addc_u32 s15, s65, 0
	s_mov_b32 m0, s73
	ds_read_b128 v[174:177], v148 offset:32768
	ds_read_b128 v[178:181], v148 offset:33792
	ds_read_b128 v[182:185], v148 offset:34816
	ds_read_b128 v[186:189], v148 offset:35840
	ds_read_b128 v[194:197], v148 offset:36864
	ds_read_b128 v[198:201], v148 offset:37888
	ds_read_b128 v[202:205], v148 offset:38912
	ds_read_b128 v[206:209], v148 offset:39936
	s_nop 0
	global_load_lds_dwordx4 v142, s[14:15]
	s_mov_b32 m0, s74
	s_nop 0
	global_load_lds_dwordx4 v144, s[14:15]
	s_waitcnt vmcnt(8)
	s_waitcnt lgkmcnt(0)
	s_barrier
	s_waitcnt lgkmcnt(0)
	v_mfma_f32_16x16x32_bf16 v[66:69], v[132:135], v[174:177], v[66:69]
	v_mfma_f32_16x16x32_bf16 v[70:73], v[150:153], v[174:177], v[70:73]
	v_mfma_f32_16x16x32_bf16 v[58:61], v[132:135], v[182:185], v[58:61]
	v_mfma_f32_16x16x32_bf16 v[62:65], v[150:153], v[182:185], v[62:65]
	v_mfma_f32_16x16x32_bf16 v[50:53], v[132:135], v[194:197], v[50:53]
	v_mfma_f32_16x16x32_bf16 v[54:57], v[150:153], v[194:197], v[54:57]
	v_mfma_f32_16x16x32_bf16 v[42:45], v[132:135], v[202:205], v[42:45]
	v_mfma_f32_16x16x32_bf16 v[46:49], v[150:153], v[202:205], v[46:49]
	v_mfma_f32_16x16x32_bf16 v[66:69], v[136:139], v[178:181], v[66:69]
	v_mfma_f32_16x16x32_bf16 v[70:73], v[154:157], v[178:181], v[70:73]
	v_mfma_f32_16x16x32_bf16 v[58:61], v[136:139], v[186:189], v[58:61]
	v_mfma_f32_16x16x32_bf16 v[62:65], v[154:157], v[186:189], v[62:65]
	v_mfma_f32_16x16x32_bf16 v[50:53], v[136:139], v[198:201], v[50:53]
	v_mfma_f32_16x16x32_bf16 v[54:57], v[154:157], v[198:201], v[54:57]
	v_mfma_f32_16x16x32_bf16 v[42:45], v[136:139], v[206:209], v[42:45]
	v_mfma_f32_16x16x32_bf16 v[46:49], v[154:157], v[206:209], v[46:49]
	v_mfma_f32_16x16x32_bf16 v[126:129], v[158:161], v[174:177], v[126:129]
	v_mfma_f32_16x16x32_bf16 v[122:125], v[166:169], v[174:177], v[122:125]
	v_mfma_f32_16x16x32_bf16 v[118:121], v[158:161], v[182:185], v[118:121]
	v_mfma_f32_16x16x32_bf16 v[114:117], v[166:169], v[182:185], v[114:117]
	v_mfma_f32_16x16x32_bf16 v[110:113], v[158:161], v[194:197], v[110:113]
	v_mfma_f32_16x16x32_bf16 v[106:109], v[166:169], v[194:197], v[106:109]
	v_mfma_f32_16x16x32_bf16 v[94:97], v[158:161], v[202:205], v[94:97]
	v_mfma_f32_16x16x32_bf16 v[90:93], v[166:169], v[202:205], v[90:93]
	v_mfma_f32_16x16x32_bf16 v[126:129], v[162:165], v[178:181], v[126:129]
	v_mfma_f32_16x16x32_bf16 v[122:125], v[170:173], v[178:181], v[122:125]
	v_mfma_f32_16x16x32_bf16 v[118:121], v[162:165], v[186:189], v[118:121]
	v_mfma_f32_16x16x32_bf16 v[114:117], v[170:173], v[186:189], v[114:117]
	v_mfma_f32_16x16x32_bf16 v[110:113], v[162:165], v[198:201], v[110:113]
	v_mfma_f32_16x16x32_bf16 v[106:109], v[170:173], v[198:201], v[106:109]
	v_mfma_f32_16x16x32_bf16 v[94:97], v[162:165], v[206:209], v[94:97]
	v_mfma_f32_16x16x32_bf16 v[90:93], v[170:173], v[206:209], v[90:93]
	s_barrier
	s_add_i32 s14, s18, s70
	s_mov_b32 m0, s14
	ds_read_b128 v[174:177], v148 offset:49152
	ds_read_b128 v[178:181], v148 offset:50176
	ds_read_b128 v[182:185], v148 offset:51200
	ds_read_b128 v[186:189], v148 offset:52224
	ds_read_b128 v[194:197], v148 offset:53248
	ds_read_b128 v[198:201], v148 offset:54272
	ds_read_b128 v[202:205], v148 offset:55296
	ds_read_b128 v[206:209], v148 offset:56320
	s_nop 0
	global_load_lds_dwordx4 v143, s[38:39]
	s_add_i32 m0, s14, 0x2000
	s_add_u32 s14, s34, 0xc000
	s_addc_u32 s15, s35, 0
	s_add_i32 s18, s20, s70
	s_nop 0
	global_load_lds_dwordx4 v145, s[38:39]
	s_mov_b32 m0, s18
	s_nop 0
	global_load_lds_dwordx4 v143, s[14:15]
	s_add_i32 m0, s18, 0x2000
	s_nop 0
	global_load_lds_dwordx4 v145, s[14:15]
	s_mov_b32 m0, s81
	s_nop 0
	global_load_lds_dwordx4 v142, s[30:31]
	s_mov_b32 m0, s82
	s_nop 0
	global_load_lds_dwordx4 v144, s[30:31]
	s_waitcnt vmcnt(8)
	s_waitcnt lgkmcnt(0)
	s_barrier
	s_waitcnt lgkmcnt(0)
	v_mfma_f32_16x16x32_bf16 v[26:29], v[132:135], v[174:177], v[26:29]
	v_mfma_f32_16x16x32_bf16 v[30:33], v[150:153], v[174:177], v[30:33]
	v_mfma_f32_16x16x32_bf16 v[18:21], v[132:135], v[182:185], v[18:21]
	v_mfma_f32_16x16x32_bf16 v[22:25], v[150:153], v[182:185], v[22:25]
	v_mfma_f32_16x16x32_bf16 v[10:13], v[132:135], v[194:197], v[10:13]
	v_mfma_f32_16x16x32_bf16 v[14:17], v[150:153], v[194:197], v[14:17]
	v_mfma_f32_16x16x32_bf16 v[2:5], v[132:135], v[202:205], v[2:5]
	v_mfma_f32_16x16x32_bf16 v[6:9], v[150:153], v[202:205], v[6:9]
	v_mfma_f32_16x16x32_bf16 v[26:29], v[136:139], v[178:181], v[26:29]
	v_mfma_f32_16x16x32_bf16 v[30:33], v[154:157], v[178:181], v[30:33]
	v_mfma_f32_16x16x32_bf16 v[18:21], v[136:139], v[186:189], v[18:21]
	v_mfma_f32_16x16x32_bf16 v[22:25], v[154:157], v[186:189], v[22:25]
	v_mfma_f32_16x16x32_bf16 v[10:13], v[136:139], v[198:201], v[10:13]
	v_mfma_f32_16x16x32_bf16 v[14:17], v[154:157], v[198:201], v[14:17]
	v_mfma_f32_16x16x32_bf16 v[2:5], v[136:139], v[206:209], v[2:5]
	v_mfma_f32_16x16x32_bf16 v[6:9], v[154:157], v[206:209], v[6:9]
	v_mfma_f32_16x16x32_bf16 v[102:105], v[158:161], v[174:177], v[102:105]
	v_mfma_f32_16x16x32_bf16 v[98:101], v[166:169], v[174:177], v[98:101]
	v_mfma_f32_16x16x32_bf16 v[82:85], v[158:161], v[182:185], v[82:85]
	v_mfma_f32_16x16x32_bf16 v[86:89], v[166:169], v[182:185], v[86:89]
	v_mfma_f32_16x16x32_bf16 v[78:81], v[158:161], v[194:197], v[78:81]
	v_mfma_f32_16x16x32_bf16 v[74:77], v[166:169], v[194:197], v[74:77]
	v_mfma_f32_16x16x32_bf16 v[34:37], v[158:161], v[202:205], v[34:37]
	v_mfma_f32_16x16x32_bf16 v[38:41], v[166:169], v[202:205], v[38:41]
	v_mfma_f32_16x16x32_bf16 v[102:105], v[162:165], v[178:181], v[102:105]
	v_mfma_f32_16x16x32_bf16 v[98:101], v[170:173], v[178:181], v[98:101]
	v_mfma_f32_16x16x32_bf16 v[82:85], v[162:165], v[186:189], v[82:85]
	v_mfma_f32_16x16x32_bf16 v[86:89], v[170:173], v[186:189], v[86:89]
	v_mfma_f32_16x16x32_bf16 v[78:81], v[162:165], v[198:201], v[78:81]
	v_mfma_f32_16x16x32_bf16 v[74:77], v[170:173], v[198:201], v[74:77]
	v_mfma_f32_16x16x32_bf16 v[34:37], v[162:165], v[206:209], v[34:37]
	v_mfma_f32_16x16x32_bf16 v[38:41], v[170:173], v[206:209], v[38:41]
	s_barrier
	s_add_u32 s1, s1, 0x10000
	s_addc_u32 s2, s2, 0
	s_add_u32 s28, s28, 0x10000
	s_addc_u32 s29, s29, 0
	s_cmp_ge_i32 s11, s78
	s_cbranch_scc1 .LBB0_457

.LBB0_498:
	s_add_i32 s83, s52, 2
	s_add_u32 s50, s48, 0x100
	s_addc_u32 s51, s49, 0
	s_add_i32 s84, 0, 0x10000
	s_cmp_eq_u32 s71, s52
	s_cselect_b32 s53, s43, s51
	s_cselect_b32 s52, s42, s50
	v_add_u32_e32 v131, s84, v137
	s_cselect_b32 s55, s47, s82
	s_cselect_b32 s54, s46, s81
	s_add_i32 s85, 0, 0x14000
	ds_read_b128 v[142:145], v131
	ds_read_b128 v[146:149], v131 offset:1024
	ds_read_b128 v[150:153], v131 offset:2048
	ds_read_b128 v[154:157], v131 offset:3072
	v_add_u32_e32 v131, s85, v137
	ds_read_b128 v[158:161], v131
	ds_read_b128 v[162:165], v131 offset:1024
	ds_read_b128 v[166:169], v131 offset:2048
	ds_read_b128 v[170:173], v131 offset:3072
	s_add_u32 s48, s48, s74
	s_addc_u32 s49, s49, s75
	s_add_i32 m0, s62, 0xc000
	ds_read_b128 v[174:177], v138
	ds_read_b128 v[178:181], v138 offset:1024
	ds_read_b128 v[182:185], v138 offset:2048
	ds_read_b128 v[186:189], v138 offset:3072
	ds_read_b128 v[194:197], v138 offset:4096
	ds_read_b128 v[198:201], v138 offset:5120
	ds_read_b128 v[202:205], v138 offset:6144
	ds_read_b128 v[206:209], v138 offset:7168
	s_nop 0
	global_load_lds_dwordx4 v130, s[48:49]
	s_add_i32 m0, s62, 0xe000
	s_nop 0
	global_load_lds_dwordx4 v132, s[48:49]
	s_waitcnt vmcnt(8)
	s_waitcnt lgkmcnt(0)
	s_barrier
	s_waitcnt lgkmcnt(0)
	v_mfma_f32_16x16x32_bf16 v[118:121], v[142:145], v[174:177], v[118:121]
	v_mfma_f32_16x16x32_bf16 v[114:117], v[150:153], v[174:177], v[114:117]
	v_mfma_f32_16x16x32_bf16 v[102:105], v[142:145], v[182:185], v[102:105]
	v_mfma_f32_16x16x32_bf16 v[98:101], v[150:153], v[182:185], v[98:101]
	v_mfma_f32_16x16x32_bf16 v[86:89], v[142:145], v[194:197], v[86:89]
	v_mfma_f32_16x16x32_bf16 v[82:85], v[150:153], v[194:197], v[82:85]
	v_mfma_f32_16x16x32_bf16 v[70:73], v[142:145], v[202:205], v[70:73]
	v_mfma_f32_16x16x32_bf16 v[66:69], v[150:153], v[202:205], v[66:69]
	v_mfma_f32_16x16x32_bf16 v[118:121], v[146:149], v[178:181], v[118:121]
	v_mfma_f32_16x16x32_bf16 v[114:117], v[154:157], v[178:181], v[114:117]
	v_mfma_f32_16x16x32_bf16 v[102:105], v[146:149], v[186:189], v[102:105]
	v_mfma_f32_16x16x32_bf16 v[98:101], v[154:157], v[186:189], v[98:101]
	v_mfma_f32_16x16x32_bf16 v[86:89], v[146:149], v[198:201], v[86:89]
	v_mfma_f32_16x16x32_bf16 v[82:85], v[154:157], v[198:201], v[82:85]
	v_mfma_f32_16x16x32_bf16 v[70:73], v[146:149], v[206:209], v[70:73]
	v_mfma_f32_16x16x32_bf16 v[66:69], v[154:157], v[206:209], v[66:69]
	v_mfma_f32_16x16x32_bf16 v[46:49], v[158:161], v[174:177], v[46:49]
	v_mfma_f32_16x16x32_bf16 v[42:45], v[166:169], v[174:177], v[42:45]
	v_mfma_f32_16x16x32_bf16 v[30:33], v[158:161], v[182:185], v[30:33]
	v_mfma_f32_16x16x32_bf16 v[26:29], v[166:169], v[182:185], v[26:29]
	v_mfma_f32_16x16x32_bf16 v[14:17], v[158:161], v[194:197], v[14:17]
	v_mfma_f32_16x16x32_bf16 v[10:13], v[166:169], v[194:197], v[10:13]
	v_mfma_f32_16x16x32_bf16 v[6:9], v[158:161], v[202:205], v[6:9]
	v_mfma_f32_16x16x32_bf16 v[2:5], v[166:169], v[202:205], v[2:5]
	v_mfma_f32_16x16x32_bf16 v[46:49], v[162:165], v[178:181], v[46:49]
	v_mfma_f32_16x16x32_bf16 v[42:45], v[170:173], v[178:181], v[42:45]
	v_mfma_f32_16x16x32_bf16 v[30:33], v[162:165], v[186:189], v[30:33]
	v_mfma_f32_16x16x32_bf16 v[26:29], v[170:173], v[186:189], v[26:29]
	v_mfma_f32_16x16x32_bf16 v[14:17], v[162:165], v[198:201], v[14:17]
	v_mfma_f32_16x16x32_bf16 v[10:13], v[170:173], v[198:201], v[10:13]
	v_mfma_f32_16x16x32_bf16 v[6:9], v[162:165], v[206:209], v[6:9]
	v_mfma_f32_16x16x32_bf16 v[2:5], v[170:173], v[206:209], v[2:5]
	s_barrier
	s_add_i32 s48, s84, s61
	s_mov_b32 m0, s48
	ds_read_b128 v[174:177], v138 offset:16384
	ds_read_b128 v[178:181], v138 offset:17408
	ds_read_b128 v[182:185], v138 offset:18432
	ds_read_b128 v[186:189], v138 offset:19456
	ds_read_b128 v[194:197], v138 offset:20480
	ds_read_b128 v[198:201], v138 offset:21504
	ds_read_b128 v[202:205], v138 offset:22528
	ds_read_b128 v[206:209], v138 offset:23552
	s_nop 0
	global_load_lds_dwordx4 v0, s[54:55]
	s_add_i32 m0, s48, 0x2000
	s_add_u32 s48, s54, s28
	s_addc_u32 s49, s55, s29
	s_add_i32 s84, s85, s61
	s_nop 0
	global_load_lds_dwordx4 v134, s[54:55]
	s_mov_b32 m0, s84
	s_nop 0
	global_load_lds_dwordx4 v0, s[48:49]
	s_add_i32 m0, s84, 0x2000
	s_nop 0
	global_load_lds_dwordx4 v134, s[48:49]
	s_mov_b32 m0, s62
	s_nop 0
	global_load_lds_dwordx4 v130, s[52:53]
	s_mov_b32 m0, s63
	s_nop 0
	global_load_lds_dwordx4 v132, s[52:53]
	s_waitcnt vmcnt(8)
	s_waitcnt lgkmcnt(0)
	s_barrier
	s_waitcnt lgkmcnt(0)
	v_mfma_f32_16x16x32_bf16 v[126:129], v[142:145], v[174:177], v[126:129]
	v_mfma_f32_16x16x32_bf16 v[122:125], v[150:153], v[174:177], v[122:125]
	v_mfma_f32_16x16x32_bf16 v[110:113], v[142:145], v[182:185], v[110:113]
	v_mfma_f32_16x16x32_bf16 v[106:109], v[150:153], v[182:185], v[106:109]
	v_mfma_f32_16x16x32_bf16 v[94:97], v[142:145], v[194:197], v[94:97]
	v_mfma_f32_16x16x32_bf16 v[90:93], v[150:153], v[194:197], v[90:93]
	v_mfma_f32_16x16x32_bf16 v[78:81], v[142:145], v[202:205], v[78:81]
	v_mfma_f32_16x16x32_bf16 v[74:77], v[150:153], v[202:205], v[74:77]
	v_mfma_f32_16x16x32_bf16 v[126:129], v[146:149], v[178:181], v[126:129]
	v_mfma_f32_16x16x32_bf16 v[122:125], v[154:157], v[178:181], v[122:125]
	v_mfma_f32_16x16x32_bf16 v[110:113], v[146:149], v[186:189], v[110:113]
	v_mfma_f32_16x16x32_bf16 v[106:109], v[154:157], v[186:189], v[106:109]
	v_mfma_f32_16x16x32_bf16 v[94:97], v[146:149], v[198:201], v[94:97]
	v_mfma_f32_16x16x32_bf16 v[90:93], v[154:157], v[198:201], v[90:93]
	v_mfma_f32_16x16x32_bf16 v[78:81], v[146:149], v[206:209], v[78:81]
	v_mfma_f32_16x16x32_bf16 v[74:77], v[154:157], v[206:209], v[74:77]
	v_mfma_f32_16x16x32_bf16 v[54:57], v[158:161], v[174:177], v[54:57]
	v_mfma_f32_16x16x32_bf16 v[50:53], v[166:169], v[174:177], v[50:53]
	v_mfma_f32_16x16x32_bf16 v[38:41], v[158:161], v[182:185], v[38:41]
	v_mfma_f32_16x16x32_bf16 v[34:37], v[166:169], v[182:185], v[34:37]
	v_mfma_f32_16x16x32_bf16 v[22:25], v[158:161], v[194:197], v[22:25]
	v_mfma_f32_16x16x32_bf16 v[18:21], v[166:169], v[194:197], v[18:21]
	v_mfma_f32_16x16x32_bf16 v[58:61], v[158:161], v[202:205], v[58:61]
	v_mfma_f32_16x16x32_bf16 v[62:65], v[166:169], v[202:205], v[62:65]
	v_mfma_f32_16x16x32_bf16 v[54:57], v[162:165], v[178:181], v[54:57]
	v_mfma_f32_16x16x32_bf16 v[50:53], v[170:173], v[178:181], v[50:53]
	v_mfma_f32_16x16x32_bf16 v[38:41], v[162:165], v[186:189], v[38:41]
	v_mfma_f32_16x16x32_bf16 v[34:37], v[170:173], v[186:189], v[34:37]
	v_mfma_f32_16x16x32_bf16 v[22:25], v[162:165], v[198:201], v[22:25]
	v_mfma_f32_16x16x32_bf16 v[18:21], v[170:173], v[198:201], v[18:21]
	v_mfma_f32_16x16x32_bf16 v[58:61], v[162:165], v[206:209], v[58:61]
	v_mfma_f32_16x16x32_bf16 v[62:65], v[170:173], v[206:209], v[62:65]
	s_barrier
	s_add_i32 s86, 0, 0x18000
	v_add_u32_e32 v131, s86, v137
	s_add_i32 s87, 0, 0x1c000
	ds_read_b128 v[142:145], v131
	ds_read_b128 v[146:149], v131 offset:1024
	ds_read_b128 v[150:153], v131 offset:2048
	ds_read_b128 v[154:157], v131 offset:3072
	v_add_u32_e32 v131, s87, v137
	ds_read_b128 v[158:161], v131
	ds_read_b128 v[162:165], v131 offset:1024
	ds_read_b128 v[166:169], v131 offset:2048
	ds_read_b128 v[170:173], v131 offset:3072
	s_add_u32 s84, s52, s28
	s_addc_u32 s85, s53, s29
	s_mov_b32 m0, s64
	ds_read_b128 v[174:177], v138 offset:32768
	ds_read_b128 v[178:181], v138 offset:33792
	ds_read_b128 v[182:185], v138 offset:34816
	ds_read_b128 v[186:189], v138 offset:35840
	ds_read_b128 v[194:197], v138 offset:36864
	ds_read_b128 v[198:201], v138 offset:37888
	ds_read_b128 v[202:205], v138 offset:38912
	ds_read_b128 v[206:209], v138 offset:39936
	s_nop 0
	global_load_lds_dwordx4 v130, s[84:85]
	s_mov_b32 m0, s65
	s_nop 0
	global_load_lds_dwordx4 v132, s[84:85]
	s_waitcnt vmcnt(8)
	s_waitcnt lgkmcnt(0)
	s_barrier
	s_waitcnt lgkmcnt(0)
	v_mfma_f32_16x16x32_bf16 v[118:121], v[142:145], v[174:177], v[118:121]
	v_mfma_f32_16x16x32_bf16 v[114:117], v[150:153], v[174:177], v[114:117]
	v_mfma_f32_16x16x32_bf16 v[102:105], v[142:145], v[182:185], v[102:105]
	v_mfma_f32_16x16x32_bf16 v[98:101], v[150:153], v[182:185], v[98:101]
	v_mfma_f32_16x16x32_bf16 v[86:89], v[142:145], v[194:197], v[86:89]
	v_mfma_f32_16x16x32_bf16 v[82:85], v[150:153], v[194:197], v[82:85]
	v_mfma_f32_16x16x32_bf16 v[70:73], v[142:145], v[202:205], v[70:73]
	v_mfma_f32_16x16x32_bf16 v[66:69], v[150:153], v[202:205], v[66:69]
	v_mfma_f32_16x16x32_bf16 v[118:121], v[146:149], v[178:181], v[118:121]
	v_mfma_f32_16x16x32_bf16 v[114:117], v[154:157], v[178:181], v[114:117]
	v_mfma_f32_16x16x32_bf16 v[102:105], v[146:149], v[186:189], v[102:105]
	v_mfma_f32_16x16x32_bf16 v[98:101], v[154:157], v[186:189], v[98:101]
	v_mfma_f32_16x16x32_bf16 v[86:89], v[146:149], v[198:201], v[86:89]
	v_mfma_f32_16x16x32_bf16 v[82:85], v[154:157], v[198:201], v[82:85]
	v_mfma_f32_16x16x32_bf16 v[70:73], v[146:149], v[206:209], v[70:73]
	v_mfma_f32_16x16x32_bf16 v[66:69], v[154:157], v[206:209], v[66:69]
	v_mfma_f32_16x16x32_bf16 v[46:49], v[158:161], v[174:177], v[46:49]
	v_mfma_f32_16x16x32_bf16 v[42:45], v[166:169], v[174:177], v[42:45]
	v_mfma_f32_16x16x32_bf16 v[30:33], v[158:161], v[182:185], v[30:33]
	v_mfma_f32_16x16x32_bf16 v[26:29], v[166:169], v[182:185], v[26:29]
	v_mfma_f32_16x16x32_bf16 v[14:17], v[158:161], v[194:197], v[14:17]
	v_mfma_f32_16x16x32_bf16 v[10:13], v[166:169], v[194:197], v[10:13]
	v_mfma_f32_16x16x32_bf16 v[6:9], v[158:161], v[202:205], v[6:9]
	v_mfma_f32_16x16x32_bf16 v[2:5], v[166:169], v[202:205], v[2:5]
	v_mfma_f32_16x16x32_bf16 v[46:49], v[162:165], v[178:181], v[46:49]
	v_mfma_f32_16x16x32_bf16 v[42:45], v[170:173], v[178:181], v[42:45]
	v_mfma_f32_16x16x32_bf16 v[30:33], v[162:165], v[186:189], v[30:33]
	v_mfma_f32_16x16x32_bf16 v[26:29], v[170:173], v[186:189], v[26:29]
	v_mfma_f32_16x16x32_bf16 v[14:17], v[162:165], v[198:201], v[14:17]
	v_mfma_f32_16x16x32_bf16 v[10:13], v[170:173], v[198:201], v[10:13]
	v_mfma_f32_16x16x32_bf16 v[6:9], v[162:165], v[206:209], v[6:9]
	v_mfma_f32_16x16x32_bf16 v[2:5], v[170:173], v[206:209], v[2:5]
	s_barrier
	ds_read_b128 v[174:177], v138 offset:49152
	ds_read_b128 v[178:181], v138 offset:50176
	ds_read_b128 v[182:185], v138 offset:51200
	ds_read_b128 v[186:189], v138 offset:52224
	ds_read_b128 v[194:197], v138 offset:53248
	ds_read_b128 v[198:201], v138 offset:54272
	ds_read_b128 v[202:205], v138 offset:55296
	ds_read_b128 v[206:209], v138 offset:56320
	s_add_i32 s84, s86, s61
	v_lshl_add_u64 v[190:191], s[54:55], 0, v[0:1]
	v_lshl_add_u64 v[190:191], v[190:191], 0, s[16:17]
	s_mov_b32 m0, s84
	v_mov_b32_e32 v135, v1
	global_load_lds_dwordx4 v[190:191], off
	s_add_i32 m0, s84, 0x2000
	v_lshl_add_u64 v[190:191], s[54:55], 0, v[134:135]
	v_lshl_add_u64 v[190:191], v[190:191], 0, s[16:17]
	global_load_lds_dwordx4 v[190:191], off
	s_add_i32 s54, s87, s61
	v_lshl_add_u64 v[190:191], s[48:49], 0, v[0:1]
	v_lshl_add_u64 v[190:191], v[190:191], 0, s[16:17]
	s_mov_b32 m0, s54
	v_mov_b32_e32 v131, v1
	global_load_lds_dwordx4 v[190:191], off
	s_add_i32 m0, s54, 0x2000
	v_lshl_add_u64 v[190:191], s[48:49], 0, v[134:135]
	v_lshl_add_u64 v[190:191], v[190:191], 0, s[16:17]
	global_load_lds_dwordx4 v[190:191], off
	s_mov_b32 m0, s66
	v_lshl_add_u64 v[190:191], s[52:53], 0, v[130:131]
	v_lshl_add_u64 v[190:191], v[190:191], 0, s[16:17]
	v_mov_b32_e32 v133, v1
	global_load_lds_dwordx4 v[190:191], off
	s_mov_b32 m0, s67
	v_lshl_add_u64 v[190:191], s[52:53], 0, v[132:133]
	v_lshl_add_u64 v[190:191], v[190:191], 0, s[16:17]
	global_load_lds_dwordx4 v[190:191], off
	s_waitcnt vmcnt(8)
	s_waitcnt lgkmcnt(0)
	s_barrier
	s_waitcnt lgkmcnt(0)
	v_mfma_f32_16x16x32_bf16 v[126:129], v[142:145], v[174:177], v[126:129]
	v_mfma_f32_16x16x32_bf16 v[122:125], v[150:153], v[174:177], v[122:125]
	v_mfma_f32_16x16x32_bf16 v[110:113], v[142:145], v[182:185], v[110:113]
	v_mfma_f32_16x16x32_bf16 v[106:109], v[150:153], v[182:185], v[106:109]
	v_mfma_f32_16x16x32_bf16 v[94:97], v[142:145], v[194:197], v[94:97]
	v_mfma_f32_16x16x32_bf16 v[90:93], v[150:153], v[194:197], v[90:93]
	v_mfma_f32_16x16x32_bf16 v[78:81], v[142:145], v[202:205], v[78:81]
	v_mfma_f32_16x16x32_bf16 v[74:77], v[150:153], v[202:205], v[74:77]
	v_mfma_f32_16x16x32_bf16 v[126:129], v[146:149], v[178:181], v[126:129]
	v_mfma_f32_16x16x32_bf16 v[122:125], v[154:157], v[178:181], v[122:125]
	v_mfma_f32_16x16x32_bf16 v[110:113], v[146:149], v[186:189], v[110:113]
	v_mfma_f32_16x16x32_bf16 v[106:109], v[154:157], v[186:189], v[106:109]
	v_mfma_f32_16x16x32_bf16 v[94:97], v[146:149], v[198:201], v[94:97]
	v_mfma_f32_16x16x32_bf16 v[90:93], v[154:157], v[198:201], v[90:93]
	v_mfma_f32_16x16x32_bf16 v[78:81], v[146:149], v[206:209], v[78:81]
	v_mfma_f32_16x16x32_bf16 v[74:77], v[154:157], v[206:209], v[74:77]
	v_mfma_f32_16x16x32_bf16 v[54:57], v[158:161], v[174:177], v[54:57]
	v_mfma_f32_16x16x32_bf16 v[50:53], v[166:169], v[174:177], v[50:53]
	v_mfma_f32_16x16x32_bf16 v[38:41], v[158:161], v[182:185], v[38:41]
	v_mfma_f32_16x16x32_bf16 v[34:37], v[166:169], v[182:185], v[34:37]
	v_mfma_f32_16x16x32_bf16 v[22:25], v[158:161], v[194:197], v[22:25]
	v_mfma_f32_16x16x32_bf16 v[18:21], v[166:169], v[194:197], v[18:21]
	v_mfma_f32_16x16x32_bf16 v[58:61], v[158:161], v[202:205], v[58:61]
	v_mfma_f32_16x16x32_bf16 v[62:65], v[166:169], v[202:205], v[62:65]
	v_mfma_f32_16x16x32_bf16 v[54:57], v[162:165], v[178:181], v[54:57]
	v_mfma_f32_16x16x32_bf16 v[50:53], v[170:173], v[178:181], v[50:53]
	v_mfma_f32_16x16x32_bf16 v[38:41], v[162:165], v[186:189], v[38:41]
	v_mfma_f32_16x16x32_bf16 v[34:37], v[170:173], v[186:189], v[34:37]
	v_mfma_f32_16x16x32_bf16 v[22:25], v[162:165], v[198:201], v[22:25]
	v_mfma_f32_16x16x32_bf16 v[18:21], v[170:173], v[198:201], v[18:21]
	v_mfma_f32_16x16x32_bf16 v[58:61], v[162:165], v[206:209], v[58:61]
	v_mfma_f32_16x16x32_bf16 v[62:65], v[170:173], v[206:209], v[62:65]
	s_barrier
	s_add_u32 s81, s81, 0x100
	s_addc_u32 s82, s82, 0
	s_cmp_ge_i32 s83, s68
	s_mov_b64 s[48:49], s[50:51]
	s_mov_b32 s52, s83
	s_cbranch_scc0 .LBB0_498

.LBB0_531:
	s_add_i32 s81, s52, 2
	s_add_u32 s50, s48, 0x100
	s_addc_u32 s51, s49, 0
	s_add_i32 s82, 0, 0x10000
	s_cmp_eq_u32 s71, s52
	s_cselect_b32 s53, s43, s51
	s_cselect_b32 s52, s42, s50
	v_add_u32_e32 v131, s82, v137
	s_cselect_b32 s55, s45, s80
	s_cselect_b32 s54, s44, s47
	s_add_i32 s83, 0, 0x14000
	ds_read_b128 v[142:145], v131
	ds_read_b128 v[146:149], v131 offset:1024
	ds_read_b128 v[150:153], v131 offset:2048
	ds_read_b128 v[154:157], v131 offset:3072
	v_add_u32_e32 v131, s83, v137
	ds_read_b128 v[158:161], v131
	ds_read_b128 v[162:165], v131 offset:1024
	ds_read_b128 v[166:169], v131 offset:2048
	ds_read_b128 v[170:173], v131 offset:3072
	s_add_u32 s48, s48, s74
	s_addc_u32 s49, s49, s75
	s_add_i32 m0, s62, 0xc000
	ds_read_b128 v[174:177], v138
	ds_read_b128 v[178:181], v138 offset:1024
	ds_read_b128 v[182:185], v138 offset:2048
	ds_read_b128 v[186:189], v138 offset:3072
	ds_read_b128 v[194:197], v138 offset:4096
	ds_read_b128 v[198:201], v138 offset:5120
	ds_read_b128 v[202:205], v138 offset:6144
	ds_read_b128 v[206:209], v138 offset:7168
	s_nop 0
	global_load_lds_dwordx4 v130, s[48:49]
	s_add_i32 m0, s62, 0xe000
	s_nop 0
	global_load_lds_dwordx4 v132, s[48:49]
	s_waitcnt vmcnt(8)
	s_waitcnt lgkmcnt(0)
	s_barrier
	s_waitcnt lgkmcnt(0)
	v_mfma_f32_16x16x32_bf16 v[118:121], v[142:145], v[174:177], v[118:121]
	v_mfma_f32_16x16x32_bf16 v[114:117], v[150:153], v[174:177], v[114:117]
	v_mfma_f32_16x16x32_bf16 v[102:105], v[142:145], v[182:185], v[102:105]
	v_mfma_f32_16x16x32_bf16 v[98:101], v[150:153], v[182:185], v[98:101]
	v_mfma_f32_16x16x32_bf16 v[86:89], v[142:145], v[194:197], v[86:89]
	v_mfma_f32_16x16x32_bf16 v[82:85], v[150:153], v[194:197], v[82:85]
	v_mfma_f32_16x16x32_bf16 v[70:73], v[142:145], v[202:205], v[70:73]
	v_mfma_f32_16x16x32_bf16 v[66:69], v[150:153], v[202:205], v[66:69]
	v_mfma_f32_16x16x32_bf16 v[118:121], v[146:149], v[178:181], v[118:121]
	v_mfma_f32_16x16x32_bf16 v[114:117], v[154:157], v[178:181], v[114:117]
	v_mfma_f32_16x16x32_bf16 v[102:105], v[146:149], v[186:189], v[102:105]
	v_mfma_f32_16x16x32_bf16 v[98:101], v[154:157], v[186:189], v[98:101]
	v_mfma_f32_16x16x32_bf16 v[86:89], v[146:149], v[198:201], v[86:89]
	v_mfma_f32_16x16x32_bf16 v[82:85], v[154:157], v[198:201], v[82:85]
	v_mfma_f32_16x16x32_bf16 v[70:73], v[146:149], v[206:209], v[70:73]
	v_mfma_f32_16x16x32_bf16 v[66:69], v[154:157], v[206:209], v[66:69]
	v_mfma_f32_16x16x32_bf16 v[46:49], v[158:161], v[174:177], v[46:49]
	v_mfma_f32_16x16x32_bf16 v[42:45], v[166:169], v[174:177], v[42:45]
	v_mfma_f32_16x16x32_bf16 v[30:33], v[158:161], v[182:185], v[30:33]
	v_mfma_f32_16x16x32_bf16 v[26:29], v[166:169], v[182:185], v[26:29]
	v_mfma_f32_16x16x32_bf16 v[14:17], v[158:161], v[194:197], v[14:17]
	v_mfma_f32_16x16x32_bf16 v[10:13], v[166:169], v[194:197], v[10:13]
	v_mfma_f32_16x16x32_bf16 v[6:9], v[158:161], v[202:205], v[6:9]
	v_mfma_f32_16x16x32_bf16 v[2:5], v[166:169], v[202:205], v[2:5]
	v_mfma_f32_16x16x32_bf16 v[46:49], v[162:165], v[178:181], v[46:49]
	v_mfma_f32_16x16x32_bf16 v[42:45], v[170:173], v[178:181], v[42:45]
	v_mfma_f32_16x16x32_bf16 v[30:33], v[162:165], v[186:189], v[30:33]
	v_mfma_f32_16x16x32_bf16 v[26:29], v[170:173], v[186:189], v[26:29]
	v_mfma_f32_16x16x32_bf16 v[14:17], v[162:165], v[198:201], v[14:17]
	v_mfma_f32_16x16x32_bf16 v[10:13], v[170:173], v[198:201], v[10:13]
	v_mfma_f32_16x16x32_bf16 v[6:9], v[162:165], v[206:209], v[6:9]
	v_mfma_f32_16x16x32_bf16 v[2:5], v[170:173], v[206:209], v[2:5]
	s_barrier
	s_add_i32 s48, s82, s61
	s_mov_b32 m0, s48
	ds_read_b128 v[174:177], v138 offset:16384
	ds_read_b128 v[178:181], v138 offset:17408
	ds_read_b128 v[182:185], v138 offset:18432
	ds_read_b128 v[186:189], v138 offset:19456
	ds_read_b128 v[194:197], v138 offset:20480
	ds_read_b128 v[198:201], v138 offset:21504
	ds_read_b128 v[202:205], v138 offset:22528
	ds_read_b128 v[206:209], v138 offset:23552
	s_nop 0
	global_load_lds_dwordx4 v0, s[54:55]
	s_add_i32 m0, s48, 0x2000
	s_add_u32 s48, s54, s26
	s_addc_u32 s49, s55, s27
	s_add_i32 s82, s83, s61
	s_nop 0
	global_load_lds_dwordx4 v134, s[54:55]
	s_mov_b32 m0, s82
	s_nop 0
	global_load_lds_dwordx4 v0, s[48:49]
	s_add_i32 m0, s82, 0x2000
	s_nop 0
	global_load_lds_dwordx4 v134, s[48:49]
	s_mov_b32 m0, s62
	s_nop 0
	global_load_lds_dwordx4 v130, s[52:53]
	s_mov_b32 m0, s63
	s_nop 0
	global_load_lds_dwordx4 v132, s[52:53]
	s_waitcnt vmcnt(8)
	s_waitcnt lgkmcnt(0)
	s_barrier
	s_waitcnt lgkmcnt(0)
	v_mfma_f32_16x16x32_bf16 v[126:129], v[142:145], v[174:177], v[126:129]
	v_mfma_f32_16x16x32_bf16 v[122:125], v[150:153], v[174:177], v[122:125]
	v_mfma_f32_16x16x32_bf16 v[110:113], v[142:145], v[182:185], v[110:113]
	v_mfma_f32_16x16x32_bf16 v[106:109], v[150:153], v[182:185], v[106:109]
	v_mfma_f32_16x16x32_bf16 v[94:97], v[142:145], v[194:197], v[94:97]
	v_mfma_f32_16x16x32_bf16 v[90:93], v[150:153], v[194:197], v[90:93]
	v_mfma_f32_16x16x32_bf16 v[78:81], v[142:145], v[202:205], v[78:81]
	v_mfma_f32_16x16x32_bf16 v[74:77], v[150:153], v[202:205], v[74:77]
	v_mfma_f32_16x16x32_bf16 v[126:129], v[146:149], v[178:181], v[126:129]
	v_mfma_f32_16x16x32_bf16 v[122:125], v[154:157], v[178:181], v[122:125]
	v_mfma_f32_16x16x32_bf16 v[110:113], v[146:149], v[186:189], v[110:113]
	v_mfma_f32_16x16x32_bf16 v[106:109], v[154:157], v[186:189], v[106:109]
	v_mfma_f32_16x16x32_bf16 v[94:97], v[146:149], v[198:201], v[94:97]
	v_mfma_f32_16x16x32_bf16 v[90:93], v[154:157], v[198:201], v[90:93]
	v_mfma_f32_16x16x32_bf16 v[78:81], v[146:149], v[206:209], v[78:81]
	v_mfma_f32_16x16x32_bf16 v[74:77], v[154:157], v[206:209], v[74:77]
	v_mfma_f32_16x16x32_bf16 v[54:57], v[158:161], v[174:177], v[54:57]
	v_mfma_f32_16x16x32_bf16 v[50:53], v[166:169], v[174:177], v[50:53]
	v_mfma_f32_16x16x32_bf16 v[38:41], v[158:161], v[182:185], v[38:41]
	v_mfma_f32_16x16x32_bf16 v[34:37], v[166:169], v[182:185], v[34:37]
	v_mfma_f32_16x16x32_bf16 v[22:25], v[158:161], v[194:197], v[22:25]
	v_mfma_f32_16x16x32_bf16 v[18:21], v[166:169], v[194:197], v[18:21]
	v_mfma_f32_16x16x32_bf16 v[58:61], v[158:161], v[202:205], v[58:61]
	v_mfma_f32_16x16x32_bf16 v[62:65], v[166:169], v[202:205], v[62:65]
	v_mfma_f32_16x16x32_bf16 v[54:57], v[162:165], v[178:181], v[54:57]
	v_mfma_f32_16x16x32_bf16 v[50:53], v[170:173], v[178:181], v[50:53]
	v_mfma_f32_16x16x32_bf16 v[38:41], v[162:165], v[186:189], v[38:41]
	v_mfma_f32_16x16x32_bf16 v[34:37], v[170:173], v[186:189], v[34:37]
	v_mfma_f32_16x16x32_bf16 v[22:25], v[162:165], v[198:201], v[22:25]
	v_mfma_f32_16x16x32_bf16 v[18:21], v[170:173], v[198:201], v[18:21]
	v_mfma_f32_16x16x32_bf16 v[58:61], v[162:165], v[206:209], v[58:61]
	v_mfma_f32_16x16x32_bf16 v[62:65], v[170:173], v[206:209], v[62:65]
	s_barrier
	s_add_i32 s84, 0, 0x18000
	v_add_u32_e32 v131, s84, v137
	s_add_i32 s85, 0, 0x1c000
	ds_read_b128 v[142:145], v131
	ds_read_b128 v[146:149], v131 offset:1024
	ds_read_b128 v[150:153], v131 offset:2048
	ds_read_b128 v[154:157], v131 offset:3072
	v_add_u32_e32 v131, s85, v137
	ds_read_b128 v[158:161], v131
	ds_read_b128 v[162:165], v131 offset:1024
	ds_read_b128 v[166:169], v131 offset:2048
	ds_read_b128 v[170:173], v131 offset:3072
	s_add_u32 s82, s52, s26
	s_addc_u32 s83, s53, s27
	s_mov_b32 m0, s64
	ds_read_b128 v[174:177], v138 offset:32768
	ds_read_b128 v[178:181], v138 offset:33792
	ds_read_b128 v[182:185], v138 offset:34816
	ds_read_b128 v[186:189], v138 offset:35840
	ds_read_b128 v[194:197], v138 offset:36864
	ds_read_b128 v[198:201], v138 offset:37888
	ds_read_b128 v[202:205], v138 offset:38912
	ds_read_b128 v[206:209], v138 offset:39936
	s_nop 0
	global_load_lds_dwordx4 v130, s[82:83]
	s_mov_b32 m0, s65
	s_nop 0
	global_load_lds_dwordx4 v132, s[82:83]
	s_waitcnt vmcnt(8)
	s_waitcnt lgkmcnt(0)
	s_barrier
	s_waitcnt lgkmcnt(0)
	v_mfma_f32_16x16x32_bf16 v[118:121], v[142:145], v[174:177], v[118:121]
	v_mfma_f32_16x16x32_bf16 v[114:117], v[150:153], v[174:177], v[114:117]
	v_mfma_f32_16x16x32_bf16 v[102:105], v[142:145], v[182:185], v[102:105]
	v_mfma_f32_16x16x32_bf16 v[98:101], v[150:153], v[182:185], v[98:101]
	v_mfma_f32_16x16x32_bf16 v[86:89], v[142:145], v[194:197], v[86:89]
	v_mfma_f32_16x16x32_bf16 v[82:85], v[150:153], v[194:197], v[82:85]
	v_mfma_f32_16x16x32_bf16 v[70:73], v[142:145], v[202:205], v[70:73]
	v_mfma_f32_16x16x32_bf16 v[66:69], v[150:153], v[202:205], v[66:69]
	v_mfma_f32_16x16x32_bf16 v[118:121], v[146:149], v[178:181], v[118:121]
	v_mfma_f32_16x16x32_bf16 v[114:117], v[154:157], v[178:181], v[114:117]
	v_mfma_f32_16x16x32_bf16 v[102:105], v[146:149], v[186:189], v[102:105]
	v_mfma_f32_16x16x32_bf16 v[98:101], v[154:157], v[186:189], v[98:101]
	v_mfma_f32_16x16x32_bf16 v[86:89], v[146:149], v[198:201], v[86:89]
	v_mfma_f32_16x16x32_bf16 v[82:85], v[154:157], v[198:201], v[82:85]
	v_mfma_f32_16x16x32_bf16 v[70:73], v[146:149], v[206:209], v[70:73]
	v_mfma_f32_16x16x32_bf16 v[66:69], v[154:157], v[206:209], v[66:69]
	v_mfma_f32_16x16x32_bf16 v[46:49], v[158:161], v[174:177], v[46:49]
	v_mfma_f32_16x16x32_bf16 v[42:45], v[166:169], v[174:177], v[42:45]
	v_mfma_f32_16x16x32_bf16 v[30:33], v[158:161], v[182:185], v[30:33]
	v_mfma_f32_16x16x32_bf16 v[26:29], v[166:169], v[182:185], v[26:29]
	v_mfma_f32_16x16x32_bf16 v[14:17], v[158:161], v[194:197], v[14:17]
	v_mfma_f32_16x16x32_bf16 v[10:13], v[166:169], v[194:197], v[10:13]
	v_mfma_f32_16x16x32_bf16 v[6:9], v[158:161], v[202:205], v[6:9]
	v_mfma_f32_16x16x32_bf16 v[2:5], v[166:169], v[202:205], v[2:5]
	v_mfma_f32_16x16x32_bf16 v[46:49], v[162:165], v[178:181], v[46:49]
	v_mfma_f32_16x16x32_bf16 v[42:45], v[170:173], v[178:181], v[42:45]
	v_mfma_f32_16x16x32_bf16 v[30:33], v[162:165], v[186:189], v[30:33]
	v_mfma_f32_16x16x32_bf16 v[26:29], v[170:173], v[186:189], v[26:29]
	v_mfma_f32_16x16x32_bf16 v[14:17], v[162:165], v[198:201], v[14:17]
	v_mfma_f32_16x16x32_bf16 v[10:13], v[170:173], v[198:201], v[10:13]
	v_mfma_f32_16x16x32_bf16 v[6:9], v[162:165], v[206:209], v[6:9]
	v_mfma_f32_16x16x32_bf16 v[2:5], v[170:173], v[206:209], v[2:5]
	s_barrier
	ds_read_b128 v[174:177], v138 offset:49152
	ds_read_b128 v[178:181], v138 offset:50176
	ds_read_b128 v[182:185], v138 offset:51200
	ds_read_b128 v[186:189], v138 offset:52224
	ds_read_b128 v[194:197], v138 offset:53248
	ds_read_b128 v[198:201], v138 offset:54272
	ds_read_b128 v[202:205], v138 offset:55296
	ds_read_b128 v[206:209], v138 offset:56320
	s_add_i32 s82, s84, s61
	v_lshl_add_u64 v[190:191], s[54:55], 0, v[0:1]
	v_lshl_add_u64 v[190:191], v[190:191], 0, s[16:17]
	s_mov_b32 m0, s82
	v_mov_b32_e32 v135, v1
	global_load_lds_dwordx4 v[190:191], off
	s_add_i32 m0, s82, 0x2000
	v_lshl_add_u64 v[190:191], s[54:55], 0, v[134:135]
	v_lshl_add_u64 v[190:191], v[190:191], 0, s[16:17]
	global_load_lds_dwordx4 v[190:191], off
	s_add_i32 s54, s85, s61
	v_lshl_add_u64 v[190:191], s[48:49], 0, v[0:1]
	v_lshl_add_u64 v[190:191], v[190:191], 0, s[16:17]
	s_mov_b32 m0, s54
	v_mov_b32_e32 v131, v1
	global_load_lds_dwordx4 v[190:191], off
	s_add_i32 m0, s54, 0x2000
	v_lshl_add_u64 v[190:191], s[48:49], 0, v[134:135]
	v_lshl_add_u64 v[190:191], v[190:191], 0, s[16:17]
	global_load_lds_dwordx4 v[190:191], off
	s_mov_b32 m0, s66
	v_lshl_add_u64 v[190:191], s[52:53], 0, v[130:131]
	v_lshl_add_u64 v[190:191], v[190:191], 0, s[16:17]
	v_mov_b32_e32 v133, v1
	global_load_lds_dwordx4 v[190:191], off
	s_mov_b32 m0, s67
	v_lshl_add_u64 v[190:191], s[52:53], 0, v[132:133]
	v_lshl_add_u64 v[190:191], v[190:191], 0, s[16:17]
	global_load_lds_dwordx4 v[190:191], off
	s_waitcnt vmcnt(8)
	s_waitcnt lgkmcnt(0)
	s_barrier
	s_waitcnt lgkmcnt(0)
	v_mfma_f32_16x16x32_bf16 v[126:129], v[142:145], v[174:177], v[126:129]
	v_mfma_f32_16x16x32_bf16 v[122:125], v[150:153], v[174:177], v[122:125]
	v_mfma_f32_16x16x32_bf16 v[110:113], v[142:145], v[182:185], v[110:113]
	v_mfma_f32_16x16x32_bf16 v[106:109], v[150:153], v[182:185], v[106:109]
	v_mfma_f32_16x16x32_bf16 v[94:97], v[142:145], v[194:197], v[94:97]
	v_mfma_f32_16x16x32_bf16 v[90:93], v[150:153], v[194:197], v[90:93]
	v_mfma_f32_16x16x32_bf16 v[78:81], v[142:145], v[202:205], v[78:81]
	v_mfma_f32_16x16x32_bf16 v[74:77], v[150:153], v[202:205], v[74:77]
	v_mfma_f32_16x16x32_bf16 v[126:129], v[146:149], v[178:181], v[126:129]
	v_mfma_f32_16x16x32_bf16 v[122:125], v[154:157], v[178:181], v[122:125]
	v_mfma_f32_16x16x32_bf16 v[110:113], v[146:149], v[186:189], v[110:113]
	v_mfma_f32_16x16x32_bf16 v[106:109], v[154:157], v[186:189], v[106:109]
	v_mfma_f32_16x16x32_bf16 v[94:97], v[146:149], v[198:201], v[94:97]
	v_mfma_f32_16x16x32_bf16 v[90:93], v[154:157], v[198:201], v[90:93]
	v_mfma_f32_16x16x32_bf16 v[78:81], v[146:149], v[206:209], v[78:81]
	v_mfma_f32_16x16x32_bf16 v[74:77], v[154:157], v[206:209], v[74:77]
	v_mfma_f32_16x16x32_bf16 v[54:57], v[158:161], v[174:177], v[54:57]
	v_mfma_f32_16x16x32_bf16 v[50:53], v[166:169], v[174:177], v[50:53]
	v_mfma_f32_16x16x32_bf16 v[38:41], v[158:161], v[182:185], v[38:41]
	v_mfma_f32_16x16x32_bf16 v[34:37], v[166:169], v[182:185], v[34:37]
	v_mfma_f32_16x16x32_bf16 v[22:25], v[158:161], v[194:197], v[22:25]
	v_mfma_f32_16x16x32_bf16 v[18:21], v[166:169], v[194:197], v[18:21]
	v_mfma_f32_16x16x32_bf16 v[58:61], v[158:161], v[202:205], v[58:61]
	v_mfma_f32_16x16x32_bf16 v[62:65], v[166:169], v[202:205], v[62:65]
	v_mfma_f32_16x16x32_bf16 v[54:57], v[162:165], v[178:181], v[54:57]
	v_mfma_f32_16x16x32_bf16 v[50:53], v[170:173], v[178:181], v[50:53]
	v_mfma_f32_16x16x32_bf16 v[38:41], v[162:165], v[186:189], v[38:41]
	v_mfma_f32_16x16x32_bf16 v[34:37], v[170:173], v[186:189], v[34:37]
	v_mfma_f32_16x16x32_bf16 v[22:25], v[162:165], v[198:201], v[22:25]
	v_mfma_f32_16x16x32_bf16 v[18:21], v[170:173], v[198:201], v[18:21]
	v_mfma_f32_16x16x32_bf16 v[58:61], v[162:165], v[206:209], v[58:61]
	v_mfma_f32_16x16x32_bf16 v[62:65], v[170:173], v[206:209], v[62:65]
	s_barrier
	s_add_u32 s47, s47, 0x100
	s_addc_u32 s80, s80, 0
	s_cmp_ge_i32 s81, s68
	s_mov_b64 s[48:49], s[50:51]
	s_mov_b32 s52, s81
	s_cbranch_scc0 .LBB0_531

.LBB0_707:
	s_add_i32 s74, s52, 2
	s_add_u32 s50, s48, 0x100
	s_addc_u32 s51, s49, 0
	s_add_i32 s75, 0, 0x10000
	s_cmp_eq_u32 s64, s52
	s_cselect_b32 s53, s41, s51
	s_cselect_b32 s52, s40, s50
	v_add_u32_e32 v139, s75, v148
	s_cselect_b32 s55, s47, s73
	s_cselect_b32 s54, s46, s72
	s_add_i32 s76, 0, 0x14000
	ds_read_b128 v[130:133], v139
	ds_read_b128 v[134:137], v139 offset:1024
	ds_read_b128 v[140:143], v139 offset:2048
	ds_read_b128 v[150:153], v139 offset:3072
	v_add_u32_e32 v139, s76, v148
	ds_read_b128 v[154:157], v139
	ds_read_b128 v[158:161], v139 offset:1024
	ds_read_b128 v[162:165], v139 offset:2048
	ds_read_b128 v[166:169], v139 offset:3072
	s_add_u32 s48, s48, s66
	s_addc_u32 s49, s49, s67
	s_add_i32 m0, s15, 0xc000
	ds_read_b128 v[170:173], v149
	ds_read_b128 v[174:177], v149 offset:1024
	ds_read_b128 v[178:181], v149 offset:2048
	ds_read_b128 v[182:185], v149 offset:3072
	ds_read_b128 v[186:189], v149 offset:4096
	ds_read_b128 v[194:197], v149 offset:5120
	ds_read_b128 v[198:201], v149 offset:6144
	ds_read_b128 v[202:205], v149 offset:7168
	s_nop 0
	global_load_lds_dwordx4 v0, s[48:49]
	s_add_i32 m0, s15, 0xe000
	s_nop 0
	global_load_lds_dwordx4 v138, s[48:49]
	s_waitcnt vmcnt(8)
	s_waitcnt lgkmcnt(0)
	s_barrier
	s_waitcnt lgkmcnt(0)
	v_mfma_f32_16x16x32_bf16 v[122:125], v[130:133], v[170:173], v[122:125]
	v_mfma_f32_16x16x32_bf16 v[126:129], v[140:143], v[170:173], v[126:129]
	v_mfma_f32_16x16x32_bf16 v[118:121], v[130:133], v[178:181], v[118:121]
	v_mfma_f32_16x16x32_bf16 v[114:117], v[140:143], v[178:181], v[114:117]
	v_mfma_f32_16x16x32_bf16 v[102:105], v[130:133], v[186:189], v[102:105]
	v_mfma_f32_16x16x32_bf16 v[98:101], v[140:143], v[186:189], v[98:101]
	v_mfma_f32_16x16x32_bf16 v[86:89], v[130:133], v[198:201], v[86:89]
	v_mfma_f32_16x16x32_bf16 v[82:85], v[140:143], v[198:201], v[82:85]
	v_mfma_f32_16x16x32_bf16 v[122:125], v[134:137], v[174:177], v[122:125]
	v_mfma_f32_16x16x32_bf16 v[126:129], v[150:153], v[174:177], v[126:129]
	v_mfma_f32_16x16x32_bf16 v[118:121], v[134:137], v[182:185], v[118:121]
	v_mfma_f32_16x16x32_bf16 v[114:117], v[150:153], v[182:185], v[114:117]
	v_mfma_f32_16x16x32_bf16 v[102:105], v[134:137], v[194:197], v[102:105]
	v_mfma_f32_16x16x32_bf16 v[98:101], v[150:153], v[194:197], v[98:101]
	v_mfma_f32_16x16x32_bf16 v[86:89], v[134:137], v[202:205], v[86:89]
	v_mfma_f32_16x16x32_bf16 v[82:85], v[150:153], v[202:205], v[82:85]
	v_mfma_f32_16x16x32_bf16 v[58:61], v[154:157], v[170:173], v[58:61]
	v_mfma_f32_16x16x32_bf16 v[62:65], v[162:165], v[170:173], v[62:65]
	v_mfma_f32_16x16x32_bf16 v[54:57], v[154:157], v[178:181], v[54:57]
	v_mfma_f32_16x16x32_bf16 v[50:53], v[162:165], v[178:181], v[50:53]
	v_mfma_f32_16x16x32_bf16 v[38:41], v[154:157], v[186:189], v[38:41]
	v_mfma_f32_16x16x32_bf16 v[34:37], v[162:165], v[186:189], v[34:37]
	v_mfma_f32_16x16x32_bf16 v[14:17], v[154:157], v[198:201], v[14:17]
	v_mfma_f32_16x16x32_bf16 v[10:13], v[162:165], v[198:201], v[10:13]
	v_mfma_f32_16x16x32_bf16 v[58:61], v[158:161], v[174:177], v[58:61]
	v_mfma_f32_16x16x32_bf16 v[62:65], v[166:169], v[174:177], v[62:65]
	v_mfma_f32_16x16x32_bf16 v[54:57], v[158:161], v[182:185], v[54:57]
	v_mfma_f32_16x16x32_bf16 v[50:53], v[166:169], v[182:185], v[50:53]
	v_mfma_f32_16x16x32_bf16 v[38:41], v[158:161], v[194:197], v[38:41]
	v_mfma_f32_16x16x32_bf16 v[34:37], v[166:169], v[194:197], v[34:37]
	v_mfma_f32_16x16x32_bf16 v[14:17], v[158:161], v[202:205], v[14:17]
	v_mfma_f32_16x16x32_bf16 v[10:13], v[166:169], v[202:205], v[10:13]
	s_barrier
	s_add_i32 s48, s75, s14
	s_mov_b32 m0, s48
	ds_read_b128 v[170:173], v149 offset:16384
	ds_read_b128 v[174:177], v149 offset:17408
	ds_read_b128 v[178:181], v149 offset:18432
	ds_read_b128 v[182:185], v149 offset:19456
	ds_read_b128 v[186:189], v149 offset:20480
	ds_read_b128 v[194:197], v149 offset:21504
	ds_read_b128 v[198:201], v149 offset:22528
	ds_read_b128 v[202:205], v149 offset:23552
	s_nop 0
	global_load_lds_dwordx4 v147, s[54:55]
	s_add_i32 m0, s48, 0x2000
	s_add_u32 s48, s54, 0x4000
	s_addc_u32 s49, s55, 0
	s_add_i32 s75, s76, s14
	s_nop 0
	global_load_lds_dwordx4 v146, s[54:55]
	s_mov_b32 m0, s75
	s_nop 0
	global_load_lds_dwordx4 v147, s[48:49]
	s_add_i32 m0, s75, 0x2000
	s_nop 0
	global_load_lds_dwordx4 v146, s[48:49]
	s_mov_b32 m0, s15
	s_nop 0
	global_load_lds_dwordx4 v0, s[52:53]
	s_mov_b32 m0, s18
	s_nop 0
	global_load_lds_dwordx4 v138, s[52:53]
	s_waitcnt vmcnt(8)
	s_waitcnt lgkmcnt(0)
	s_barrier
	s_waitcnt lgkmcnt(0)
	v_mfma_f32_16x16x32_bf16 v[110:113], v[130:133], v[170:173], v[110:113]
	v_mfma_f32_16x16x32_bf16 v[106:109], v[140:143], v[170:173], v[106:109]
	v_mfma_f32_16x16x32_bf16 v[94:97], v[130:133], v[178:181], v[94:97]
	v_mfma_f32_16x16x32_bf16 v[90:93], v[140:143], v[178:181], v[90:93]
	v_mfma_f32_16x16x32_bf16 v[78:81], v[130:133], v[186:189], v[78:81]
	v_mfma_f32_16x16x32_bf16 v[74:77], v[140:143], v[186:189], v[74:77]
	v_mfma_f32_16x16x32_bf16 v[70:73], v[130:133], v[198:201], v[70:73]
	v_mfma_f32_16x16x32_bf16 v[66:69], v[140:143], v[198:201], v[66:69]
	v_mfma_f32_16x16x32_bf16 v[110:113], v[134:137], v[174:177], v[110:113]
	v_mfma_f32_16x16x32_bf16 v[106:109], v[150:153], v[174:177], v[106:109]
	v_mfma_f32_16x16x32_bf16 v[94:97], v[134:137], v[182:185], v[94:97]
	v_mfma_f32_16x16x32_bf16 v[90:93], v[150:153], v[182:185], v[90:93]
	v_mfma_f32_16x16x32_bf16 v[78:81], v[134:137], v[194:197], v[78:81]
	v_mfma_f32_16x16x32_bf16 v[74:77], v[150:153], v[194:197], v[74:77]
	v_mfma_f32_16x16x32_bf16 v[70:73], v[134:137], v[202:205], v[70:73]
	v_mfma_f32_16x16x32_bf16 v[66:69], v[150:153], v[202:205], v[66:69]
	v_mfma_f32_16x16x32_bf16 v[46:49], v[154:157], v[170:173], v[46:49]
	v_mfma_f32_16x16x32_bf16 v[42:45], v[162:165], v[170:173], v[42:45]
	v_mfma_f32_16x16x32_bf16 v[26:29], v[154:157], v[178:181], v[26:29]
	v_mfma_f32_16x16x32_bf16 v[22:25], v[162:165], v[178:181], v[22:25]
	v_mfma_f32_16x16x32_bf16 v[6:9], v[154:157], v[186:189], v[6:9]
	v_mfma_f32_16x16x32_bf16 v[2:5], v[162:165], v[186:189], v[2:5]
	v_mfma_f32_16x16x32_bf16 v[18:21], v[154:157], v[198:201], v[18:21]
	v_mfma_f32_16x16x32_bf16 v[30:33], v[162:165], v[198:201], v[30:33]
	v_mfma_f32_16x16x32_bf16 v[46:49], v[158:161], v[174:177], v[46:49]
	v_mfma_f32_16x16x32_bf16 v[42:45], v[166:169], v[174:177], v[42:45]
	v_mfma_f32_16x16x32_bf16 v[26:29], v[158:161], v[182:185], v[26:29]
	v_mfma_f32_16x16x32_bf16 v[22:25], v[166:169], v[182:185], v[22:25]
	v_mfma_f32_16x16x32_bf16 v[6:9], v[158:161], v[194:197], v[6:9]
	v_mfma_f32_16x16x32_bf16 v[2:5], v[166:169], v[194:197], v[2:5]
	v_mfma_f32_16x16x32_bf16 v[18:21], v[158:161], v[202:205], v[18:21]
	v_mfma_f32_16x16x32_bf16 v[30:33], v[166:169], v[202:205], v[30:33]
	s_barrier
	s_add_i32 s75, 0, 0x18000
	v_add_u32_e32 v139, s75, v148
	s_add_i32 s76, 0, 0x1c000
	ds_read_b128 v[130:133], v139
	ds_read_b128 v[134:137], v139 offset:1024
	ds_read_b128 v[140:143], v139 offset:2048
	ds_read_b128 v[150:153], v139 offset:3072
	v_add_u32_e32 v139, s76, v148
	ds_read_b128 v[154:157], v139
	ds_read_b128 v[158:161], v139 offset:1024
	ds_read_b128 v[162:165], v139 offset:2048
	ds_read_b128 v[166:169], v139 offset:3072
	s_add_u32 s48, s52, s26
	s_addc_u32 s49, s53, s27
	s_mov_b32 m0, s20
	ds_read_b128 v[170:173], v149 offset:32768
	ds_read_b128 v[174:177], v149 offset:33792
	ds_read_b128 v[178:181], v149 offset:34816
	ds_read_b128 v[182:185], v149 offset:35840
	ds_read_b128 v[186:189], v149 offset:36864
	ds_read_b128 v[194:197], v149 offset:37888
	ds_read_b128 v[198:201], v149 offset:38912
	ds_read_b128 v[202:205], v149 offset:39936
	s_nop 0
	global_load_lds_dwordx4 v0, s[48:49]
	s_mov_b32 m0, s21
	s_nop 0
	global_load_lds_dwordx4 v138, s[48:49]
	s_waitcnt vmcnt(8)
	s_waitcnt lgkmcnt(0)
	s_barrier
	s_waitcnt lgkmcnt(0)
	v_mfma_f32_16x16x32_bf16 v[122:125], v[130:133], v[170:173], v[122:125]
	v_mfma_f32_16x16x32_bf16 v[126:129], v[140:143], v[170:173], v[126:129]
	v_mfma_f32_16x16x32_bf16 v[118:121], v[130:133], v[178:181], v[118:121]
	v_mfma_f32_16x16x32_bf16 v[114:117], v[140:143], v[178:181], v[114:117]
	v_mfma_f32_16x16x32_bf16 v[102:105], v[130:133], v[186:189], v[102:105]
	v_mfma_f32_16x16x32_bf16 v[98:101], v[140:143], v[186:189], v[98:101]
	v_mfma_f32_16x16x32_bf16 v[86:89], v[130:133], v[198:201], v[86:89]
	v_mfma_f32_16x16x32_bf16 v[82:85], v[140:143], v[198:201], v[82:85]
	v_mfma_f32_16x16x32_bf16 v[122:125], v[134:137], v[174:177], v[122:125]
	v_mfma_f32_16x16x32_bf16 v[126:129], v[150:153], v[174:177], v[126:129]
	v_mfma_f32_16x16x32_bf16 v[118:121], v[134:137], v[182:185], v[118:121]
	v_mfma_f32_16x16x32_bf16 v[114:117], v[150:153], v[182:185], v[114:117]
	v_mfma_f32_16x16x32_bf16 v[102:105], v[134:137], v[194:197], v[102:105]
	v_mfma_f32_16x16x32_bf16 v[98:101], v[150:153], v[194:197], v[98:101]
	v_mfma_f32_16x16x32_bf16 v[86:89], v[134:137], v[202:205], v[86:89]
	v_mfma_f32_16x16x32_bf16 v[82:85], v[150:153], v[202:205], v[82:85]
	v_mfma_f32_16x16x32_bf16 v[58:61], v[154:157], v[170:173], v[58:61]
	v_mfma_f32_16x16x32_bf16 v[62:65], v[162:165], v[170:173], v[62:65]
	v_mfma_f32_16x16x32_bf16 v[54:57], v[154:157], v[178:181], v[54:57]
	v_mfma_f32_16x16x32_bf16 v[50:53], v[162:165], v[178:181], v[50:53]
	v_mfma_f32_16x16x32_bf16 v[38:41], v[154:157], v[186:189], v[38:41]
	v_mfma_f32_16x16x32_bf16 v[34:37], v[162:165], v[186:189], v[34:37]
	v_mfma_f32_16x16x32_bf16 v[14:17], v[154:157], v[198:201], v[14:17]
	v_mfma_f32_16x16x32_bf16 v[10:13], v[162:165], v[198:201], v[10:13]
	v_mfma_f32_16x16x32_bf16 v[58:61], v[158:161], v[174:177], v[58:61]
	v_mfma_f32_16x16x32_bf16 v[62:65], v[166:169], v[174:177], v[62:65]
	v_mfma_f32_16x16x32_bf16 v[54:57], v[158:161], v[182:185], v[54:57]
	v_mfma_f32_16x16x32_bf16 v[50:53], v[166:169], v[182:185], v[50:53]
	v_mfma_f32_16x16x32_bf16 v[38:41], v[158:161], v[194:197], v[38:41]
	v_mfma_f32_16x16x32_bf16 v[34:37], v[166:169], v[194:197], v[34:37]
	v_mfma_f32_16x16x32_bf16 v[14:17], v[158:161], v[202:205], v[14:17]
	v_mfma_f32_16x16x32_bf16 v[10:13], v[166:169], v[202:205], v[10:13]
	s_barrier
	s_add_u32 s48, s54, 0x8000
	s_addc_u32 s49, s55, 0
	s_add_i32 s75, s75, s14
	s_mov_b32 m0, s75
	ds_read_b128 v[170:173], v149 offset:49152
	ds_read_b128 v[174:177], v149 offset:50176
	ds_read_b128 v[178:181], v149 offset:51200
	ds_read_b128 v[182:185], v149 offset:52224
	ds_read_b128 v[186:189], v149 offset:53248
	ds_read_b128 v[194:197], v149 offset:54272
	ds_read_b128 v[198:201], v149 offset:55296
	ds_read_b128 v[202:205], v149 offset:56320
	v_mov_b32_e32 v139, v1
	global_load_lds_dwordx4 v147, s[48:49]
	s_add_i32 m0, s75, 0x2000
	s_nop 0
	global_load_lds_dwordx4 v146, s[48:49]
	s_add_u32 s48, s54, 0xc000
	s_addc_u32 s49, s55, 0
	s_add_i32 s54, s76, s14
	s_mov_b32 m0, s54
	s_nop 0
	global_load_lds_dwordx4 v147, s[48:49]
	s_add_i32 m0, s54, 0x2000
	s_nop 0
	global_load_lds_dwordx4 v146, s[48:49]
	s_mov_b32 m0, s62
	v_lshl_add_u64 v[190:191], s[52:53], 0, v[0:1]
	v_lshl_add_u64 v[190:191], v[190:191], 0, s[16:17]
	global_load_lds_dwordx4 v[190:191], off
	s_mov_b32 m0, s63
	v_lshl_add_u64 v[190:191], s[52:53], 0, v[138:139]
	v_lshl_add_u64 v[190:191], v[190:191], 0, s[16:17]
	global_load_lds_dwordx4 v[190:191], off
	s_waitcnt vmcnt(8)
	s_waitcnt lgkmcnt(0)
	s_barrier
	s_waitcnt lgkmcnt(0)
	v_mfma_f32_16x16x32_bf16 v[110:113], v[130:133], v[170:173], v[110:113]
	v_mfma_f32_16x16x32_bf16 v[106:109], v[140:143], v[170:173], v[106:109]
	v_mfma_f32_16x16x32_bf16 v[94:97], v[130:133], v[178:181], v[94:97]
	v_mfma_f32_16x16x32_bf16 v[90:93], v[140:143], v[178:181], v[90:93]
	v_mfma_f32_16x16x32_bf16 v[78:81], v[130:133], v[186:189], v[78:81]
	v_mfma_f32_16x16x32_bf16 v[74:77], v[140:143], v[186:189], v[74:77]
	v_mfma_f32_16x16x32_bf16 v[70:73], v[130:133], v[198:201], v[70:73]
	v_mfma_f32_16x16x32_bf16 v[66:69], v[140:143], v[198:201], v[66:69]
	v_mfma_f32_16x16x32_bf16 v[110:113], v[134:137], v[174:177], v[110:113]
	v_mfma_f32_16x16x32_bf16 v[106:109], v[150:153], v[174:177], v[106:109]
	v_mfma_f32_16x16x32_bf16 v[94:97], v[134:137], v[182:185], v[94:97]
	v_mfma_f32_16x16x32_bf16 v[90:93], v[150:153], v[182:185], v[90:93]
	v_mfma_f32_16x16x32_bf16 v[78:81], v[134:137], v[194:197], v[78:81]
	v_mfma_f32_16x16x32_bf16 v[74:77], v[150:153], v[194:197], v[74:77]
	v_mfma_f32_16x16x32_bf16 v[70:73], v[134:137], v[202:205], v[70:73]
	v_mfma_f32_16x16x32_bf16 v[66:69], v[150:153], v[202:205], v[66:69]
	v_mfma_f32_16x16x32_bf16 v[46:49], v[154:157], v[170:173], v[46:49]
	v_mfma_f32_16x16x32_bf16 v[42:45], v[162:165], v[170:173], v[42:45]
	v_mfma_f32_16x16x32_bf16 v[26:29], v[154:157], v[178:181], v[26:29]
	v_mfma_f32_16x16x32_bf16 v[22:25], v[162:165], v[178:181], v[22:25]
	v_mfma_f32_16x16x32_bf16 v[6:9], v[154:157], v[186:189], v[6:9]
	v_mfma_f32_16x16x32_bf16 v[2:5], v[162:165], v[186:189], v[2:5]
	v_mfma_f32_16x16x32_bf16 v[18:21], v[154:157], v[198:201], v[18:21]
	v_mfma_f32_16x16x32_bf16 v[30:33], v[162:165], v[198:201], v[30:33]
	v_mfma_f32_16x16x32_bf16 v[46:49], v[158:161], v[174:177], v[46:49]
	v_mfma_f32_16x16x32_bf16 v[42:45], v[166:169], v[174:177], v[42:45]
	v_mfma_f32_16x16x32_bf16 v[26:29], v[158:161], v[182:185], v[26:29]
	v_mfma_f32_16x16x32_bf16 v[22:25], v[166:169], v[182:185], v[22:25]
	v_mfma_f32_16x16x32_bf16 v[6:9], v[158:161], v[194:197], v[6:9]
	v_mfma_f32_16x16x32_bf16 v[2:5], v[166:169], v[194:197], v[2:5]
	v_mfma_f32_16x16x32_bf16 v[18:21], v[158:161], v[202:205], v[18:21]
	v_mfma_f32_16x16x32_bf16 v[30:33], v[166:169], v[202:205], v[30:33]
	s_barrier
	s_add_u32 s72, s72, 0x10000
	s_addc_u32 s73, s73, 0
	s_cmp_ge_i32 s74, s59
	s_mov_b64 s[48:49], s[50:51]
	s_mov_b32 s52, s74
	s_cbranch_scc0 .LBB0_707

.LBB0_890:
	s_add_u32 s34, s26, 0x10000
	s_addc_u32 s35, s27, 0
	s_and_b64 s[30:31], s[48:49], exec
	s_cselect_b32 s47, s41, s35
	s_cselect_b32 s46, s40, s34
	s_add_u32 s65, s28, 0x10000
	s_addc_u32 s66, s29, 0
	s_add_u32 s30, s46, 0x8000
	s_addc_u32 s31, s47, 0
	s_add_i32 s67, 0, 0x10000
	s_and_b64 s[34:35], s[48:49], exec
	s_cselect_b32 s35, s45, s66
	s_cselect_b32 s34, s44, s65
	s_add_i32 s70, 0, 0x14000
	v_add_u32_e32 v114, s67, v236
	v_add_u32_e32 v115, s70, v236
	ds_read_b128 v[2:5], v114
	s_waitcnt lgkmcnt(0)
	ds_read_b128 v[6:9], v114 offset:1024
	ds_read_b128 v[10:13], v114 offset:2048
	ds_read_b128 v[14:17], v114 offset:3072
	ds_read_b128 v[18:21], v115
	ds_read_b128 v[22:25], v115 offset:1024
	ds_read_b128 v[26:29], v115 offset:2048
	ds_read_b128 v[30:33], v115 offset:3072
	s_add_u32 s68, s26, 0xc000
	s_addc_u32 s69, s27, 0
	s_add_i32 s65, s20, 0xc000
	s_mov_b32 m0, s65
	s_add_i32 s66, s20, 0xe000
	ds_read_b128 v[34:37], v237
	ds_read_b128 v[38:41], v237 offset:1024
	ds_read_b128 v[42:45], v237 offset:2048
	ds_read_b128 v[46:49], v237 offset:3072
	ds_read_b128 v[50:53], v237 offset:4096
	ds_read_b128 v[54:57], v237 offset:5120
	ds_read_b128 v[58:61], v237 offset:6144
	ds_read_b128 v[62:65], v237 offset:7168
	s_nop 0
	global_load_lds_dwordx4 v235, s[68:69]
	s_mov_b32 m0, s66
	s_nop 0
	global_load_lds_dwordx4 v226, s[68:69]
	s_waitcnt vmcnt(8)
	s_waitcnt lgkmcnt(0)
	s_barrier
	s_waitcnt lgkmcnt(0)
	v_mfma_f32_16x16x32_bf16 v[90:93], v[2:5], v[58:61], 0
	v_mfma_f32_16x16x32_bf16 v[66:69], v[2:5], v[34:37], 0
	v_mfma_f32_16x16x32_bf16 v[70:73], v[10:13], v[34:37], 0
	v_mfma_f32_16x16x32_bf16 v[74:77], v[2:5], v[42:45], 0
	v_mfma_f32_16x16x32_bf16 v[78:81], v[10:13], v[42:45], 0
	v_mfma_f32_16x16x32_bf16 v[82:85], v[2:5], v[50:53], 0
	v_mfma_f32_16x16x32_bf16 v[86:89], v[10:13], v[50:53], 0
	v_mfma_f32_16x16x32_bf16 v[98:101], v[6:9], v[62:65], v[90:93]
	v_mfma_f32_16x16x32_bf16 v[90:93], v[10:13], v[58:61], 0
	v_mfma_f32_16x16x32_bf16 v[66:69], v[6:9], v[38:41], v[66:69]
	v_mfma_f32_16x16x32_bf16 v[70:73], v[14:17], v[38:41], v[70:73]
	v_mfma_f32_16x16x32_bf16 v[74:77], v[6:9], v[46:49], v[74:77]
	v_mfma_f32_16x16x32_bf16 v[78:81], v[14:17], v[46:49], v[78:81]
	v_mfma_f32_16x16x32_bf16 v[82:85], v[6:9], v[54:57], v[82:85]
	v_mfma_f32_16x16x32_bf16 v[86:89], v[14:17], v[54:57], v[86:89]
	v_mfma_f32_16x16x32_bf16 v[102:105], v[14:17], v[62:65], v[90:93]
	v_mfma_f32_16x16x32_bf16 v[90:93], v[18:21], v[34:37], 0
	v_mfma_f32_16x16x32_bf16 v[34:37], v[26:29], v[34:37], 0
	v_mfma_f32_16x16x32_bf16 v[118:121], v[22:25], v[38:41], v[90:93]
	v_mfma_f32_16x16x32_bf16 v[34:37], v[30:33], v[38:41], v[34:37]
	v_mfma_f32_16x16x32_bf16 v[38:41], v[18:21], v[42:45], 0
	v_mfma_f32_16x16x32_bf16 v[42:45], v[26:29], v[42:45], 0
	v_mfma_f32_16x16x32_bf16 v[38:41], v[22:25], v[46:49], v[38:41]
	v_mfma_f32_16x16x32_bf16 v[42:45], v[30:33], v[46:49], v[42:45]
	v_mfma_f32_16x16x32_bf16 v[46:49], v[18:21], v[50:53], 0
	v_mfma_f32_16x16x32_bf16 v[50:53], v[26:29], v[50:53], 0
	v_mfma_f32_16x16x32_bf16 v[46:49], v[22:25], v[54:57], v[46:49]
	v_mfma_f32_16x16x32_bf16 v[50:53], v[30:33], v[54:57], v[50:53]
	v_mfma_f32_16x16x32_bf16 v[54:57], v[18:21], v[58:61], 0
	v_mfma_f32_16x16x32_bf16 v[58:61], v[26:29], v[58:61], 0
	v_mfma_f32_16x16x32_bf16 v[54:57], v[22:25], v[62:65], v[54:57]
	v_mfma_f32_16x16x32_bf16 v[58:61], v[30:33], v[62:65], v[58:61]
	s_barrier
	s_add_i32 s67, s67, s18
	s_add_i32 s68, s67, 0x2000
	s_mov_b32 m0, s67
	s_add_u32 s72, s34, 0x4000
	ds_read_b128 v[62:65], v237 offset:16384
	ds_read_b128 v[90:93], v237 offset:17408
	ds_read_b128 v[94:97], v237 offset:18432
	ds_read_b128 v[106:109], v237 offset:19456
	ds_read_b128 v[110:113], v237 offset:20480
	ds_read_b128 v[122:125], v237 offset:21504
	ds_read_b128 v[126:129], v237 offset:22528
	ds_read_b128 v[130:133], v237 offset:23552
	s_addc_u32 s73, s35, 0
	global_load_lds_dwordx4 v227, s[34:35]
	s_mov_b32 m0, s68
	s_add_i32 s69, s70, s18
	s_add_i32 s70, s69, 0x2000
	global_load_lds_dwordx4 v0, s[34:35]
	s_mov_b32 m0, s69
	s_nop 0
	global_load_lds_dwordx4 v227, s[72:73]
	s_mov_b32 m0, s70
	s_nop 0
	global_load_lds_dwordx4 v0, s[72:73]
	s_mov_b32 m0, s20
	s_nop 0
	global_load_lds_dwordx4 v235, s[46:47]
	s_mov_b32 m0, s25
	s_nop 0
	global_load_lds_dwordx4 v226, s[46:47]
	s_waitcnt vmcnt(8)
	s_waitcnt lgkmcnt(0)
	s_barrier
	s_waitcnt lgkmcnt(0)
	v_mfma_f32_16x16x32_bf16 v[134:137], v[2:5], v[62:65], 0
	v_mfma_f32_16x16x32_bf16 v[142:145], v[2:5], v[94:97], 0
	v_mfma_f32_16x16x32_bf16 v[150:153], v[2:5], v[110:113], 0
	v_mfma_f32_16x16x32_bf16 v[2:5], v[2:5], v[126:129], 0
	v_mfma_f32_16x16x32_bf16 v[134:137], v[6:9], v[90:93], v[134:137]
	v_mfma_f32_16x16x32_bf16 v[142:145], v[6:9], v[106:109], v[142:145]
	v_mfma_f32_16x16x32_bf16 v[150:153], v[6:9], v[122:125], v[150:153]
	v_mfma_f32_16x16x32_bf16 v[2:5], v[6:9], v[130:133], v[2:5]
	v_mfma_f32_16x16x32_bf16 v[6:9], v[10:13], v[126:129], 0
	v_mfma_f32_16x16x32_bf16 v[138:141], v[10:13], v[62:65], 0
	v_mfma_f32_16x16x32_bf16 v[146:149], v[10:13], v[94:97], 0
	v_mfma_f32_16x16x32_bf16 v[154:157], v[10:13], v[110:113], 0
	v_mfma_f32_16x16x32_bf16 v[6:9], v[14:17], v[130:133], v[6:9]
	v_mfma_f32_16x16x32_bf16 v[138:141], v[14:17], v[90:93], v[138:141]
	v_mfma_f32_16x16x32_bf16 v[146:149], v[14:17], v[106:109], v[146:149]
	v_mfma_f32_16x16x32_bf16 v[154:157], v[14:17], v[122:125], v[154:157]
	v_mfma_f32_16x16x32_bf16 v[10:13], v[18:21], v[62:65], 0
	v_mfma_f32_16x16x32_bf16 v[158:161], v[22:25], v[90:93], v[10:13]
	v_mfma_f32_16x16x32_bf16 v[10:13], v[26:29], v[62:65], 0
	v_mfma_f32_16x16x32_bf16 v[162:165], v[30:33], v[90:93], v[10:13]
	v_mfma_f32_16x16x32_bf16 v[10:13], v[18:21], v[94:97], 0
	v_mfma_f32_16x16x32_bf16 v[174:177], v[22:25], v[106:109], v[10:13]
	v_mfma_f32_16x16x32_bf16 v[10:13], v[26:29], v[94:97], 0
	v_mfma_f32_16x16x32_bf16 v[178:181], v[30:33], v[106:109], v[10:13]
	v_mfma_f32_16x16x32_bf16 v[10:13], v[18:21], v[110:113], 0
	v_mfma_f32_16x16x32_bf16 v[182:185], v[22:25], v[122:125], v[10:13]
	v_mfma_f32_16x16x32_bf16 v[10:13], v[26:29], v[110:113], 0
	v_mfma_f32_16x16x32_bf16 v[122:125], v[30:33], v[122:125], v[10:13]
	v_mfma_f32_16x16x32_bf16 v[10:13], v[18:21], v[126:129], 0
	v_mfma_f32_16x16x32_bf16 v[186:189], v[22:25], v[130:133], v[10:13]
	v_mfma_f32_16x16x32_bf16 v[10:13], v[26:29], v[126:129], 0
	v_mfma_f32_16x16x32_bf16 v[130:133], v[30:33], v[130:133], v[10:13]
	s_barrier
	s_add_i32 s71, 0, 0x18000
	s_add_i32 s74, 0, 0x1c000
	v_add_u32_e32 v116, s71, v236
	v_add_u32_e32 v117, s74, v236
	s_nop 0
	ds_read_b128 v[10:13], v116
	ds_read_b128 v[14:17], v116 offset:1024
	ds_read_b128 v[18:21], v116 offset:2048
	ds_read_b128 v[22:25], v116 offset:3072
	ds_read_b128 v[194:197], v117
	ds_read_b128 v[198:201], v117 offset:1024
	ds_read_b128 v[202:205], v117 offset:2048
	ds_read_b128 v[206:209], v117 offset:3072
	s_add_u32 s46, s46, 0x4000
	s_addc_u32 s47, s47, 0
	s_mov_b32 m0, s54
	ds_read_b128 v[26:29], v237 offset:32768
	ds_read_b128 v[30:33], v237 offset:33792
	ds_read_b128 v[62:65], v237 offset:34816
	ds_read_b128 v[210:213], v237 offset:35840
	ds_read_b128 v[214:217], v237 offset:36864
	ds_read_b128 v[218:221], v237 offset:37888
	ds_read_b128 v[222:225], v237 offset:38912
	ds_read_b128 v[238:241], v237 offset:39936
	s_nop 0
	global_load_lds_dwordx4 v235, s[46:47]
	s_mov_b32 m0, s55
	s_nop 0
	global_load_lds_dwordx4 v226, s[46:47]
	s_waitcnt vmcnt(8)
	s_waitcnt lgkmcnt(0)
	s_barrier
	s_waitcnt lgkmcnt(0)
	v_mfma_f32_16x16x32_bf16 v[66:69], v[10:13], v[26:29], v[66:69]
	v_mfma_f32_16x16x32_bf16 v[166:169], v[14:17], v[30:33], v[66:69]
	v_mfma_f32_16x16x32_bf16 v[66:69], v[18:21], v[26:29], v[70:73]
	v_mfma_f32_16x16x32_bf16 v[170:173], v[22:25], v[30:33], v[66:69]
	v_mfma_f32_16x16x32_bf16 v[66:69], v[10:13], v[62:65], v[74:77]
	v_mfma_f32_16x16x32_bf16 v[110:113], v[14:17], v[210:213], v[66:69]
	v_mfma_f32_16x16x32_bf16 v[66:69], v[18:21], v[62:65], v[78:81]
	v_mfma_f32_16x16x32_bf16 v[106:109], v[22:25], v[210:213], v[66:69]
	v_mfma_f32_16x16x32_bf16 v[66:69], v[10:13], v[214:217], v[82:85]
	v_mfma_f32_16x16x32_bf16 v[94:97], v[14:17], v[218:221], v[66:69]
	v_mfma_f32_16x16x32_bf16 v[66:69], v[18:21], v[214:217], v[86:89]
	v_mfma_f32_16x16x32_bf16 v[90:93], v[22:25], v[218:221], v[66:69]
	v_mfma_f32_16x16x32_bf16 v[66:69], v[10:13], v[222:225], v[98:101]
	v_mfma_f32_16x16x32_bf16 v[78:81], v[14:17], v[238:241], v[66:69]
	v_mfma_f32_16x16x32_bf16 v[66:69], v[18:21], v[222:225], v[102:105]
	v_mfma_f32_16x16x32_bf16 v[70:73], v[22:25], v[238:241], v[66:69]
	v_mfma_f32_16x16x32_bf16 v[66:69], v[194:197], v[26:29], v[118:121]
	v_mfma_f32_16x16x32_bf16 v[26:29], v[202:205], v[26:29], v[34:37]
	v_mfma_f32_16x16x32_bf16 v[118:121], v[206:209], v[30:33], v[26:29]
	v_mfma_f32_16x16x32_bf16 v[26:29], v[194:197], v[62:65], v[38:41]
	v_mfma_f32_16x16x32_bf16 v[102:105], v[198:201], v[210:213], v[26:29]
	v_mfma_f32_16x16x32_bf16 v[26:29], v[202:205], v[62:65], v[42:45]
	v_mfma_f32_16x16x32_bf16 v[98:101], v[206:209], v[210:213], v[26:29]
	v_mfma_f32_16x16x32_bf16 v[26:29], v[194:197], v[214:217], v[46:49]
	v_mfma_f32_16x16x32_bf16 v[86:89], v[198:201], v[218:221], v[26:29]
	v_mfma_f32_16x16x32_bf16 v[26:29], v[202:205], v[214:217], v[50:53]
	v_mfma_f32_16x16x32_bf16 v[82:85], v[206:209], v[218:221], v[26:29]
	v_mfma_f32_16x16x32_bf16 v[26:29], v[194:197], v[222:225], v[54:57]
	v_mfma_f32_16x16x32_bf16 v[62:65], v[198:201], v[238:241], v[26:29]
	v_mfma_f32_16x16x32_bf16 v[26:29], v[202:205], v[222:225], v[58:61]
	v_mfma_f32_16x16x32_bf16 v[126:129], v[198:201], v[30:33], v[66:69]
	v_mfma_f32_16x16x32_bf16 v[54:57], v[206:209], v[238:241], v[26:29]
	s_barrier
	s_add_u32 s72, s34, 0x8000
	s_addc_u32 s73, s35, 0
	s_add_i32 s46, s71, s18
	s_add_i32 s47, s46, 0x2000
	s_mov_b32 m0, s46
	s_add_u32 s34, s34, 0xc000
	ds_read_b128 v[34:37], v237 offset:49152
	ds_read_b128 v[38:41], v237 offset:50176
	ds_read_b128 v[210:213], v237 offset:51200
	ds_read_b128 v[214:217], v237 offset:52224
	ds_read_b128 v[218:221], v237 offset:53248
	ds_read_b128 v[222:225], v237 offset:54272
	ds_read_b128 v[238:241], v237 offset:55296
	ds_read_b128 v[242:245], v237 offset:56320
	s_addc_u32 s35, s35, 0
	global_load_lds_dwordx4 v227, s[72:73]
	s_mov_b32 m0, s47
	s_add_i32 s71, s74, s18
	s_nop 0
	global_load_lds_dwordx4 v0, s[72:73]
	s_mov_b32 m0, s71
	s_add_i32 s72, s71, 0x2000
	s_nop 0
	global_load_lds_dwordx4 v227, s[34:35]
	s_mov_b32 m0, s72
	s_nop 0
	global_load_lds_dwordx4 v0, s[34:35]
	s_mov_b32 m0, s58
	s_nop 0
	global_load_lds_dwordx4 v235, s[30:31]
	s_mov_b32 m0, s59
	s_nop 0
	global_load_lds_dwordx4 v226, s[30:31]
	s_waitcnt vmcnt(8)
	s_waitcnt lgkmcnt(0)
	s_barrier
	s_waitcnt lgkmcnt(0)
	v_mfma_f32_16x16x32_bf16 v[26:29], v[10:13], v[34:37], v[134:137]
	v_mfma_f32_16x16x32_bf16 v[74:77], v[14:17], v[38:41], v[26:29]
	v_mfma_f32_16x16x32_bf16 v[26:29], v[18:21], v[34:37], v[138:141]
	v_mfma_f32_16x16x32_bf16 v[66:69], v[22:25], v[38:41], v[26:29]
	v_mfma_f32_16x16x32_bf16 v[26:29], v[10:13], v[210:213], v[142:145]
	v_mfma_f32_16x16x32_bf16 v[46:49], v[14:17], v[214:217], v[26:29]
	v_mfma_f32_16x16x32_bf16 v[26:29], v[18:21], v[210:213], v[146:149]
	v_mfma_f32_16x16x32_bf16 v[42:45], v[22:25], v[214:217], v[26:29]
	v_mfma_f32_16x16x32_bf16 v[26:29], v[10:13], v[218:221], v[150:153]
	v_mfma_f32_16x16x32_bf16 v[2:5], v[10:13], v[238:241], v[2:5]
	v_mfma_f32_16x16x32_bf16 v[30:33], v[14:17], v[222:225], v[26:29]
	v_mfma_f32_16x16x32_bf16 v[26:29], v[18:21], v[218:221], v[154:157]
	v_mfma_f32_16x16x32_bf16 v[14:17], v[14:17], v[242:245], v[2:5]
	v_mfma_f32_16x16x32_bf16 v[2:5], v[18:21], v[238:241], v[6:9]
	v_mfma_f32_16x16x32_bf16 v[26:29], v[22:25], v[222:225], v[26:29]
	v_mfma_f32_16x16x32_bf16 v[10:13], v[22:25], v[242:245], v[2:5]
	v_mfma_f32_16x16x32_bf16 v[2:5], v[194:197], v[34:37], v[158:161]
	v_mfma_f32_16x16x32_bf16 v[58:61], v[198:201], v[38:41], v[2:5]
	v_mfma_f32_16x16x32_bf16 v[2:5], v[202:205], v[34:37], v[162:165]
	v_mfma_f32_16x16x32_bf16 v[50:53], v[206:209], v[38:41], v[2:5]
	v_mfma_f32_16x16x32_bf16 v[2:5], v[194:197], v[210:213], v[174:177]
	v_mfma_f32_16x16x32_bf16 v[38:41], v[198:201], v[214:217], v[2:5]
	v_mfma_f32_16x16x32_bf16 v[2:5], v[202:205], v[210:213], v[178:181]
	v_mfma_f32_16x16x32_bf16 v[34:37], v[206:209], v[214:217], v[2:5]
	v_mfma_f32_16x16x32_bf16 v[2:5], v[194:197], v[218:221], v[182:185]
	v_mfma_f32_16x16x32_bf16 v[22:25], v[198:201], v[222:225], v[2:5]
	v_mfma_f32_16x16x32_bf16 v[2:5], v[202:205], v[218:221], v[122:125]
	v_mfma_f32_16x16x32_bf16 v[18:21], v[206:209], v[222:225], v[2:5]
	v_mfma_f32_16x16x32_bf16 v[2:5], v[194:197], v[238:241], v[186:189]
	v_mfma_f32_16x16x32_bf16 v[6:9], v[198:201], v[242:245], v[2:5]
	v_mfma_f32_16x16x32_bf16 v[2:5], v[202:205], v[238:241], v[130:133]
	v_mfma_f32_16x16x32_bf16 v[2:5], v[206:209], v[242:245], v[2:5]
	s_barrier
	s_andn2_b64 vcc, exec, s[50:51]
	s_cbranch_vccnz .LBB0_893
	s_add_u32 s73, s28, 0x20000
	s_addc_u32 s74, s29, 0
	s_add_u32 s26, s26, 0x1c000
	s_addc_u32 s27, s27, 0
	s_mov_b32 s75, 4
.LBB0_892:
	ds_read_b128 v[122:125], v114
	ds_read_b128 v[130:133], v114 offset:1024
	ds_read_b128 v[134:137], v114 offset:2048
	ds_read_b128 v[138:141], v114 offset:3072
	ds_read_b128 v[142:145], v115
	ds_read_b128 v[146:149], v115 offset:1024
	ds_read_b128 v[150:153], v115 offset:2048
	ds_read_b128 v[154:157], v115 offset:3072
	s_add_u32 s28, s26, 0x4000
	s_addc_u32 s29, s27, 0
	s_cmp_eq_u32 s56, s75
	s_cselect_b32 s34, s40, s28
	s_cselect_b32 s35, s41, s29
	s_cselect_b32 s30, s44, s73
	s_cselect_b32 s31, s45, s74
	s_add_u32 s28, s34, 0x8000
	s_addc_u32 s29, s35, 0
	s_mov_b32 m0, s65
	ds_read_b128 v[158:161], v237
	ds_read_b128 v[162:165], v237 offset:1024
	ds_read_b128 v[174:177], v237 offset:2048
	ds_read_b128 v[178:181], v237 offset:3072
	ds_read_b128 v[182:185], v237 offset:4096
	ds_read_b128 v[186:189], v237 offset:5120
	ds_read_b128 v[194:197], v237 offset:6144
	ds_read_b128 v[198:201], v237 offset:7168
	s_nop 0
	global_load_lds_dwordx4 v235, s[26:27]
	s_mov_b32 m0, s66
	s_nop 0
	global_load_lds_dwordx4 v226, s[26:27]
	s_waitcnt vmcnt(8)
	s_waitcnt lgkmcnt(0)
	s_barrier
	s_waitcnt lgkmcnt(0)
	v_mfma_f32_16x16x32_bf16 v[166:169], v[122:125], v[158:161], v[166:169]
	v_mfma_f32_16x16x32_bf16 v[170:173], v[134:137], v[158:161], v[170:173]
	v_mfma_f32_16x16x32_bf16 v[110:113], v[122:125], v[174:177], v[110:113]
	v_mfma_f32_16x16x32_bf16 v[106:109], v[134:137], v[174:177], v[106:109]
	v_mfma_f32_16x16x32_bf16 v[94:97], v[122:125], v[182:185], v[94:97]
	v_mfma_f32_16x16x32_bf16 v[90:93], v[134:137], v[182:185], v[90:93]
	v_mfma_f32_16x16x32_bf16 v[78:81], v[122:125], v[194:197], v[78:81]
	v_mfma_f32_16x16x32_bf16 v[70:73], v[134:137], v[194:197], v[70:73]
	v_mfma_f32_16x16x32_bf16 v[166:169], v[130:133], v[162:165], v[166:169]
	v_mfma_f32_16x16x32_bf16 v[170:173], v[138:141], v[162:165], v[170:173]
	v_mfma_f32_16x16x32_bf16 v[110:113], v[130:133], v[178:181], v[110:113]
	v_mfma_f32_16x16x32_bf16 v[106:109], v[138:141], v[178:181], v[106:109]
	v_mfma_f32_16x16x32_bf16 v[94:97], v[130:133], v[186:189], v[94:97]
	v_mfma_f32_16x16x32_bf16 v[90:93], v[138:141], v[186:189], v[90:93]
	v_mfma_f32_16x16x32_bf16 v[78:81], v[130:133], v[198:201], v[78:81]
	v_mfma_f32_16x16x32_bf16 v[70:73], v[138:141], v[198:201], v[70:73]
	v_mfma_f32_16x16x32_bf16 v[126:129], v[142:145], v[158:161], v[126:129]
	v_mfma_f32_16x16x32_bf16 v[118:121], v[150:153], v[158:161], v[118:121]
	v_mfma_f32_16x16x32_bf16 v[102:105], v[142:145], v[174:177], v[102:105]
	v_mfma_f32_16x16x32_bf16 v[98:101], v[150:153], v[174:177], v[98:101]
	v_mfma_f32_16x16x32_bf16 v[86:89], v[142:145], v[182:185], v[86:89]
	v_mfma_f32_16x16x32_bf16 v[82:85], v[150:153], v[182:185], v[82:85]
	v_mfma_f32_16x16x32_bf16 v[62:65], v[142:145], v[194:197], v[62:65]
	v_mfma_f32_16x16x32_bf16 v[54:57], v[150:153], v[194:197], v[54:57]
	v_mfma_f32_16x16x32_bf16 v[126:129], v[146:149], v[162:165], v[126:129]
	v_mfma_f32_16x16x32_bf16 v[118:121], v[154:157], v[162:165], v[118:121]
	v_mfma_f32_16x16x32_bf16 v[102:105], v[146:149], v[178:181], v[102:105]
	v_mfma_f32_16x16x32_bf16 v[98:101], v[154:157], v[178:181], v[98:101]
	v_mfma_f32_16x16x32_bf16 v[86:89], v[146:149], v[186:189], v[86:89]
	v_mfma_f32_16x16x32_bf16 v[82:85], v[154:157], v[186:189], v[82:85]
	v_mfma_f32_16x16x32_bf16 v[62:65], v[146:149], v[198:201], v[62:65]
	v_mfma_f32_16x16x32_bf16 v[54:57], v[154:157], v[198:201], v[54:57]
	s_barrier
	s_mov_b32 m0, s67
	ds_read_b128 v[158:161], v237 offset:16384
	ds_read_b128 v[162:165], v237 offset:17408
	ds_read_b128 v[174:177], v237 offset:18432
	ds_read_b128 v[178:181], v237 offset:19456
	ds_read_b128 v[182:185], v237 offset:20480
	ds_read_b128 v[186:189], v237 offset:21504
	ds_read_b128 v[194:197], v237 offset:22528
	ds_read_b128 v[198:201], v237 offset:23552
	s_add_u32 s76, s30, 0x4000
	global_load_lds_dwordx4 v227, s[30:31]
	s_mov_b32 m0, s68
	s_addc_u32 s77, s31, 0
	global_load_lds_dwordx4 v0, s[30:31]
	s_mov_b32 m0, s69
	s_nop 0
	global_load_lds_dwordx4 v227, s[76:77]
	s_mov_b32 m0, s70
	s_nop 0
	global_load_lds_dwordx4 v0, s[76:77]
	s_mov_b32 m0, s20
	s_nop 0
	global_load_lds_dwordx4 v235, s[34:35]
	s_mov_b32 m0, s25
	s_nop 0
	global_load_lds_dwordx4 v226, s[34:35]
	s_waitcnt vmcnt(8)
	s_waitcnt lgkmcnt(0)
	s_barrier
	s_waitcnt lgkmcnt(0)
	v_mfma_f32_16x16x32_bf16 v[74:77], v[122:125], v[158:161], v[74:77]
	v_mfma_f32_16x16x32_bf16 v[66:69], v[134:137], v[158:161], v[66:69]
	v_mfma_f32_16x16x32_bf16 v[46:49], v[122:125], v[174:177], v[46:49]
	v_mfma_f32_16x16x32_bf16 v[42:45], v[134:137], v[174:177], v[42:45]
	v_mfma_f32_16x16x32_bf16 v[30:33], v[122:125], v[182:185], v[30:33]
	v_mfma_f32_16x16x32_bf16 v[26:29], v[134:137], v[182:185], v[26:29]
	v_mfma_f32_16x16x32_bf16 v[14:17], v[122:125], v[194:197], v[14:17]
	v_mfma_f32_16x16x32_bf16 v[10:13], v[134:137], v[194:197], v[10:13]
	v_mfma_f32_16x16x32_bf16 v[74:77], v[130:133], v[162:165], v[74:77]
	v_mfma_f32_16x16x32_bf16 v[66:69], v[138:141], v[162:165], v[66:69]
	v_mfma_f32_16x16x32_bf16 v[46:49], v[130:133], v[178:181], v[46:49]
	v_mfma_f32_16x16x32_bf16 v[42:45], v[138:141], v[178:181], v[42:45]
	v_mfma_f32_16x16x32_bf16 v[30:33], v[130:133], v[186:189], v[30:33]
	v_mfma_f32_16x16x32_bf16 v[26:29], v[138:141], v[186:189], v[26:29]
	v_mfma_f32_16x16x32_bf16 v[14:17], v[130:133], v[198:201], v[14:17]
	v_mfma_f32_16x16x32_bf16 v[10:13], v[138:141], v[198:201], v[10:13]
	v_mfma_f32_16x16x32_bf16 v[58:61], v[142:145], v[158:161], v[58:61]
	v_mfma_f32_16x16x32_bf16 v[50:53], v[150:153], v[158:161], v[50:53]
	v_mfma_f32_16x16x32_bf16 v[38:41], v[142:145], v[174:177], v[38:41]
	v_mfma_f32_16x16x32_bf16 v[34:37], v[150:153], v[174:177], v[34:37]
	v_mfma_f32_16x16x32_bf16 v[22:25], v[142:145], v[182:185], v[22:25]
	v_mfma_f32_16x16x32_bf16 v[18:21], v[150:153], v[182:185], v[18:21]
	v_mfma_f32_16x16x32_bf16 v[6:9], v[142:145], v[194:197], v[6:9]
	v_mfma_f32_16x16x32_bf16 v[2:5], v[150:153], v[194:197], v[2:5]
	v_mfma_f32_16x16x32_bf16 v[58:61], v[146:149], v[162:165], v[58:61]
	v_mfma_f32_16x16x32_bf16 v[50:53], v[154:157], v[162:165], v[50:53]
	v_mfma_f32_16x16x32_bf16 v[38:41], v[146:149], v[178:181], v[38:41]
	v_mfma_f32_16x16x32_bf16 v[34:37], v[154:157], v[178:181], v[34:37]
	v_mfma_f32_16x16x32_bf16 v[22:25], v[146:149], v[186:189], v[22:25]
	v_mfma_f32_16x16x32_bf16 v[18:21], v[154:157], v[186:189], v[18:21]
	v_mfma_f32_16x16x32_bf16 v[6:9], v[146:149], v[198:201], v[6:9]
	v_mfma_f32_16x16x32_bf16 v[2:5], v[154:157], v[198:201], v[2:5]
	s_barrier
	ds_read_b128 v[122:125], v116
	ds_read_b128 v[130:133], v116 offset:1024
	ds_read_b128 v[134:137], v116 offset:2048
	ds_read_b128 v[138:141], v116 offset:3072
	ds_read_b128 v[142:145], v117
	ds_read_b128 v[146:149], v117 offset:1024
	ds_read_b128 v[150:153], v117 offset:2048
	ds_read_b128 v[154:157], v117 offset:3072
	s_add_u32 s34, s34, 0x4000
	s_addc_u32 s35, s35, 0
	s_mov_b32 m0, s54
	ds_read_b128 v[158:161], v237 offset:32768
	ds_read_b128 v[162:165], v237 offset:33792
	ds_read_b128 v[174:177], v237 offset:34816
	ds_read_b128 v[178:181], v237 offset:35840
	ds_read_b128 v[182:185], v237 offset:36864
	ds_read_b128 v[186:189], v237 offset:37888
	ds_read_b128 v[194:197], v237 offset:38912
	ds_read_b128 v[198:201], v237 offset:39936
	s_nop 0
	global_load_lds_dwordx4 v235, s[34:35]
	s_mov_b32 m0, s55
	s_nop 0
	global_load_lds_dwordx4 v226, s[34:35]
	s_waitcnt vmcnt(8)
	s_waitcnt lgkmcnt(0)
	s_barrier
	s_waitcnt lgkmcnt(0)
	v_mfma_f32_16x16x32_bf16 v[166:169], v[122:125], v[158:161], v[166:169]
	v_mfma_f32_16x16x32_bf16 v[170:173], v[134:137], v[158:161], v[170:173]
	v_mfma_f32_16x16x32_bf16 v[110:113], v[122:125], v[174:177], v[110:113]
	v_mfma_f32_16x16x32_bf16 v[106:109], v[134:137], v[174:177], v[106:109]
	v_mfma_f32_16x16x32_bf16 v[94:97], v[122:125], v[182:185], v[94:97]
	v_mfma_f32_16x16x32_bf16 v[90:93], v[134:137], v[182:185], v[90:93]
	v_mfma_f32_16x16x32_bf16 v[78:81], v[122:125], v[194:197], v[78:81]
	v_mfma_f32_16x16x32_bf16 v[70:73], v[134:137], v[194:197], v[70:73]
	v_mfma_f32_16x16x32_bf16 v[166:169], v[130:133], v[162:165], v[166:169]
	v_mfma_f32_16x16x32_bf16 v[170:173], v[138:141], v[162:165], v[170:173]
	v_mfma_f32_16x16x32_bf16 v[110:113], v[130:133], v[178:181], v[110:113]
	v_mfma_f32_16x16x32_bf16 v[106:109], v[138:141], v[178:181], v[106:109]
	v_mfma_f32_16x16x32_bf16 v[94:97], v[130:133], v[186:189], v[94:97]
	v_mfma_f32_16x16x32_bf16 v[90:93], v[138:141], v[186:189], v[90:93]
	v_mfma_f32_16x16x32_bf16 v[78:81], v[130:133], v[198:201], v[78:81]
	v_mfma_f32_16x16x32_bf16 v[70:73], v[138:141], v[198:201], v[70:73]
	v_mfma_f32_16x16x32_bf16 v[126:129], v[142:145], v[158:161], v[126:129]
	v_mfma_f32_16x16x32_bf16 v[118:121], v[150:153], v[158:161], v[118:121]
	v_mfma_f32_16x16x32_bf16 v[102:105], v[142:145], v[174:177], v[102:105]
	v_mfma_f32_16x16x32_bf16 v[98:101], v[150:153], v[174:177], v[98:101]
	v_mfma_f32_16x16x32_bf16 v[86:89], v[142:145], v[182:185], v[86:89]
	v_mfma_f32_16x16x32_bf16 v[82:85], v[150:153], v[182:185], v[82:85]
	v_mfma_f32_16x16x32_bf16 v[62:65], v[142:145], v[194:197], v[62:65]
	v_mfma_f32_16x16x32_bf16 v[54:57], v[150:153], v[194:197], v[54:57]
	v_mfma_f32_16x16x32_bf16 v[126:129], v[146:149], v[162:165], v[126:129]
	v_mfma_f32_16x16x32_bf16 v[118:121], v[154:157], v[162:165], v[118:121]
	v_mfma_f32_16x16x32_bf16 v[102:105], v[146:149], v[178:181], v[102:105]
	v_mfma_f32_16x16x32_bf16 v[98:101], v[154:157], v[178:181], v[98:101]
	v_mfma_f32_16x16x32_bf16 v[86:89], v[146:149], v[186:189], v[86:89]
	v_mfma_f32_16x16x32_bf16 v[82:85], v[154:157], v[186:189], v[82:85]
	v_mfma_f32_16x16x32_bf16 v[62:65], v[146:149], v[198:201], v[62:65]
	v_mfma_f32_16x16x32_bf16 v[54:57], v[154:157], v[198:201], v[54:57]
	s_barrier
	s_add_u32 s34, s30, 0x8000
	s_mov_b32 m0, s46
	s_addc_u32 s35, s31, 0
	ds_read_b128 v[158:161], v237 offset:49152
	ds_read_b128 v[162:165], v237 offset:50176
	ds_read_b128 v[174:177], v237 offset:51200
	ds_read_b128 v[178:181], v237 offset:52224
	ds_read_b128 v[182:185], v237 offset:53248
	ds_read_b128 v[186:189], v237 offset:54272
	ds_read_b128 v[194:197], v237 offset:55296
	ds_read_b128 v[198:201], v237 offset:56320
	s_add_u32 s30, s30, 0xc000
	global_load_lds_dwordx4 v227, s[34:35]
	s_mov_b32 m0, s47
	s_addc_u32 s31, s31, 0
	global_load_lds_dwordx4 v0, s[34:35]
	s_mov_b32 m0, s71
	s_nop 0
	global_load_lds_dwordx4 v227, s[30:31]
	s_mov_b32 m0, s72
	s_nop 0
	global_load_lds_dwordx4 v0, s[30:31]
	s_mov_b32 m0, s58
	s_nop 0
	global_load_lds_dwordx4 v235, s[28:29]
	s_mov_b32 m0, s59
	s_nop 0
	global_load_lds_dwordx4 v226, s[28:29]
	s_waitcnt vmcnt(8)
	s_waitcnt lgkmcnt(0)
	s_barrier
	s_waitcnt lgkmcnt(0)
	v_mfma_f32_16x16x32_bf16 v[74:77], v[122:125], v[158:161], v[74:77]
	v_mfma_f32_16x16x32_bf16 v[66:69], v[134:137], v[158:161], v[66:69]
	v_mfma_f32_16x16x32_bf16 v[46:49], v[122:125], v[174:177], v[46:49]
	v_mfma_f32_16x16x32_bf16 v[42:45], v[134:137], v[174:177], v[42:45]
	v_mfma_f32_16x16x32_bf16 v[30:33], v[122:125], v[182:185], v[30:33]
	v_mfma_f32_16x16x32_bf16 v[26:29], v[134:137], v[182:185], v[26:29]
	v_mfma_f32_16x16x32_bf16 v[14:17], v[122:125], v[194:197], v[14:17]
	v_mfma_f32_16x16x32_bf16 v[10:13], v[134:137], v[194:197], v[10:13]
	v_mfma_f32_16x16x32_bf16 v[74:77], v[130:133], v[162:165], v[74:77]
	v_mfma_f32_16x16x32_bf16 v[66:69], v[138:141], v[162:165], v[66:69]
	v_mfma_f32_16x16x32_bf16 v[46:49], v[130:133], v[178:181], v[46:49]
	v_mfma_f32_16x16x32_bf16 v[42:45], v[138:141], v[178:181], v[42:45]
	v_mfma_f32_16x16x32_bf16 v[30:33], v[130:133], v[186:189], v[30:33]
	v_mfma_f32_16x16x32_bf16 v[26:29], v[138:141], v[186:189], v[26:29]
	v_mfma_f32_16x16x32_bf16 v[14:17], v[130:133], v[198:201], v[14:17]
	v_mfma_f32_16x16x32_bf16 v[10:13], v[138:141], v[198:201], v[10:13]
	v_mfma_f32_16x16x32_bf16 v[58:61], v[142:145], v[158:161], v[58:61]
	v_mfma_f32_16x16x32_bf16 v[50:53], v[150:153], v[158:161], v[50:53]
	v_mfma_f32_16x16x32_bf16 v[38:41], v[142:145], v[174:177], v[38:41]
	v_mfma_f32_16x16x32_bf16 v[34:37], v[150:153], v[174:177], v[34:37]
	v_mfma_f32_16x16x32_bf16 v[22:25], v[142:145], v[182:185], v[22:25]
	v_mfma_f32_16x16x32_bf16 v[18:21], v[150:153], v[182:185], v[18:21]
	v_mfma_f32_16x16x32_bf16 v[6:9], v[142:145], v[194:197], v[6:9]
	v_mfma_f32_16x16x32_bf16 v[2:5], v[150:153], v[194:197], v[2:5]
	v_mfma_f32_16x16x32_bf16 v[58:61], v[146:149], v[162:165], v[58:61]
	v_mfma_f32_16x16x32_bf16 v[50:53], v[154:157], v[162:165], v[50:53]
	v_mfma_f32_16x16x32_bf16 v[38:41], v[146:149], v[178:181], v[38:41]
	v_mfma_f32_16x16x32_bf16 v[34:37], v[154:157], v[178:181], v[34:37]
	v_mfma_f32_16x16x32_bf16 v[22:25], v[146:149], v[186:189], v[22:25]
	v_mfma_f32_16x16x32_bf16 v[18:21], v[154:157], v[186:189], v[18:21]
	v_mfma_f32_16x16x32_bf16 v[6:9], v[146:149], v[198:201], v[6:9]
	v_mfma_f32_16x16x32_bf16 v[2:5], v[154:157], v[198:201], v[2:5]
	s_barrier
	s_add_i32 s28, s75, 2
	s_add_u32 s73, s73, 0x10000
	s_addc_u32 s74, s74, 0
	s_add_u32 s26, s26, 0x10000
	s_addc_u32 s27, s27, 0
	s_cmp_lt_i32 s75, s56
	s_mov_b32 s75, s28
	s_cbranch_scc1 .LBB0_892

.LBB0_965:
	s_add_u32 s34, s28, 0x10000
	s_addc_u32 s35, s29, 0
	s_and_b64 s[30:31], s[48:49], exec
	s_cselect_b32 s57, s43, s35
	s_cselect_b32 s56, s42, s34
	s_add_u32 s58, s26, 0x100
	s_addc_u32 s59, s27, 0
	s_add_u32 s30, s56, 0x8000
	s_addc_u32 s31, s57, 0
	s_add_i32 s74, 0, 0x10000
	s_and_b64 s[34:35], s[48:49], exec
	s_cselect_b32 s35, s55, s59
	s_cselect_b32 s34, s54, s58
	s_add_i32 s76, 0, 0x14000
	v_add_u32_e32 v132, s74, v218
	v_add_u32_e32 v133, s76, v218
	ds_read_b128 v[2:5], v132
	ds_read_b128 v[6:9], v132 offset:1024
	ds_read_b128 v[10:13], v132 offset:2048
	ds_read_b128 v[14:17], v132 offset:3072
	ds_read_b128 v[18:21], v133
	ds_read_b128 v[22:25], v133 offset:1024
	ds_read_b128 v[26:29], v133 offset:2048
	ds_read_b128 v[30:33], v133 offset:3072
	s_add_u32 s58, s28, 0xc000
	s_addc_u32 s59, s29, 0
	s_add_i32 s72, s18, 0xc000
	s_mov_b32 m0, s72
	s_add_i32 s73, s18, 0xe000
	ds_read_b128 v[34:37], v219
	ds_read_b128 v[38:41], v219 offset:1024
	ds_read_b128 v[42:45], v219 offset:2048
	ds_read_b128 v[46:49], v219 offset:3072
	ds_read_b128 v[50:53], v219 offset:4096
	ds_read_b128 v[54:57], v219 offset:5120
	ds_read_b128 v[58:61], v219 offset:6144
	ds_read_b128 v[62:65], v219 offset:7168
	s_nop 0
	global_load_lds_dwordx4 v217, s[58:59]
	s_mov_b32 m0, s73
	s_nop 0
	global_load_lds_dwordx4 v216, s[58:59]
	s_waitcnt vmcnt(8)
	s_waitcnt lgkmcnt(0)
	s_barrier
	s_waitcnt lgkmcnt(0)
	v_mfma_f32_16x16x32_bf16 v[86:89], v[10:13], v[50:53], 0
	v_mfma_f32_16x16x32_bf16 v[90:93], v[14:17], v[54:57], v[86:89]
	v_mfma_f32_16x16x32_bf16 v[86:89], v[2:5], v[58:61], 0
	v_mfma_f32_16x16x32_bf16 v[66:69], v[2:5], v[34:37], 0
	v_mfma_f32_16x16x32_bf16 v[70:73], v[10:13], v[34:37], 0
	v_mfma_f32_16x16x32_bf16 v[74:77], v[2:5], v[42:45], 0
	v_mfma_f32_16x16x32_bf16 v[78:81], v[10:13], v[42:45], 0
	v_mfma_f32_16x16x32_bf16 v[82:85], v[2:5], v[50:53], 0
	v_mfma_f32_16x16x32_bf16 v[94:97], v[6:9], v[62:65], v[86:89]
	v_mfma_f32_16x16x32_bf16 v[86:89], v[10:13], v[58:61], 0
	v_mfma_f32_16x16x32_bf16 v[66:69], v[6:9], v[38:41], v[66:69]
	v_mfma_f32_16x16x32_bf16 v[70:73], v[14:17], v[38:41], v[70:73]
	v_mfma_f32_16x16x32_bf16 v[74:77], v[6:9], v[46:49], v[74:77]
	v_mfma_f32_16x16x32_bf16 v[78:81], v[14:17], v[46:49], v[78:81]
	v_mfma_f32_16x16x32_bf16 v[82:85], v[6:9], v[54:57], v[82:85]
	v_mfma_f32_16x16x32_bf16 v[106:109], v[14:17], v[62:65], v[86:89]
	v_mfma_f32_16x16x32_bf16 v[86:89], v[18:21], v[34:37], 0
	v_mfma_f32_16x16x32_bf16 v[34:37], v[26:29], v[34:37], 0
	v_mfma_f32_16x16x32_bf16 v[110:113], v[22:25], v[38:41], v[86:89]
	v_mfma_f32_16x16x32_bf16 v[34:37], v[30:33], v[38:41], v[34:37]
	v_mfma_f32_16x16x32_bf16 v[38:41], v[18:21], v[42:45], 0
	v_mfma_f32_16x16x32_bf16 v[42:45], v[26:29], v[42:45], 0
	v_mfma_f32_16x16x32_bf16 v[38:41], v[22:25], v[46:49], v[38:41]
	v_mfma_f32_16x16x32_bf16 v[42:45], v[30:33], v[46:49], v[42:45]
	v_mfma_f32_16x16x32_bf16 v[46:49], v[18:21], v[50:53], 0
	v_mfma_f32_16x16x32_bf16 v[50:53], v[26:29], v[50:53], 0
	v_mfma_f32_16x16x32_bf16 v[136:139], v[30:33], v[54:57], v[50:53]
	v_mfma_f32_16x16x32_bf16 v[50:53], v[18:21], v[58:61], 0
	v_mfma_f32_16x16x32_bf16 v[140:143], v[22:25], v[62:65], v[50:53]
	v_mfma_f32_16x16x32_bf16 v[50:53], v[26:29], v[58:61], 0
	v_mfma_f32_16x16x32_bf16 v[46:49], v[22:25], v[54:57], v[46:49]
	v_mfma_f32_16x16x32_bf16 v[58:61], v[30:33], v[62:65], v[50:53]
	s_barrier
	s_add_i32 s74, s74, s15
	s_add_i32 s75, s74, 0x2000
	s_mov_b32 m0, s74
	s_add_u32 s58, s34, s36
	ds_read_b128 v[50:53], v219 offset:16384
	ds_read_b128 v[54:57], v219 offset:17408
	ds_read_b128 v[62:65], v219 offset:18432
	ds_read_b128 v[86:89], v219 offset:19456
	ds_read_b128 v[98:101], v219 offset:20480
	ds_read_b128 v[102:105], v219 offset:21504
	ds_read_b128 v[114:117], v219 offset:22528
	ds_read_b128 v[118:121], v219 offset:23552
	s_addc_u32 s59, s35, s37
	global_load_lds_dwordx4 v0, s[34:35]
	s_mov_b32 m0, s75
	s_add_i32 s76, s76, s15
	s_add_i32 s77, s76, 0x2000
	global_load_lds_dwordx4 v130, s[34:35]
	s_mov_b32 m0, s76
	s_nop 0
	global_load_lds_dwordx4 v0, s[58:59]
	s_mov_b32 m0, s77
	s_nop 0
	global_load_lds_dwordx4 v130, s[58:59]
	s_mov_b32 m0, s18
	s_nop 0
	global_load_lds_dwordx4 v217, s[56:57]
	s_mov_b32 m0, s20
	s_nop 0
	global_load_lds_dwordx4 v216, s[56:57]
	s_waitcnt vmcnt(8)
	s_waitcnt lgkmcnt(0)
	s_barrier
	s_waitcnt lgkmcnt(0)
	v_mfma_f32_16x16x32_bf16 v[122:125], v[2:5], v[50:53], 0
	v_mfma_f32_16x16x32_bf16 v[144:147], v[6:9], v[54:57], v[122:125]
	v_mfma_f32_16x16x32_bf16 v[122:125], v[10:13], v[50:53], 0
	v_mfma_f32_16x16x32_bf16 v[148:151], v[14:17], v[54:57], v[122:125]
	v_mfma_f32_16x16x32_bf16 v[122:125], v[2:5], v[62:65], 0
	v_mfma_f32_16x16x32_bf16 v[152:155], v[6:9], v[86:89], v[122:125]
	v_mfma_f32_16x16x32_bf16 v[122:125], v[10:13], v[62:65], 0
	v_mfma_f32_16x16x32_bf16 v[156:159], v[14:17], v[86:89], v[122:125]
	v_mfma_f32_16x16x32_bf16 v[122:125], v[2:5], v[98:101], 0
	v_mfma_f32_16x16x32_bf16 v[2:5], v[2:5], v[114:117], 0
	v_mfma_f32_16x16x32_bf16 v[160:163], v[6:9], v[102:105], v[122:125]
	v_mfma_f32_16x16x32_bf16 v[2:5], v[6:9], v[118:121], v[2:5]
	v_mfma_f32_16x16x32_bf16 v[6:9], v[10:13], v[114:117], 0
	v_mfma_f32_16x16x32_bf16 v[122:125], v[10:13], v[98:101], 0
	v_mfma_f32_16x16x32_bf16 v[10:13], v[14:17], v[118:121], v[6:9]
	v_mfma_f32_16x16x32_bf16 v[164:167], v[14:17], v[102:105], v[122:125]
	v_mfma_f32_16x16x32_bf16 v[6:9], v[18:21], v[50:53], 0
	v_mfma_f32_16x16x32_bf16 v[14:17], v[22:25], v[54:57], v[6:9]
	v_mfma_f32_16x16x32_bf16 v[6:9], v[26:29], v[50:53], 0
	v_mfma_f32_16x16x32_bf16 v[168:171], v[30:33], v[54:57], v[6:9]
	v_mfma_f32_16x16x32_bf16 v[6:9], v[18:21], v[62:65], 0
	v_mfma_f32_16x16x32_bf16 v[172:175], v[22:25], v[86:89], v[6:9]
	v_mfma_f32_16x16x32_bf16 v[6:9], v[26:29], v[62:65], 0
	v_mfma_f32_16x16x32_bf16 v[176:179], v[30:33], v[86:89], v[6:9]
	v_mfma_f32_16x16x32_bf16 v[6:9], v[18:21], v[98:101], 0
	v_mfma_f32_16x16x32_bf16 v[180:183], v[22:25], v[102:105], v[6:9]
	v_mfma_f32_16x16x32_bf16 v[6:9], v[26:29], v[98:101], 0
	v_mfma_f32_16x16x32_bf16 v[184:187], v[30:33], v[102:105], v[6:9]
	v_mfma_f32_16x16x32_bf16 v[6:9], v[18:21], v[114:117], 0
	v_mfma_f32_16x16x32_bf16 v[188:191], v[22:25], v[118:121], v[6:9]
	v_mfma_f32_16x16x32_bf16 v[6:9], v[26:29], v[114:117], 0
	v_mfma_f32_16x16x32_bf16 v[194:197], v[30:33], v[118:121], v[6:9]
	s_barrier
	s_add_i32 s78, 0, 0x18000
	s_add_i32 s80, 0, 0x1c000
	v_add_u32_e32 v134, s78, v218
	v_add_u32_e32 v135, s80, v218
	s_nop 0
	ds_read_b128 v[6:9], v134
	ds_read_b128 v[26:29], v134 offset:1024
	ds_read_b128 v[30:33], v134 offset:2048
	ds_read_b128 v[198:201], v134 offset:3072
	ds_read_b128 v[202:205], v135
	ds_read_b128 v[206:209], v135 offset:1024
	ds_read_b128 v[210:213], v135 offset:2048
	ds_read_b128 v[220:223], v135 offset:3072
	s_add_u32 s56, s56, 0x4000
	s_addc_u32 s57, s57, 0
	s_mov_b32 m0, s25
	ds_read_b128 v[18:21], v219 offset:32768
	ds_read_b128 v[22:25], v219 offset:33792
	ds_read_b128 v[62:65], v219 offset:34816
	ds_read_b128 v[224:227], v219 offset:35840
	ds_read_b128 v[232:235], v219 offset:36864
	ds_read_b128 v[236:239], v219 offset:37888
	ds_read_b128 v[240:243], v219 offset:38912
	ds_read_b128 v[244:247], v219 offset:39936
	s_nop 0
	global_load_lds_dwordx4 v217, s[56:57]
	s_mov_b32 m0, s60
	s_nop 0
	global_load_lds_dwordx4 v216, s[56:57]
	s_waitcnt vmcnt(8)
	s_waitcnt lgkmcnt(0)
	s_barrier
	s_waitcnt lgkmcnt(0)
	v_mfma_f32_16x16x32_bf16 v[50:53], v[6:9], v[18:21], v[66:69]
	v_mfma_f32_16x16x32_bf16 v[126:129], v[26:29], v[22:25], v[50:53]
	v_mfma_f32_16x16x32_bf16 v[50:53], v[30:33], v[18:21], v[70:73]
	v_mfma_f32_16x16x32_bf16 v[122:125], v[198:201], v[22:25], v[50:53]
	v_mfma_f32_16x16x32_bf16 v[50:53], v[6:9], v[62:65], v[74:77]
	v_mfma_f32_16x16x32_bf16 v[102:105], v[26:29], v[224:227], v[50:53]
	v_mfma_f32_16x16x32_bf16 v[50:53], v[30:33], v[62:65], v[78:81]
	v_mfma_f32_16x16x32_bf16 v[98:101], v[198:201], v[224:227], v[50:53]
	v_mfma_f32_16x16x32_bf16 v[50:53], v[6:9], v[232:235], v[82:85]
	v_mfma_f32_16x16x32_bf16 v[86:89], v[26:29], v[236:239], v[50:53]
	v_mfma_f32_16x16x32_bf16 v[50:53], v[30:33], v[232:235], v[90:93]
	v_mfma_f32_16x16x32_bf16 v[82:85], v[198:201], v[236:239], v[50:53]
	v_mfma_f32_16x16x32_bf16 v[50:53], v[6:9], v[240:243], v[94:97]
	v_mfma_f32_16x16x32_bf16 v[54:57], v[26:29], v[244:247], v[50:53]
	v_mfma_f32_16x16x32_bf16 v[50:53], v[30:33], v[240:243], v[106:109]
	v_mfma_f32_16x16x32_bf16 v[50:53], v[198:201], v[244:247], v[50:53]
	v_mfma_f32_16x16x32_bf16 v[66:69], v[202:205], v[18:21], v[110:113]
	v_mfma_f32_16x16x32_bf16 v[18:21], v[210:213], v[18:21], v[34:37]
	v_mfma_f32_16x16x32_bf16 v[114:117], v[220:223], v[22:25], v[18:21]
	v_mfma_f32_16x16x32_bf16 v[18:21], v[202:205], v[62:65], v[38:41]
	v_mfma_f32_16x16x32_bf16 v[110:113], v[206:209], v[224:227], v[18:21]
	v_mfma_f32_16x16x32_bf16 v[18:21], v[210:213], v[62:65], v[42:45]
	v_mfma_f32_16x16x32_bf16 v[106:109], v[220:223], v[224:227], v[18:21]
	v_mfma_f32_16x16x32_bf16 v[18:21], v[202:205], v[232:235], v[46:49]
	v_mfma_f32_16x16x32_bf16 v[94:97], v[206:209], v[236:239], v[18:21]
	v_mfma_f32_16x16x32_bf16 v[18:21], v[210:213], v[232:235], v[136:139]
	v_mfma_f32_16x16x32_bf16 v[90:93], v[220:223], v[236:239], v[18:21]
	v_mfma_f32_16x16x32_bf16 v[18:21], v[202:205], v[240:243], v[140:143]
	v_mfma_f32_16x16x32_bf16 v[62:65], v[206:209], v[244:247], v[18:21]
	v_mfma_f32_16x16x32_bf16 v[18:21], v[210:213], v[240:243], v[58:61]
	v_mfma_f32_16x16x32_bf16 v[118:121], v[206:209], v[22:25], v[66:69]
	v_mfma_f32_16x16x32_bf16 v[58:61], v[220:223], v[244:247], v[18:21]
	s_barrier
	ds_read_b128 v[42:45], v219 offset:49152
	ds_read_b128 v[46:49], v219 offset:50176
	ds_read_b128 v[136:139], v219 offset:51200
	ds_read_b128 v[140:143], v219 offset:52224
	ds_read_b128 v[224:227], v219 offset:53248
	ds_read_b128 v[232:235], v219 offset:54272
	ds_read_b128 v[236:239], v219 offset:55296
	ds_read_b128 v[240:243], v219 offset:56320
	s_add_i32 s78, s78, s15
	v_lshl_add_u64 v[18:19], s[34:35], 0, v[0:1]
	v_lshl_add_u64 v[18:19], v[18:19], 0, s[16:17]
	s_mov_b32 m0, s78
	v_mov_b32_e32 v131, v1
	global_load_lds_dwordx4 v[18:19], off
	s_add_i32 s79, s78, 0x2000
	v_lshl_add_u64 v[18:19], s[34:35], 0, v[130:131]
	v_lshl_add_u64 v[18:19], v[18:19], 0, s[16:17]
	s_mov_b32 m0, s79
	s_add_i32 s80, s80, s15
	global_load_lds_dwordx4 v[18:19], off
	s_mov_b32 m0, s80
	v_lshl_add_u64 v[18:19], s[58:59], 0, v[0:1]
	v_lshl_add_u64 v[18:19], v[18:19], 0, s[16:17]
	global_load_lds_dwordx4 v[18:19], off
	s_nop 0
	v_lshl_add_u64 v[18:19], s[58:59], 0, v[130:131]
	s_add_i32 s58, s80, 0x2000
	v_lshl_add_u64 v[18:19], v[18:19], 0, s[16:17]
	s_mov_b32 m0, s58
	s_nop 0
	global_load_lds_dwordx4 v[18:19], off
	s_mov_b32 m0, s65
	s_nop 0
	global_load_lds_dwordx4 v217, s[30:31]
	s_mov_b32 m0, s66
	s_nop 0
	global_load_lds_dwordx4 v216, s[30:31]
	s_waitcnt vmcnt(8)
	s_waitcnt lgkmcnt(0)
	s_barrier
	s_waitcnt lgkmcnt(0)
	v_mfma_f32_16x16x32_bf16 v[18:21], v[6:9], v[42:45], v[144:147]
	v_mfma_f32_16x16x32_bf16 v[70:73], v[26:29], v[46:49], v[18:21]
	v_mfma_f32_16x16x32_bf16 v[18:21], v[30:33], v[42:45], v[148:151]
	v_mfma_f32_16x16x32_bf16 v[66:69], v[198:201], v[46:49], v[18:21]
	v_mfma_f32_16x16x32_bf16 v[18:21], v[6:9], v[136:139], v[152:155]
	v_mfma_f32_16x16x32_bf16 v[38:41], v[26:29], v[140:143], v[18:21]
	v_mfma_f32_16x16x32_bf16 v[18:21], v[30:33], v[136:139], v[156:159]
	v_mfma_f32_16x16x32_bf16 v[34:37], v[198:201], v[140:143], v[18:21]
	v_mfma_f32_16x16x32_bf16 v[18:21], v[6:9], v[224:227], v[160:163]
	v_mfma_f32_16x16x32_bf16 v[2:5], v[6:9], v[236:239], v[2:5]
	v_mfma_f32_16x16x32_bf16 v[22:25], v[26:29], v[232:235], v[18:21]
	v_mfma_f32_16x16x32_bf16 v[18:21], v[30:33], v[224:227], v[164:167]
	v_mfma_f32_16x16x32_bf16 v[6:9], v[26:29], v[240:243], v[2:5]
	v_mfma_f32_16x16x32_bf16 v[2:5], v[30:33], v[236:239], v[10:13]
	v_mfma_f32_16x16x32_bf16 v[18:21], v[198:201], v[232:235], v[18:21]
	v_mfma_f32_16x16x32_bf16 v[2:5], v[198:201], v[240:243], v[2:5]
	v_mfma_f32_16x16x32_bf16 v[10:13], v[202:205], v[42:45], v[14:17]
	v_mfma_f32_16x16x32_bf16 v[78:81], v[206:209], v[46:49], v[10:13]
	v_mfma_f32_16x16x32_bf16 v[10:13], v[210:213], v[42:45], v[168:171]
	v_mfma_f32_16x16x32_bf16 v[74:77], v[220:223], v[46:49], v[10:13]
	v_mfma_f32_16x16x32_bf16 v[10:13], v[202:205], v[136:139], v[172:175]
	v_mfma_f32_16x16x32_bf16 v[46:49], v[206:209], v[140:143], v[10:13]
	v_mfma_f32_16x16x32_bf16 v[10:13], v[210:213], v[136:139], v[176:179]
	v_mfma_f32_16x16x32_bf16 v[42:45], v[220:223], v[140:143], v[10:13]
	v_mfma_f32_16x16x32_bf16 v[10:13], v[202:205], v[224:227], v[180:183]
	v_mfma_f32_16x16x32_bf16 v[30:33], v[206:209], v[232:235], v[10:13]
	v_mfma_f32_16x16x32_bf16 v[10:13], v[210:213], v[224:227], v[184:187]
	v_mfma_f32_16x16x32_bf16 v[26:29], v[220:223], v[232:235], v[10:13]
	v_mfma_f32_16x16x32_bf16 v[10:13], v[202:205], v[236:239], v[188:191]
	v_mfma_f32_16x16x32_bf16 v[14:17], v[206:209], v[240:243], v[10:13]
	v_mfma_f32_16x16x32_bf16 v[10:13], v[210:213], v[236:239], v[194:197]
	v_mfma_f32_16x16x32_bf16 v[10:13], v[220:223], v[240:243], v[10:13]
	s_barrier
	s_andn2_b64 vcc, exec, s[50:51]
	s_cbranch_vccnz .LBB0_968
	s_add_u32 s59, s26, 0x200
	s_addc_u32 s81, s27, 0
	s_add_u32 s26, s28, 0x1c000
	s_addc_u32 s27, s29, 0
	s_mov_b32 s82, 4
.LBB0_967:
	ds_read_b128 v[136:139], v132
	ds_read_b128 v[140:143], v132 offset:1024
	ds_read_b128 v[144:147], v132 offset:2048
	ds_read_b128 v[148:151], v132 offset:3072
	ds_read_b128 v[152:155], v133
	ds_read_b128 v[156:159], v133 offset:1024
	ds_read_b128 v[160:163], v133 offset:2048
	ds_read_b128 v[164:167], v133 offset:3072
	s_add_u32 s28, s26, 0x4000
	s_addc_u32 s29, s27, 0
	s_cmp_eq_u32 s63, s82
	s_cselect_b32 s34, s42, s28
	s_cselect_b32 s35, s43, s29
	s_cselect_b32 s30, s54, s59
	s_cselect_b32 s31, s55, s81
	s_add_u32 s28, s34, 0x8000
	s_addc_u32 s29, s35, 0
	s_mov_b32 m0, s72
	ds_read_b128 v[168:171], v219
	ds_read_b128 v[172:175], v219 offset:1024
	ds_read_b128 v[176:179], v219 offset:2048
	ds_read_b128 v[180:183], v219 offset:3072
	ds_read_b128 v[184:187], v219 offset:4096
	ds_read_b128 v[188:191], v219 offset:5120
	ds_read_b128 v[194:197], v219 offset:6144
	ds_read_b128 v[198:201], v219 offset:7168
	s_nop 0
	global_load_lds_dwordx4 v217, s[26:27]
	s_mov_b32 m0, s73
	s_nop 0
	global_load_lds_dwordx4 v216, s[26:27]
	s_waitcnt vmcnt(8)
	s_waitcnt lgkmcnt(0)
	s_barrier
	s_waitcnt lgkmcnt(0)
	v_mfma_f32_16x16x32_bf16 v[126:129], v[136:139], v[168:171], v[126:129]
	v_mfma_f32_16x16x32_bf16 v[122:125], v[144:147], v[168:171], v[122:125]
	v_mfma_f32_16x16x32_bf16 v[102:105], v[136:139], v[176:179], v[102:105]
	v_mfma_f32_16x16x32_bf16 v[98:101], v[144:147], v[176:179], v[98:101]
	v_mfma_f32_16x16x32_bf16 v[86:89], v[136:139], v[184:187], v[86:89]
	v_mfma_f32_16x16x32_bf16 v[82:85], v[144:147], v[184:187], v[82:85]
	v_mfma_f32_16x16x32_bf16 v[54:57], v[136:139], v[194:197], v[54:57]
	v_mfma_f32_16x16x32_bf16 v[50:53], v[144:147], v[194:197], v[50:53]
	v_mfma_f32_16x16x32_bf16 v[126:129], v[140:143], v[172:175], v[126:129]
	v_mfma_f32_16x16x32_bf16 v[122:125], v[148:151], v[172:175], v[122:125]
	v_mfma_f32_16x16x32_bf16 v[102:105], v[140:143], v[180:183], v[102:105]
	v_mfma_f32_16x16x32_bf16 v[98:101], v[148:151], v[180:183], v[98:101]
	v_mfma_f32_16x16x32_bf16 v[86:89], v[140:143], v[188:191], v[86:89]
	v_mfma_f32_16x16x32_bf16 v[82:85], v[148:151], v[188:191], v[82:85]
	v_mfma_f32_16x16x32_bf16 v[54:57], v[140:143], v[198:201], v[54:57]
	v_mfma_f32_16x16x32_bf16 v[50:53], v[148:151], v[198:201], v[50:53]
	v_mfma_f32_16x16x32_bf16 v[118:121], v[152:155], v[168:171], v[118:121]
	v_mfma_f32_16x16x32_bf16 v[114:117], v[160:163], v[168:171], v[114:117]
	v_mfma_f32_16x16x32_bf16 v[110:113], v[152:155], v[176:179], v[110:113]
	v_mfma_f32_16x16x32_bf16 v[106:109], v[160:163], v[176:179], v[106:109]
	v_mfma_f32_16x16x32_bf16 v[94:97], v[152:155], v[184:187], v[94:97]
	v_mfma_f32_16x16x32_bf16 v[90:93], v[160:163], v[184:187], v[90:93]
	v_mfma_f32_16x16x32_bf16 v[62:65], v[152:155], v[194:197], v[62:65]
	v_mfma_f32_16x16x32_bf16 v[58:61], v[160:163], v[194:197], v[58:61]
	v_mfma_f32_16x16x32_bf16 v[118:121], v[156:159], v[172:175], v[118:121]
	v_mfma_f32_16x16x32_bf16 v[114:117], v[164:167], v[172:175], v[114:117]
	v_mfma_f32_16x16x32_bf16 v[110:113], v[156:159], v[180:183], v[110:113]
	v_mfma_f32_16x16x32_bf16 v[106:109], v[164:167], v[180:183], v[106:109]
	v_mfma_f32_16x16x32_bf16 v[94:97], v[156:159], v[188:191], v[94:97]
	v_mfma_f32_16x16x32_bf16 v[90:93], v[164:167], v[188:191], v[90:93]
	v_mfma_f32_16x16x32_bf16 v[62:65], v[156:159], v[198:201], v[62:65]
	v_mfma_f32_16x16x32_bf16 v[58:61], v[164:167], v[198:201], v[58:61]
	s_barrier
	s_mov_b32 m0, s74
	ds_read_b128 v[168:171], v219 offset:16384
	ds_read_b128 v[172:175], v219 offset:17408
	ds_read_b128 v[176:179], v219 offset:18432
	ds_read_b128 v[180:183], v219 offset:19456
	ds_read_b128 v[184:187], v219 offset:20480
	ds_read_b128 v[188:191], v219 offset:21504
	ds_read_b128 v[194:197], v219 offset:22528
	ds_read_b128 v[198:201], v219 offset:23552
	s_add_u32 s56, s30, s36
	global_load_lds_dwordx4 v0, s[30:31]
	s_mov_b32 m0, s75
	s_addc_u32 s57, s31, s37
	global_load_lds_dwordx4 v130, s[30:31]
	s_mov_b32 m0, s76
	s_nop 0
	global_load_lds_dwordx4 v0, s[56:57]
	s_mov_b32 m0, s77
	s_nop 0
	global_load_lds_dwordx4 v130, s[56:57]
	s_mov_b32 m0, s18
	s_nop 0
	global_load_lds_dwordx4 v217, s[34:35]
	s_mov_b32 m0, s20
	s_nop 0
	global_load_lds_dwordx4 v216, s[34:35]
	s_waitcnt vmcnt(8)
	s_waitcnt lgkmcnt(0)
	s_barrier
	s_waitcnt lgkmcnt(0)
	v_mfma_f32_16x16x32_bf16 v[70:73], v[136:139], v[168:171], v[70:73]
	v_mfma_f32_16x16x32_bf16 v[66:69], v[144:147], v[168:171], v[66:69]
	v_mfma_f32_16x16x32_bf16 v[38:41], v[136:139], v[176:179], v[38:41]
	v_mfma_f32_16x16x32_bf16 v[34:37], v[144:147], v[176:179], v[34:37]
	v_mfma_f32_16x16x32_bf16 v[22:25], v[136:139], v[184:187], v[22:25]
	v_mfma_f32_16x16x32_bf16 v[18:21], v[144:147], v[184:187], v[18:21]
	v_mfma_f32_16x16x32_bf16 v[6:9], v[136:139], v[194:197], v[6:9]
	v_mfma_f32_16x16x32_bf16 v[2:5], v[144:147], v[194:197], v[2:5]
	v_mfma_f32_16x16x32_bf16 v[70:73], v[140:143], v[172:175], v[70:73]
	v_mfma_f32_16x16x32_bf16 v[66:69], v[148:151], v[172:175], v[66:69]
	v_mfma_f32_16x16x32_bf16 v[38:41], v[140:143], v[180:183], v[38:41]
	v_mfma_f32_16x16x32_bf16 v[34:37], v[148:151], v[180:183], v[34:37]
	v_mfma_f32_16x16x32_bf16 v[22:25], v[140:143], v[188:191], v[22:25]
	v_mfma_f32_16x16x32_bf16 v[18:21], v[148:151], v[188:191], v[18:21]
	v_mfma_f32_16x16x32_bf16 v[6:9], v[140:143], v[198:201], v[6:9]
	v_mfma_f32_16x16x32_bf16 v[2:5], v[148:151], v[198:201], v[2:5]
	v_mfma_f32_16x16x32_bf16 v[78:81], v[152:155], v[168:171], v[78:81]
	v_mfma_f32_16x16x32_bf16 v[74:77], v[160:163], v[168:171], v[74:77]
	v_mfma_f32_16x16x32_bf16 v[46:49], v[152:155], v[176:179], v[46:49]
	v_mfma_f32_16x16x32_bf16 v[42:45], v[160:163], v[176:179], v[42:45]
	v_mfma_f32_16x16x32_bf16 v[30:33], v[152:155], v[184:187], v[30:33]
	v_mfma_f32_16x16x32_bf16 v[26:29], v[160:163], v[184:187], v[26:29]
	v_mfma_f32_16x16x32_bf16 v[14:17], v[152:155], v[194:197], v[14:17]
	v_mfma_f32_16x16x32_bf16 v[10:13], v[160:163], v[194:197], v[10:13]
	v_mfma_f32_16x16x32_bf16 v[78:81], v[156:159], v[172:175], v[78:81]
	v_mfma_f32_16x16x32_bf16 v[74:77], v[164:167], v[172:175], v[74:77]
	v_mfma_f32_16x16x32_bf16 v[46:49], v[156:159], v[180:183], v[46:49]
	v_mfma_f32_16x16x32_bf16 v[42:45], v[164:167], v[180:183], v[42:45]
	v_mfma_f32_16x16x32_bf16 v[30:33], v[156:159], v[188:191], v[30:33]
	v_mfma_f32_16x16x32_bf16 v[26:29], v[164:167], v[188:191], v[26:29]
	v_mfma_f32_16x16x32_bf16 v[14:17], v[156:159], v[198:201], v[14:17]
	v_mfma_f32_16x16x32_bf16 v[10:13], v[164:167], v[198:201], v[10:13]
	s_barrier
	ds_read_b128 v[136:139], v134
	ds_read_b128 v[140:143], v134 offset:1024
	ds_read_b128 v[144:147], v134 offset:2048
	ds_read_b128 v[148:151], v134 offset:3072
	ds_read_b128 v[152:155], v135
	ds_read_b128 v[156:159], v135 offset:1024
	ds_read_b128 v[160:163], v135 offset:2048
	ds_read_b128 v[164:167], v135 offset:3072
	s_add_u32 s34, s34, 0x4000
	s_addc_u32 s35, s35, 0
	s_mov_b32 m0, s25
	ds_read_b128 v[168:171], v219 offset:32768
	ds_read_b128 v[172:175], v219 offset:33792
	ds_read_b128 v[176:179], v219 offset:34816
	ds_read_b128 v[180:183], v219 offset:35840
	ds_read_b128 v[184:187], v219 offset:36864
	ds_read_b128 v[188:191], v219 offset:37888
	ds_read_b128 v[194:197], v219 offset:38912
	ds_read_b128 v[198:201], v219 offset:39936
	s_nop 0
	global_load_lds_dwordx4 v217, s[34:35]
	s_mov_b32 m0, s60
	s_nop 0
	global_load_lds_dwordx4 v216, s[34:35]
	s_waitcnt vmcnt(8)
	s_waitcnt lgkmcnt(0)
	s_barrier
	s_waitcnt lgkmcnt(0)
	v_mfma_f32_16x16x32_bf16 v[126:129], v[136:139], v[168:171], v[126:129]
	v_mfma_f32_16x16x32_bf16 v[122:125], v[144:147], v[168:171], v[122:125]
	v_mfma_f32_16x16x32_bf16 v[102:105], v[136:139], v[176:179], v[102:105]
	v_mfma_f32_16x16x32_bf16 v[98:101], v[144:147], v[176:179], v[98:101]
	v_mfma_f32_16x16x32_bf16 v[86:89], v[136:139], v[184:187], v[86:89]
	v_mfma_f32_16x16x32_bf16 v[82:85], v[144:147], v[184:187], v[82:85]
	v_mfma_f32_16x16x32_bf16 v[54:57], v[136:139], v[194:197], v[54:57]
	v_mfma_f32_16x16x32_bf16 v[50:53], v[144:147], v[194:197], v[50:53]
	v_mfma_f32_16x16x32_bf16 v[126:129], v[140:143], v[172:175], v[126:129]
	v_mfma_f32_16x16x32_bf16 v[122:125], v[148:151], v[172:175], v[122:125]
	v_mfma_f32_16x16x32_bf16 v[102:105], v[140:143], v[180:183], v[102:105]
	v_mfma_f32_16x16x32_bf16 v[98:101], v[148:151], v[180:183], v[98:101]
	v_mfma_f32_16x16x32_bf16 v[86:89], v[140:143], v[188:191], v[86:89]
	v_mfma_f32_16x16x32_bf16 v[82:85], v[148:151], v[188:191], v[82:85]
	v_mfma_f32_16x16x32_bf16 v[54:57], v[140:143], v[198:201], v[54:57]
	v_mfma_f32_16x16x32_bf16 v[50:53], v[148:151], v[198:201], v[50:53]
	v_mfma_f32_16x16x32_bf16 v[118:121], v[152:155], v[168:171], v[118:121]
	v_mfma_f32_16x16x32_bf16 v[114:117], v[160:163], v[168:171], v[114:117]
	v_mfma_f32_16x16x32_bf16 v[110:113], v[152:155], v[176:179], v[110:113]
	v_mfma_f32_16x16x32_bf16 v[106:109], v[160:163], v[176:179], v[106:109]
	v_mfma_f32_16x16x32_bf16 v[94:97], v[152:155], v[184:187], v[94:97]
	v_mfma_f32_16x16x32_bf16 v[90:93], v[160:163], v[184:187], v[90:93]
	v_mfma_f32_16x16x32_bf16 v[62:65], v[152:155], v[194:197], v[62:65]
	v_mfma_f32_16x16x32_bf16 v[58:61], v[160:163], v[194:197], v[58:61]
	v_mfma_f32_16x16x32_bf16 v[118:121], v[156:159], v[172:175], v[118:121]
	v_mfma_f32_16x16x32_bf16 v[114:117], v[164:167], v[172:175], v[114:117]
	v_mfma_f32_16x16x32_bf16 v[110:113], v[156:159], v[180:183], v[110:113]
	v_mfma_f32_16x16x32_bf16 v[106:109], v[164:167], v[180:183], v[106:109]
	v_mfma_f32_16x16x32_bf16 v[94:97], v[156:159], v[188:191], v[94:97]
	v_mfma_f32_16x16x32_bf16 v[90:93], v[164:167], v[188:191], v[90:93]
	v_mfma_f32_16x16x32_bf16 v[62:65], v[156:159], v[198:201], v[62:65]
	v_mfma_f32_16x16x32_bf16 v[58:61], v[164:167], v[198:201], v[58:61]
	s_barrier
	ds_read_b128 v[168:171], v219 offset:49152
	ds_read_b128 v[172:175], v219 offset:50176
	ds_read_b128 v[176:179], v219 offset:51200
	ds_read_b128 v[180:183], v219 offset:52224
	ds_read_b128 v[184:187], v219 offset:53248
	ds_read_b128 v[188:191], v219 offset:54272
	ds_read_b128 v[194:197], v219 offset:55296
	ds_read_b128 v[198:201], v219 offset:56320
	s_mov_b32 m0, s78
	v_lshl_add_u64 v[202:203], s[30:31], 0, v[0:1]
	v_lshl_add_u64 v[202:203], v[202:203], 0, s[16:17]
	v_mov_b32_e32 v131, v1
	global_load_lds_dwordx4 v[202:203], off
	s_mov_b32 m0, s79
	v_lshl_add_u64 v[202:203], s[30:31], 0, v[130:131]
	v_lshl_add_u64 v[202:203], v[202:203], 0, s[16:17]
	global_load_lds_dwordx4 v[202:203], off
	s_mov_b32 m0, s80
	v_lshl_add_u64 v[202:203], s[56:57], 0, v[0:1]
	v_lshl_add_u64 v[202:203], v[202:203], 0, s[16:17]
	global_load_lds_dwordx4 v[202:203], off
	s_mov_b32 m0, s58
	v_lshl_add_u64 v[202:203], s[56:57], 0, v[130:131]
	v_lshl_add_u64 v[202:203], v[202:203], 0, s[16:17]
	global_load_lds_dwordx4 v[202:203], off
	s_mov_b32 m0, s65
	s_nop 0
	global_load_lds_dwordx4 v217, s[28:29]
	s_mov_b32 m0, s66
	s_nop 0
	global_load_lds_dwordx4 v216, s[28:29]
	s_waitcnt vmcnt(8)
	s_waitcnt lgkmcnt(0)
	s_barrier
	s_waitcnt lgkmcnt(0)
	v_mfma_f32_16x16x32_bf16 v[70:73], v[136:139], v[168:171], v[70:73]
	v_mfma_f32_16x16x32_bf16 v[66:69], v[144:147], v[168:171], v[66:69]
	v_mfma_f32_16x16x32_bf16 v[38:41], v[136:139], v[176:179], v[38:41]
	v_mfma_f32_16x16x32_bf16 v[34:37], v[144:147], v[176:179], v[34:37]
	v_mfma_f32_16x16x32_bf16 v[22:25], v[136:139], v[184:187], v[22:25]
	v_mfma_f32_16x16x32_bf16 v[18:21], v[144:147], v[184:187], v[18:21]
	v_mfma_f32_16x16x32_bf16 v[6:9], v[136:139], v[194:197], v[6:9]
	v_mfma_f32_16x16x32_bf16 v[2:5], v[144:147], v[194:197], v[2:5]
	v_mfma_f32_16x16x32_bf16 v[70:73], v[140:143], v[172:175], v[70:73]
	v_mfma_f32_16x16x32_bf16 v[66:69], v[148:151], v[172:175], v[66:69]
	v_mfma_f32_16x16x32_bf16 v[38:41], v[140:143], v[180:183], v[38:41]
	v_mfma_f32_16x16x32_bf16 v[34:37], v[148:151], v[180:183], v[34:37]
	v_mfma_f32_16x16x32_bf16 v[22:25], v[140:143], v[188:191], v[22:25]
	v_mfma_f32_16x16x32_bf16 v[18:21], v[148:151], v[188:191], v[18:21]
	v_mfma_f32_16x16x32_bf16 v[6:9], v[140:143], v[198:201], v[6:9]
	v_mfma_f32_16x16x32_bf16 v[2:5], v[148:151], v[198:201], v[2:5]
	v_mfma_f32_16x16x32_bf16 v[78:81], v[152:155], v[168:171], v[78:81]
	v_mfma_f32_16x16x32_bf16 v[74:77], v[160:163], v[168:171], v[74:77]
	v_mfma_f32_16x16x32_bf16 v[46:49], v[152:155], v[176:179], v[46:49]
	v_mfma_f32_16x16x32_bf16 v[42:45], v[160:163], v[176:179], v[42:45]
	v_mfma_f32_16x16x32_bf16 v[30:33], v[152:155], v[184:187], v[30:33]
	v_mfma_f32_16x16x32_bf16 v[26:29], v[160:163], v[184:187], v[26:29]
	v_mfma_f32_16x16x32_bf16 v[14:17], v[152:155], v[194:197], v[14:17]
	v_mfma_f32_16x16x32_bf16 v[10:13], v[160:163], v[194:197], v[10:13]
	v_mfma_f32_16x16x32_bf16 v[78:81], v[156:159], v[172:175], v[78:81]
	v_mfma_f32_16x16x32_bf16 v[74:77], v[164:167], v[172:175], v[74:77]
	v_mfma_f32_16x16x32_bf16 v[46:49], v[156:159], v[180:183], v[46:49]
	v_mfma_f32_16x16x32_bf16 v[42:45], v[164:167], v[180:183], v[42:45]
	v_mfma_f32_16x16x32_bf16 v[30:33], v[156:159], v[188:191], v[30:33]
	v_mfma_f32_16x16x32_bf16 v[26:29], v[164:167], v[188:191], v[26:29]
	v_mfma_f32_16x16x32_bf16 v[14:17], v[156:159], v[198:201], v[14:17]
	v_mfma_f32_16x16x32_bf16 v[10:13], v[164:167], v[198:201], v[10:13]
	s_barrier
	s_add_i32 s28, s82, 2
	s_add_u32 s59, s59, 0x100
	s_addc_u32 s81, s81, 0
	s_add_u32 s26, s26, 0x10000
	s_addc_u32 s27, s27, 0
	s_cmp_lt_i32 s82, s63
	s_mov_b32 s82, s28
	s_cbranch_scc1 .LBB0_967

.LBB0_1072:
	s_add_u32 s21, s26, 0x10000
	s_addc_u32 s34, s27, 0
	s_and_b64 s[30:31], s[48:49], exec
	s_cselect_b32 s55, s43, s34
	s_cselect_b32 s54, s42, s21
	s_add_u32 s21, s28, 0x100
	s_addc_u32 s56, s29, 0
	s_add_u32 s30, s54, 0x8000
	s_addc_u32 s31, s55, 0
	s_add_i32 s71, 0, 0x10000
	s_and_b64 s[34:35], s[48:49], exec
	s_cselect_b32 s35, s45, s56
	s_cselect_b32 s34, s44, s21
	s_add_i32 s73, 0, 0x14000
	v_add_u32_e32 v114, s71, v237
	v_add_u32_e32 v115, s73, v237
	ds_read_b128 v[2:5], v114
	s_waitcnt lgkmcnt(0)
	ds_read_b128 v[6:9], v114 offset:1024
	ds_read_b128 v[10:13], v114 offset:2048
	ds_read_b128 v[14:17], v114 offset:3072
	ds_read_b128 v[18:21], v115
	ds_read_b128 v[22:25], v115 offset:1024
	ds_read_b128 v[26:29], v115 offset:2048
	ds_read_b128 v[30:33], v115 offset:3072
	s_add_u32 s56, s26, 0xc000
	s_addc_u32 s57, s27, 0
	s_add_i32 s21, s20, 0xc000
	s_mov_b32 m0, s21
	s_add_i32 s70, s20, 0xe000
	ds_read_b128 v[34:37], v238
	ds_read_b128 v[38:41], v238 offset:1024
	ds_read_b128 v[42:45], v238 offset:2048
	ds_read_b128 v[46:49], v238 offset:3072
	ds_read_b128 v[50:53], v238 offset:4096
	ds_read_b128 v[54:57], v238 offset:5120
	ds_read_b128 v[58:61], v238 offset:6144
	ds_read_b128 v[62:65], v238 offset:7168
	s_nop 0
	global_load_lds_dwordx4 v236, s[56:57]
	s_mov_b32 m0, s70
	s_nop 0
	global_load_lds_dwordx4 v235, s[56:57]
	s_waitcnt vmcnt(8)
	s_waitcnt lgkmcnt(0)
	s_barrier
	s_waitcnt lgkmcnt(0)
	v_mfma_f32_16x16x32_bf16 v[90:93], v[2:5], v[58:61], 0
	v_mfma_f32_16x16x32_bf16 v[66:69], v[2:5], v[34:37], 0
	v_mfma_f32_16x16x32_bf16 v[70:73], v[10:13], v[34:37], 0
	v_mfma_f32_16x16x32_bf16 v[74:77], v[2:5], v[42:45], 0
	v_mfma_f32_16x16x32_bf16 v[78:81], v[10:13], v[42:45], 0
	v_mfma_f32_16x16x32_bf16 v[82:85], v[2:5], v[50:53], 0
	v_mfma_f32_16x16x32_bf16 v[86:89], v[10:13], v[50:53], 0
	v_mfma_f32_16x16x32_bf16 v[98:101], v[6:9], v[62:65], v[90:93]
	v_mfma_f32_16x16x32_bf16 v[90:93], v[10:13], v[58:61], 0
	v_mfma_f32_16x16x32_bf16 v[66:69], v[6:9], v[38:41], v[66:69]
	v_mfma_f32_16x16x32_bf16 v[70:73], v[14:17], v[38:41], v[70:73]
	v_mfma_f32_16x16x32_bf16 v[74:77], v[6:9], v[46:49], v[74:77]
	v_mfma_f32_16x16x32_bf16 v[78:81], v[14:17], v[46:49], v[78:81]
	v_mfma_f32_16x16x32_bf16 v[82:85], v[6:9], v[54:57], v[82:85]
	v_mfma_f32_16x16x32_bf16 v[86:89], v[14:17], v[54:57], v[86:89]
	v_mfma_f32_16x16x32_bf16 v[102:105], v[14:17], v[62:65], v[90:93]
	v_mfma_f32_16x16x32_bf16 v[90:93], v[18:21], v[34:37], 0
	v_mfma_f32_16x16x32_bf16 v[34:37], v[26:29], v[34:37], 0
	v_mfma_f32_16x16x32_bf16 v[118:121], v[22:25], v[38:41], v[90:93]
	v_mfma_f32_16x16x32_bf16 v[34:37], v[30:33], v[38:41], v[34:37]
	v_mfma_f32_16x16x32_bf16 v[38:41], v[18:21], v[42:45], 0
	v_mfma_f32_16x16x32_bf16 v[42:45], v[26:29], v[42:45], 0
	v_mfma_f32_16x16x32_bf16 v[38:41], v[22:25], v[46:49], v[38:41]
	v_mfma_f32_16x16x32_bf16 v[42:45], v[30:33], v[46:49], v[42:45]
	v_mfma_f32_16x16x32_bf16 v[46:49], v[18:21], v[50:53], 0
	v_mfma_f32_16x16x32_bf16 v[50:53], v[26:29], v[50:53], 0
	v_mfma_f32_16x16x32_bf16 v[46:49], v[22:25], v[54:57], v[46:49]
	v_mfma_f32_16x16x32_bf16 v[50:53], v[30:33], v[54:57], v[50:53]
	v_mfma_f32_16x16x32_bf16 v[54:57], v[18:21], v[58:61], 0
	v_mfma_f32_16x16x32_bf16 v[58:61], v[26:29], v[58:61], 0
	v_mfma_f32_16x16x32_bf16 v[54:57], v[22:25], v[62:65], v[54:57]
	v_mfma_f32_16x16x32_bf16 v[58:61], v[30:33], v[62:65], v[58:61]
	s_barrier
	s_add_i32 s71, s71, s18
	s_add_i32 s72, s71, 0x2000
	s_mov_b32 m0, s71
	s_add_u32 s56, s34, s36
	ds_read_b128 v[62:65], v238 offset:16384
	ds_read_b128 v[90:93], v238 offset:17408
	ds_read_b128 v[94:97], v238 offset:18432
	ds_read_b128 v[106:109], v238 offset:19456
	ds_read_b128 v[110:113], v238 offset:20480
	ds_read_b128 v[122:125], v238 offset:21504
	ds_read_b128 v[126:129], v238 offset:22528
	ds_read_b128 v[130:133], v238 offset:23552
	s_addc_u32 s57, s35, s37
	global_load_lds_dwordx4 v0, s[34:35]
	s_mov_b32 m0, s72
	s_add_i32 s73, s73, s18
	s_add_i32 s74, s73, 0x2000
	global_load_lds_dwordx4 v210, s[34:35]
	s_mov_b32 m0, s73
	s_nop 0
	global_load_lds_dwordx4 v0, s[56:57]
	s_mov_b32 m0, s74
	s_nop 0
	global_load_lds_dwordx4 v210, s[56:57]
	s_mov_b32 m0, s20
	s_nop 0
	global_load_lds_dwordx4 v236, s[54:55]
	s_mov_b32 m0, s25
	s_nop 0
	global_load_lds_dwordx4 v235, s[54:55]
	s_waitcnt vmcnt(8)
	s_waitcnt lgkmcnt(0)
	s_barrier
	s_waitcnt lgkmcnt(0)
	v_mfma_f32_16x16x32_bf16 v[134:137], v[2:5], v[62:65], 0
	v_mfma_f32_16x16x32_bf16 v[142:145], v[2:5], v[94:97], 0
	v_mfma_f32_16x16x32_bf16 v[150:153], v[2:5], v[110:113], 0
	v_mfma_f32_16x16x32_bf16 v[2:5], v[2:5], v[126:129], 0
	v_mfma_f32_16x16x32_bf16 v[134:137], v[6:9], v[90:93], v[134:137]
	v_mfma_f32_16x16x32_bf16 v[142:145], v[6:9], v[106:109], v[142:145]
	v_mfma_f32_16x16x32_bf16 v[150:153], v[6:9], v[122:125], v[150:153]
	v_mfma_f32_16x16x32_bf16 v[2:5], v[6:9], v[130:133], v[2:5]
	v_mfma_f32_16x16x32_bf16 v[6:9], v[10:13], v[126:129], 0
	v_mfma_f32_16x16x32_bf16 v[138:141], v[10:13], v[62:65], 0
	v_mfma_f32_16x16x32_bf16 v[146:149], v[10:13], v[94:97], 0
	v_mfma_f32_16x16x32_bf16 v[154:157], v[10:13], v[110:113], 0
	v_mfma_f32_16x16x32_bf16 v[6:9], v[14:17], v[130:133], v[6:9]
	v_mfma_f32_16x16x32_bf16 v[138:141], v[14:17], v[90:93], v[138:141]
	v_mfma_f32_16x16x32_bf16 v[146:149], v[14:17], v[106:109], v[146:149]
	v_mfma_f32_16x16x32_bf16 v[154:157], v[14:17], v[122:125], v[154:157]
	v_mfma_f32_16x16x32_bf16 v[10:13], v[18:21], v[62:65], 0
	v_mfma_f32_16x16x32_bf16 v[158:161], v[22:25], v[90:93], v[10:13]
	v_mfma_f32_16x16x32_bf16 v[10:13], v[26:29], v[62:65], 0
	v_mfma_f32_16x16x32_bf16 v[170:173], v[30:33], v[90:93], v[10:13]
	v_mfma_f32_16x16x32_bf16 v[10:13], v[18:21], v[94:97], 0
	v_mfma_f32_16x16x32_bf16 v[174:177], v[22:25], v[106:109], v[10:13]
	v_mfma_f32_16x16x32_bf16 v[10:13], v[26:29], v[94:97], 0
	v_mfma_f32_16x16x32_bf16 v[178:181], v[30:33], v[106:109], v[10:13]
	v_mfma_f32_16x16x32_bf16 v[10:13], v[18:21], v[110:113], 0
	v_mfma_f32_16x16x32_bf16 v[182:185], v[22:25], v[122:125], v[10:13]
	v_mfma_f32_16x16x32_bf16 v[10:13], v[26:29], v[110:113], 0
	v_mfma_f32_16x16x32_bf16 v[186:189], v[30:33], v[122:125], v[10:13]
	v_mfma_f32_16x16x32_bf16 v[10:13], v[18:21], v[126:129], 0
	v_mfma_f32_16x16x32_bf16 v[194:197], v[22:25], v[130:133], v[10:13]
	v_mfma_f32_16x16x32_bf16 v[10:13], v[26:29], v[126:129], 0
	v_mfma_f32_16x16x32_bf16 v[126:129], v[30:33], v[130:133], v[10:13]
	s_barrier
	s_add_i32 s75, 0, 0x18000
	s_add_i32 s77, 0, 0x1c000
	v_add_u32_e32 v116, s75, v237
	v_add_u32_e32 v117, s77, v237
	s_nop 0
	ds_read_b128 v[10:13], v116
	ds_read_b128 v[14:17], v116 offset:1024
	ds_read_b128 v[18:21], v116 offset:2048
	ds_read_b128 v[22:25], v116 offset:3072
	ds_read_b128 v[130:133], v117
	ds_read_b128 v[198:201], v117 offset:1024
	ds_read_b128 v[202:205], v117 offset:2048
	ds_read_b128 v[206:209], v117 offset:3072
	s_add_u32 s54, s54, 0x4000
	s_addc_u32 s55, s55, 0
	s_mov_b32 m0, s58
	ds_read_b128 v[26:29], v238 offset:32768
	ds_read_b128 v[30:33], v238 offset:33792
	ds_read_b128 v[62:65], v238 offset:34816
	ds_read_b128 v[212:215], v238 offset:35840
	ds_read_b128 v[216:219], v238 offset:36864
	ds_read_b128 v[220:223], v238 offset:37888
	ds_read_b128 v[224:227], v238 offset:38912
	ds_read_b128 v[240:243], v238 offset:39936
	s_nop 0
	global_load_lds_dwordx4 v236, s[54:55]
	s_mov_b32 m0, s59
	s_nop 0
	global_load_lds_dwordx4 v235, s[54:55]
	s_waitcnt vmcnt(8)
	s_waitcnt lgkmcnt(0)
	s_barrier
	s_waitcnt lgkmcnt(0)
	v_mfma_f32_16x16x32_bf16 v[66:69], v[10:13], v[26:29], v[66:69]
	v_mfma_f32_16x16x32_bf16 v[162:165], v[14:17], v[30:33], v[66:69]
	v_mfma_f32_16x16x32_bf16 v[66:69], v[18:21], v[26:29], v[70:73]
	v_mfma_f32_16x16x32_bf16 v[166:169], v[22:25], v[30:33], v[66:69]
	v_mfma_f32_16x16x32_bf16 v[66:69], v[10:13], v[62:65], v[74:77]
	v_mfma_f32_16x16x32_bf16 v[110:113], v[14:17], v[212:215], v[66:69]
	v_mfma_f32_16x16x32_bf16 v[66:69], v[18:21], v[62:65], v[78:81]
	v_mfma_f32_16x16x32_bf16 v[106:109], v[22:25], v[212:215], v[66:69]
	v_mfma_f32_16x16x32_bf16 v[66:69], v[10:13], v[216:219], v[82:85]
	v_mfma_f32_16x16x32_bf16 v[94:97], v[14:17], v[220:223], v[66:69]
	v_mfma_f32_16x16x32_bf16 v[66:69], v[18:21], v[216:219], v[86:89]
	v_mfma_f32_16x16x32_bf16 v[90:93], v[22:25], v[220:223], v[66:69]
	v_mfma_f32_16x16x32_bf16 v[66:69], v[10:13], v[224:227], v[98:101]
	v_mfma_f32_16x16x32_bf16 v[70:73], v[14:17], v[240:243], v[66:69]
	v_mfma_f32_16x16x32_bf16 v[66:69], v[18:21], v[224:227], v[102:105]
	v_mfma_f32_16x16x32_bf16 v[66:69], v[22:25], v[240:243], v[66:69]
	v_mfma_f32_16x16x32_bf16 v[74:77], v[130:133], v[26:29], v[118:121]
	v_mfma_f32_16x16x32_bf16 v[26:29], v[202:205], v[26:29], v[34:37]
	v_mfma_f32_16x16x32_bf16 v[118:121], v[206:209], v[30:33], v[26:29]
	v_mfma_f32_16x16x32_bf16 v[26:29], v[130:133], v[62:65], v[38:41]
	v_mfma_f32_16x16x32_bf16 v[102:105], v[198:201], v[212:215], v[26:29]
	v_mfma_f32_16x16x32_bf16 v[26:29], v[202:205], v[62:65], v[42:45]
	v_mfma_f32_16x16x32_bf16 v[98:101], v[206:209], v[212:215], v[26:29]
	v_mfma_f32_16x16x32_bf16 v[26:29], v[130:133], v[216:219], v[46:49]
	v_mfma_f32_16x16x32_bf16 v[86:89], v[198:201], v[220:223], v[26:29]
	v_mfma_f32_16x16x32_bf16 v[26:29], v[202:205], v[216:219], v[50:53]
	v_mfma_f32_16x16x32_bf16 v[82:85], v[206:209], v[220:223], v[26:29]
	v_mfma_f32_16x16x32_bf16 v[26:29], v[130:133], v[224:227], v[54:57]
	v_mfma_f32_16x16x32_bf16 v[54:57], v[198:201], v[240:243], v[26:29]
	v_mfma_f32_16x16x32_bf16 v[26:29], v[202:205], v[224:227], v[58:61]
	v_mfma_f32_16x16x32_bf16 v[122:125], v[198:201], v[30:33], v[74:77]
	v_mfma_f32_16x16x32_bf16 v[50:53], v[206:209], v[240:243], v[26:29]
	s_barrier
	ds_read_b128 v[34:37], v238 offset:49152
	ds_read_b128 v[38:41], v238 offset:50176
	ds_read_b128 v[212:215], v238 offset:51200
	ds_read_b128 v[216:219], v238 offset:52224
	ds_read_b128 v[220:223], v238 offset:53248
	ds_read_b128 v[224:227], v238 offset:54272
	ds_read_b128 v[240:243], v238 offset:55296
	ds_read_b128 v[244:247], v238 offset:56320
	s_add_i32 s75, s75, s18
	v_lshl_add_u64 v[26:27], s[34:35], 0, v[0:1]
	v_lshl_add_u64 v[26:27], v[26:27], 0, s[16:17]
	s_mov_b32 m0, s75
	v_mov_b32_e32 v211, v1
	global_load_lds_dwordx4 v[26:27], off
	s_add_i32 s76, s75, 0x2000
	v_lshl_add_u64 v[26:27], s[34:35], 0, v[210:211]
	v_lshl_add_u64 v[26:27], v[26:27], 0, s[16:17]
	s_mov_b32 m0, s76
	s_add_i32 s77, s77, s18
	global_load_lds_dwordx4 v[26:27], off
	s_mov_b32 m0, s77
	v_lshl_add_u64 v[26:27], s[56:57], 0, v[0:1]
	v_lshl_add_u64 v[26:27], v[26:27], 0, s[16:17]
	global_load_lds_dwordx4 v[26:27], off
	s_nop 0
	v_lshl_add_u64 v[26:27], s[56:57], 0, v[210:211]
	s_add_i32 s56, s77, 0x2000
	v_lshl_add_u64 v[26:27], v[26:27], 0, s[16:17]
	s_mov_b32 m0, s56
	s_nop 0
	global_load_lds_dwordx4 v[26:27], off
	s_mov_b32 m0, s62
	s_nop 0
	global_load_lds_dwordx4 v236, s[30:31]
	s_mov_b32 m0, s63
	s_nop 0
	global_load_lds_dwordx4 v235, s[30:31]
	s_waitcnt vmcnt(8)
	s_waitcnt lgkmcnt(0)
	s_barrier
	s_waitcnt lgkmcnt(0)
	v_mfma_f32_16x16x32_bf16 v[26:29], v[10:13], v[34:37], v[134:137]
	v_mfma_f32_16x16x32_bf16 v[78:81], v[14:17], v[38:41], v[26:29]
	v_mfma_f32_16x16x32_bf16 v[26:29], v[18:21], v[34:37], v[138:141]
	v_mfma_f32_16x16x32_bf16 v[74:77], v[22:25], v[38:41], v[26:29]
	v_mfma_f32_16x16x32_bf16 v[26:29], v[10:13], v[212:215], v[142:145]
	v_mfma_f32_16x16x32_bf16 v[46:49], v[14:17], v[216:219], v[26:29]
	v_mfma_f32_16x16x32_bf16 v[26:29], v[18:21], v[212:215], v[146:149]
	v_mfma_f32_16x16x32_bf16 v[42:45], v[22:25], v[216:219], v[26:29]
	v_mfma_f32_16x16x32_bf16 v[26:29], v[10:13], v[220:223], v[150:153]
	v_mfma_f32_16x16x32_bf16 v[2:5], v[10:13], v[240:243], v[2:5]
	v_mfma_f32_16x16x32_bf16 v[30:33], v[14:17], v[224:227], v[26:29]
	v_mfma_f32_16x16x32_bf16 v[26:29], v[18:21], v[220:223], v[154:157]
	v_mfma_f32_16x16x32_bf16 v[14:17], v[14:17], v[244:247], v[2:5]
	v_mfma_f32_16x16x32_bf16 v[2:5], v[18:21], v[240:243], v[6:9]
	v_mfma_f32_16x16x32_bf16 v[26:29], v[22:25], v[224:227], v[26:29]
	v_mfma_f32_16x16x32_bf16 v[10:13], v[22:25], v[244:247], v[2:5]
	v_mfma_f32_16x16x32_bf16 v[2:5], v[130:133], v[34:37], v[158:161]
	v_mfma_f32_16x16x32_bf16 v[62:65], v[198:201], v[38:41], v[2:5]
	v_mfma_f32_16x16x32_bf16 v[2:5], v[202:205], v[34:37], v[170:173]
	v_mfma_f32_16x16x32_bf16 v[58:61], v[206:209], v[38:41], v[2:5]
	v_mfma_f32_16x16x32_bf16 v[2:5], v[130:133], v[212:215], v[174:177]
	v_mfma_f32_16x16x32_bf16 v[38:41], v[198:201], v[216:219], v[2:5]
	v_mfma_f32_16x16x32_bf16 v[2:5], v[202:205], v[212:215], v[178:181]
	v_mfma_f32_16x16x32_bf16 v[34:37], v[206:209], v[216:219], v[2:5]
	v_mfma_f32_16x16x32_bf16 v[2:5], v[130:133], v[220:223], v[182:185]
	v_mfma_f32_16x16x32_bf16 v[22:25], v[198:201], v[224:227], v[2:5]
	v_mfma_f32_16x16x32_bf16 v[2:5], v[202:205], v[220:223], v[186:189]
	v_mfma_f32_16x16x32_bf16 v[18:21], v[206:209], v[224:227], v[2:5]
	v_mfma_f32_16x16x32_bf16 v[2:5], v[130:133], v[240:243], v[194:197]
	v_mfma_f32_16x16x32_bf16 v[6:9], v[198:201], v[244:247], v[2:5]
	v_mfma_f32_16x16x32_bf16 v[2:5], v[202:205], v[240:243], v[126:129]
	v_mfma_f32_16x16x32_bf16 v[2:5], v[206:209], v[244:247], v[2:5]
	s_barrier
	s_andn2_b64 vcc, exec, s[50:51]
	s_cbranch_vccnz .LBB0_1075
	s_add_u32 s57, s28, 0x200
	s_addc_u32 s78, s29, 0
	s_add_u32 s26, s26, 0x1c000
	s_addc_u32 s27, s27, 0
	s_mov_b32 s79, 4
.LBB0_1074:
	ds_read_b128 v[126:129], v114
	ds_read_b128 v[130:133], v114 offset:1024
	ds_read_b128 v[134:137], v114 offset:2048
	ds_read_b128 v[138:141], v114 offset:3072
	ds_read_b128 v[142:145], v115
	ds_read_b128 v[146:149], v115 offset:1024
	ds_read_b128 v[150:153], v115 offset:2048
	ds_read_b128 v[154:157], v115 offset:3072
	s_add_u32 s28, s26, 0x4000
	s_addc_u32 s29, s27, 0
	s_cmp_eq_u32 s60, s79
	s_cselect_b32 s34, s42, s28
	s_cselect_b32 s35, s43, s29
	s_cselect_b32 s30, s44, s57
	s_cselect_b32 s31, s45, s78
	s_add_u32 s28, s34, 0x8000
	s_addc_u32 s29, s35, 0
	s_mov_b32 m0, s21
	ds_read_b128 v[158:161], v238
	ds_read_b128 v[170:173], v238 offset:1024
	ds_read_b128 v[174:177], v238 offset:2048
	ds_read_b128 v[178:181], v238 offset:3072
	ds_read_b128 v[182:185], v238 offset:4096
	ds_read_b128 v[186:189], v238 offset:5120
	ds_read_b128 v[194:197], v238 offset:6144
	ds_read_b128 v[198:201], v238 offset:7168
	s_nop 0
	global_load_lds_dwordx4 v236, s[26:27]
	s_mov_b32 m0, s70
	s_nop 0
	global_load_lds_dwordx4 v235, s[26:27]
	s_waitcnt vmcnt(8)
	s_waitcnt lgkmcnt(0)
	s_barrier
	s_waitcnt lgkmcnt(0)
	v_mfma_f32_16x16x32_bf16 v[162:165], v[126:129], v[158:161], v[162:165]
	v_mfma_f32_16x16x32_bf16 v[166:169], v[134:137], v[158:161], v[166:169]
	v_mfma_f32_16x16x32_bf16 v[110:113], v[126:129], v[174:177], v[110:113]
	v_mfma_f32_16x16x32_bf16 v[106:109], v[134:137], v[174:177], v[106:109]
	v_mfma_f32_16x16x32_bf16 v[94:97], v[126:129], v[182:185], v[94:97]
	v_mfma_f32_16x16x32_bf16 v[90:93], v[134:137], v[182:185], v[90:93]
	v_mfma_f32_16x16x32_bf16 v[70:73], v[126:129], v[194:197], v[70:73]
	v_mfma_f32_16x16x32_bf16 v[66:69], v[134:137], v[194:197], v[66:69]
	v_mfma_f32_16x16x32_bf16 v[162:165], v[130:133], v[170:173], v[162:165]
	v_mfma_f32_16x16x32_bf16 v[166:169], v[138:141], v[170:173], v[166:169]
	v_mfma_f32_16x16x32_bf16 v[110:113], v[130:133], v[178:181], v[110:113]
	v_mfma_f32_16x16x32_bf16 v[106:109], v[138:141], v[178:181], v[106:109]
	v_mfma_f32_16x16x32_bf16 v[94:97], v[130:133], v[186:189], v[94:97]
	v_mfma_f32_16x16x32_bf16 v[90:93], v[138:141], v[186:189], v[90:93]
	v_mfma_f32_16x16x32_bf16 v[70:73], v[130:133], v[198:201], v[70:73]
	v_mfma_f32_16x16x32_bf16 v[66:69], v[138:141], v[198:201], v[66:69]
	v_mfma_f32_16x16x32_bf16 v[122:125], v[142:145], v[158:161], v[122:125]
	v_mfma_f32_16x16x32_bf16 v[118:121], v[150:153], v[158:161], v[118:121]
	v_mfma_f32_16x16x32_bf16 v[102:105], v[142:145], v[174:177], v[102:105]
	v_mfma_f32_16x16x32_bf16 v[98:101], v[150:153], v[174:177], v[98:101]
	v_mfma_f32_16x16x32_bf16 v[86:89], v[142:145], v[182:185], v[86:89]
	v_mfma_f32_16x16x32_bf16 v[82:85], v[150:153], v[182:185], v[82:85]
	v_mfma_f32_16x16x32_bf16 v[54:57], v[142:145], v[194:197], v[54:57]
	v_mfma_f32_16x16x32_bf16 v[50:53], v[150:153], v[194:197], v[50:53]
	v_mfma_f32_16x16x32_bf16 v[122:125], v[146:149], v[170:173], v[122:125]
	v_mfma_f32_16x16x32_bf16 v[118:121], v[154:157], v[170:173], v[118:121]
	v_mfma_f32_16x16x32_bf16 v[102:105], v[146:149], v[178:181], v[102:105]
	v_mfma_f32_16x16x32_bf16 v[98:101], v[154:157], v[178:181], v[98:101]
	v_mfma_f32_16x16x32_bf16 v[86:89], v[146:149], v[186:189], v[86:89]
	v_mfma_f32_16x16x32_bf16 v[82:85], v[154:157], v[186:189], v[82:85]
	v_mfma_f32_16x16x32_bf16 v[54:57], v[146:149], v[198:201], v[54:57]
	v_mfma_f32_16x16x32_bf16 v[50:53], v[154:157], v[198:201], v[50:53]
	s_barrier
	s_mov_b32 m0, s71
	ds_read_b128 v[158:161], v238 offset:16384
	ds_read_b128 v[170:173], v238 offset:17408
	ds_read_b128 v[174:177], v238 offset:18432
	ds_read_b128 v[178:181], v238 offset:19456
	ds_read_b128 v[182:185], v238 offset:20480
	ds_read_b128 v[186:189], v238 offset:21504
	ds_read_b128 v[194:197], v238 offset:22528
	ds_read_b128 v[198:201], v238 offset:23552
	s_add_u32 s54, s30, s36
	global_load_lds_dwordx4 v0, s[30:31]
	s_mov_b32 m0, s72
	s_addc_u32 s55, s31, s37
	global_load_lds_dwordx4 v210, s[30:31]
	s_mov_b32 m0, s73
	s_nop 0
	global_load_lds_dwordx4 v0, s[54:55]
	s_mov_b32 m0, s74
	s_nop 0
	global_load_lds_dwordx4 v210, s[54:55]
	s_mov_b32 m0, s20
	s_nop 0
	global_load_lds_dwordx4 v236, s[34:35]
	s_mov_b32 m0, s25
	s_nop 0
	global_load_lds_dwordx4 v235, s[34:35]
	s_waitcnt vmcnt(8)
	s_waitcnt lgkmcnt(0)
	s_barrier
	s_waitcnt lgkmcnt(0)
	v_mfma_f32_16x16x32_bf16 v[78:81], v[126:129], v[158:161], v[78:81]
	v_mfma_f32_16x16x32_bf16 v[74:77], v[134:137], v[158:161], v[74:77]
	v_mfma_f32_16x16x32_bf16 v[46:49], v[126:129], v[174:177], v[46:49]
	v_mfma_f32_16x16x32_bf16 v[42:45], v[134:137], v[174:177], v[42:45]
	v_mfma_f32_16x16x32_bf16 v[30:33], v[126:129], v[182:185], v[30:33]
	v_mfma_f32_16x16x32_bf16 v[26:29], v[134:137], v[182:185], v[26:29]
	v_mfma_f32_16x16x32_bf16 v[14:17], v[126:129], v[194:197], v[14:17]
	v_mfma_f32_16x16x32_bf16 v[10:13], v[134:137], v[194:197], v[10:13]
	v_mfma_f32_16x16x32_bf16 v[78:81], v[130:133], v[170:173], v[78:81]
	v_mfma_f32_16x16x32_bf16 v[74:77], v[138:141], v[170:173], v[74:77]
	v_mfma_f32_16x16x32_bf16 v[46:49], v[130:133], v[178:181], v[46:49]
	v_mfma_f32_16x16x32_bf16 v[42:45], v[138:141], v[178:181], v[42:45]
	v_mfma_f32_16x16x32_bf16 v[30:33], v[130:133], v[186:189], v[30:33]
	v_mfma_f32_16x16x32_bf16 v[26:29], v[138:141], v[186:189], v[26:29]
	v_mfma_f32_16x16x32_bf16 v[14:17], v[130:133], v[198:201], v[14:17]
	v_mfma_f32_16x16x32_bf16 v[10:13], v[138:141], v[198:201], v[10:13]
	v_mfma_f32_16x16x32_bf16 v[62:65], v[142:145], v[158:161], v[62:65]
	v_mfma_f32_16x16x32_bf16 v[58:61], v[150:153], v[158:161], v[58:61]
	v_mfma_f32_16x16x32_bf16 v[38:41], v[142:145], v[174:177], v[38:41]
	v_mfma_f32_16x16x32_bf16 v[34:37], v[150:153], v[174:177], v[34:37]
	v_mfma_f32_16x16x32_bf16 v[22:25], v[142:145], v[182:185], v[22:25]
	v_mfma_f32_16x16x32_bf16 v[18:21], v[150:153], v[182:185], v[18:21]
	v_mfma_f32_16x16x32_bf16 v[6:9], v[142:145], v[194:197], v[6:9]
	v_mfma_f32_16x16x32_bf16 v[2:5], v[150:153], v[194:197], v[2:5]
	v_mfma_f32_16x16x32_bf16 v[62:65], v[146:149], v[170:173], v[62:65]
	v_mfma_f32_16x16x32_bf16 v[58:61], v[154:157], v[170:173], v[58:61]
	v_mfma_f32_16x16x32_bf16 v[38:41], v[146:149], v[178:181], v[38:41]
	v_mfma_f32_16x16x32_bf16 v[34:37], v[154:157], v[178:181], v[34:37]
	v_mfma_f32_16x16x32_bf16 v[22:25], v[146:149], v[186:189], v[22:25]
	v_mfma_f32_16x16x32_bf16 v[18:21], v[154:157], v[186:189], v[18:21]
	v_mfma_f32_16x16x32_bf16 v[6:9], v[146:149], v[198:201], v[6:9]
	v_mfma_f32_16x16x32_bf16 v[2:5], v[154:157], v[198:201], v[2:5]
	s_barrier
	ds_read_b128 v[126:129], v116
	ds_read_b128 v[130:133], v116 offset:1024
	ds_read_b128 v[134:137], v116 offset:2048
	ds_read_b128 v[138:141], v116 offset:3072
	ds_read_b128 v[142:145], v117
	ds_read_b128 v[146:149], v117 offset:1024
	ds_read_b128 v[150:153], v117 offset:2048
	ds_read_b128 v[154:157], v117 offset:3072
	s_add_u32 s34, s34, 0x4000
	s_addc_u32 s35, s35, 0
	s_mov_b32 m0, s58
	ds_read_b128 v[158:161], v238 offset:32768
	ds_read_b128 v[170:173], v238 offset:33792
	ds_read_b128 v[174:177], v238 offset:34816
	ds_read_b128 v[178:181], v238 offset:35840
	ds_read_b128 v[182:185], v238 offset:36864
	ds_read_b128 v[186:189], v238 offset:37888
	ds_read_b128 v[194:197], v238 offset:38912
	ds_read_b128 v[198:201], v238 offset:39936
	s_nop 0
	global_load_lds_dwordx4 v236, s[34:35]
	s_mov_b32 m0, s59
	s_nop 0
	global_load_lds_dwordx4 v235, s[34:35]
	s_waitcnt vmcnt(8)
	s_waitcnt lgkmcnt(0)
	s_barrier
	s_waitcnt lgkmcnt(0)
	v_mfma_f32_16x16x32_bf16 v[162:165], v[126:129], v[158:161], v[162:165]
	v_mfma_f32_16x16x32_bf16 v[166:169], v[134:137], v[158:161], v[166:169]
	v_mfma_f32_16x16x32_bf16 v[110:113], v[126:129], v[174:177], v[110:113]
	v_mfma_f32_16x16x32_bf16 v[106:109], v[134:137], v[174:177], v[106:109]
	v_mfma_f32_16x16x32_bf16 v[94:97], v[126:129], v[182:185], v[94:97]
	v_mfma_f32_16x16x32_bf16 v[90:93], v[134:137], v[182:185], v[90:93]
	v_mfma_f32_16x16x32_bf16 v[70:73], v[126:129], v[194:197], v[70:73]
	v_mfma_f32_16x16x32_bf16 v[66:69], v[134:137], v[194:197], v[66:69]
	v_mfma_f32_16x16x32_bf16 v[162:165], v[130:133], v[170:173], v[162:165]
	v_mfma_f32_16x16x32_bf16 v[166:169], v[138:141], v[170:173], v[166:169]
	v_mfma_f32_16x16x32_bf16 v[110:113], v[130:133], v[178:181], v[110:113]
	v_mfma_f32_16x16x32_bf16 v[106:109], v[138:141], v[178:181], v[106:109]
	v_mfma_f32_16x16x32_bf16 v[94:97], v[130:133], v[186:189], v[94:97]
	v_mfma_f32_16x16x32_bf16 v[90:93], v[138:141], v[186:189], v[90:93]
	v_mfma_f32_16x16x32_bf16 v[70:73], v[130:133], v[198:201], v[70:73]
	v_mfma_f32_16x16x32_bf16 v[66:69], v[138:141], v[198:201], v[66:69]
	v_mfma_f32_16x16x32_bf16 v[122:125], v[142:145], v[158:161], v[122:125]
	v_mfma_f32_16x16x32_bf16 v[118:121], v[150:153], v[158:161], v[118:121]
	v_mfma_f32_16x16x32_bf16 v[102:105], v[142:145], v[174:177], v[102:105]
	v_mfma_f32_16x16x32_bf16 v[98:101], v[150:153], v[174:177], v[98:101]
	v_mfma_f32_16x16x32_bf16 v[86:89], v[142:145], v[182:185], v[86:89]
	v_mfma_f32_16x16x32_bf16 v[82:85], v[150:153], v[182:185], v[82:85]
	v_mfma_f32_16x16x32_bf16 v[54:57], v[142:145], v[194:197], v[54:57]
	v_mfma_f32_16x16x32_bf16 v[50:53], v[150:153], v[194:197], v[50:53]
	v_mfma_f32_16x16x32_bf16 v[122:125], v[146:149], v[170:173], v[122:125]
	v_mfma_f32_16x16x32_bf16 v[118:121], v[154:157], v[170:173], v[118:121]
	v_mfma_f32_16x16x32_bf16 v[102:105], v[146:149], v[178:181], v[102:105]
	v_mfma_f32_16x16x32_bf16 v[98:101], v[154:157], v[178:181], v[98:101]
	v_mfma_f32_16x16x32_bf16 v[86:89], v[146:149], v[186:189], v[86:89]
	v_mfma_f32_16x16x32_bf16 v[82:85], v[154:157], v[186:189], v[82:85]
	v_mfma_f32_16x16x32_bf16 v[54:57], v[146:149], v[198:201], v[54:57]
	v_mfma_f32_16x16x32_bf16 v[50:53], v[154:157], v[198:201], v[50:53]
	s_barrier
	ds_read_b128 v[158:161], v238 offset:49152
	ds_read_b128 v[170:173], v238 offset:50176
	ds_read_b128 v[174:177], v238 offset:51200
	ds_read_b128 v[178:181], v238 offset:52224
	ds_read_b128 v[182:185], v238 offset:53248
	ds_read_b128 v[186:189], v238 offset:54272
	ds_read_b128 v[194:197], v238 offset:55296
	ds_read_b128 v[198:201], v238 offset:56320
	s_mov_b32 m0, s75
	v_lshl_add_u64 v[190:191], s[30:31], 0, v[0:1]
	v_lshl_add_u64 v[190:191], v[190:191], 0, s[16:17]
	v_mov_b32_e32 v211, v1
	global_load_lds_dwordx4 v[190:191], off
	s_mov_b32 m0, s76
	v_lshl_add_u64 v[190:191], s[30:31], 0, v[210:211]
	v_lshl_add_u64 v[190:191], v[190:191], 0, s[16:17]
	global_load_lds_dwordx4 v[190:191], off
	s_mov_b32 m0, s77
	v_lshl_add_u64 v[190:191], s[54:55], 0, v[0:1]
	v_lshl_add_u64 v[190:191], v[190:191], 0, s[16:17]
	global_load_lds_dwordx4 v[190:191], off
	s_mov_b32 m0, s56
	v_lshl_add_u64 v[190:191], s[54:55], 0, v[210:211]
	v_lshl_add_u64 v[190:191], v[190:191], 0, s[16:17]
	global_load_lds_dwordx4 v[190:191], off
	s_mov_b32 m0, s62
	s_nop 0
	global_load_lds_dwordx4 v236, s[28:29]
	s_mov_b32 m0, s63
	s_nop 0
	global_load_lds_dwordx4 v235, s[28:29]
	s_waitcnt vmcnt(8)
	s_waitcnt lgkmcnt(0)
	s_barrier
	s_waitcnt lgkmcnt(0)
	v_mfma_f32_16x16x32_bf16 v[78:81], v[126:129], v[158:161], v[78:81]
	v_mfma_f32_16x16x32_bf16 v[74:77], v[134:137], v[158:161], v[74:77]
	v_mfma_f32_16x16x32_bf16 v[46:49], v[126:129], v[174:177], v[46:49]
	v_mfma_f32_16x16x32_bf16 v[42:45], v[134:137], v[174:177], v[42:45]
	v_mfma_f32_16x16x32_bf16 v[30:33], v[126:129], v[182:185], v[30:33]
	v_mfma_f32_16x16x32_bf16 v[26:29], v[134:137], v[182:185], v[26:29]
	v_mfma_f32_16x16x32_bf16 v[14:17], v[126:129], v[194:197], v[14:17]
	v_mfma_f32_16x16x32_bf16 v[10:13], v[134:137], v[194:197], v[10:13]
	v_mfma_f32_16x16x32_bf16 v[78:81], v[130:133], v[170:173], v[78:81]
	v_mfma_f32_16x16x32_bf16 v[74:77], v[138:141], v[170:173], v[74:77]
	v_mfma_f32_16x16x32_bf16 v[46:49], v[130:133], v[178:181], v[46:49]
	v_mfma_f32_16x16x32_bf16 v[42:45], v[138:141], v[178:181], v[42:45]
	v_mfma_f32_16x16x32_bf16 v[30:33], v[130:133], v[186:189], v[30:33]
	v_mfma_f32_16x16x32_bf16 v[26:29], v[138:141], v[186:189], v[26:29]
	v_mfma_f32_16x16x32_bf16 v[14:17], v[130:133], v[198:201], v[14:17]
	v_mfma_f32_16x16x32_bf16 v[10:13], v[138:141], v[198:201], v[10:13]
	v_mfma_f32_16x16x32_bf16 v[62:65], v[142:145], v[158:161], v[62:65]
	v_mfma_f32_16x16x32_bf16 v[58:61], v[150:153], v[158:161], v[58:61]
	v_mfma_f32_16x16x32_bf16 v[38:41], v[142:145], v[174:177], v[38:41]
	v_mfma_f32_16x16x32_bf16 v[34:37], v[150:153], v[174:177], v[34:37]
	v_mfma_f32_16x16x32_bf16 v[22:25], v[142:145], v[182:185], v[22:25]
	v_mfma_f32_16x16x32_bf16 v[18:21], v[150:153], v[182:185], v[18:21]
	v_mfma_f32_16x16x32_bf16 v[6:9], v[142:145], v[194:197], v[6:9]
	v_mfma_f32_16x16x32_bf16 v[2:5], v[150:153], v[194:197], v[2:5]
	v_mfma_f32_16x16x32_bf16 v[62:65], v[146:149], v[170:173], v[62:65]
	v_mfma_f32_16x16x32_bf16 v[58:61], v[154:157], v[170:173], v[58:61]
	v_mfma_f32_16x16x32_bf16 v[38:41], v[146:149], v[178:181], v[38:41]
	v_mfma_f32_16x16x32_bf16 v[34:37], v[154:157], v[178:181], v[34:37]
	v_mfma_f32_16x16x32_bf16 v[22:25], v[146:149], v[186:189], v[22:25]
	v_mfma_f32_16x16x32_bf16 v[18:21], v[154:157], v[186:189], v[18:21]
	v_mfma_f32_16x16x32_bf16 v[6:9], v[146:149], v[198:201], v[6:9]
	v_mfma_f32_16x16x32_bf16 v[2:5], v[154:157], v[198:201], v[2:5]
	s_barrier
	s_add_i32 s28, s79, 2
	s_add_u32 s57, s57, 0x100
	s_addc_u32 s78, s78, 0
	s_add_u32 s26, s26, 0x10000
	s_addc_u32 s27, s27, 0
	s_cmp_lt_i32 s79, s60
	s_mov_b32 s79, s28
	s_cbranch_scc1 .LBB0_1074

.LBB0_1147:
	s_or_b64 exec, exec, s[58:59]
	s_add_u32 s60, s54, 0x10000
	s_addc_u32 s61, s55, 0
	s_and_b64 s[58:59], s[34:35], exec
	s_cselect_b32 s65, s49, s61
	s_cselect_b32 s64, s48, s60
	s_add_u32 s60, s56, 0x10000
	s_addc_u32 s61, s57, 0
	s_and_b64 s[58:59], s[34:35], exec
	s_cselect_b32 s61, s51, s61
	s_cselect_b32 s60, s50, s60
	s_add_u32 s58, s64, 0x8000
	s_addc_u32 s59, s65, 0
	s_add_u32 s62, s60, 0x8000
	s_addc_u32 s63, s61, 0
	s_add_i32 s82, 0, 0x10000
	s_add_i32 s83, 0, 0x14000
	v_add_u32_e32 v132, s82, v140
	v_add_u32_e32 v133, s83, v140
	ds_read_b128 v[2:5], v132
	ds_read_b128 v[6:9], v132 offset:1024
	ds_read_b128 v[10:13], v132 offset:2048
	ds_read_b128 v[14:17], v132 offset:3072
	ds_read_b128 v[18:21], v133
	ds_read_b128 v[22:25], v133 offset:1024
	ds_read_b128 v[26:29], v133 offset:2048
	ds_read_b128 v[30:33], v133 offset:3072
	s_add_u32 s80, s54, 0xc000
	s_addc_u32 s81, s55, 0
	s_add_i32 s78, s15, 0xc000
	s_mov_b32 m0, s78
	s_add_i32 s79, s15, 0xe000
	ds_read_b128 v[34:37], v142
	ds_read_b128 v[38:41], v142 offset:1024
	ds_read_b128 v[42:45], v142 offset:2048
	ds_read_b128 v[46:49], v142 offset:3072
	ds_read_b128 v[50:53], v142 offset:4096
	ds_read_b128 v[54:57], v142 offset:5120
	ds_read_b128 v[58:61], v142 offset:6144
	ds_read_b128 v[62:65], v142 offset:7168
	s_nop 0
	global_load_lds_dwordx4 v136, s[80:81]
	s_mov_b32 m0, s79
	s_nop 0
	global_load_lds_dwordx4 v138, s[80:81]
	s_waitcnt vmcnt(8)
	s_waitcnt lgkmcnt(0)
	s_barrier
	s_waitcnt lgkmcnt(0)
	v_mfma_f32_16x16x32_bf16 v[86:89], v[10:13], v[50:53], 0
	v_mfma_f32_16x16x32_bf16 v[90:93], v[14:17], v[54:57], v[86:89]
	v_mfma_f32_16x16x32_bf16 v[86:89], v[2:5], v[58:61], 0
	v_mfma_f32_16x16x32_bf16 v[66:69], v[2:5], v[34:37], 0
	v_mfma_f32_16x16x32_bf16 v[70:73], v[10:13], v[34:37], 0
	v_mfma_f32_16x16x32_bf16 v[74:77], v[2:5], v[42:45], 0
	v_mfma_f32_16x16x32_bf16 v[78:81], v[10:13], v[42:45], 0
	v_mfma_f32_16x16x32_bf16 v[82:85], v[2:5], v[50:53], 0
	v_mfma_f32_16x16x32_bf16 v[94:97], v[6:9], v[62:65], v[86:89]
	v_mfma_f32_16x16x32_bf16 v[86:89], v[10:13], v[58:61], 0
	v_mfma_f32_16x16x32_bf16 v[66:69], v[6:9], v[38:41], v[66:69]
	v_mfma_f32_16x16x32_bf16 v[70:73], v[14:17], v[38:41], v[70:73]
	v_mfma_f32_16x16x32_bf16 v[74:77], v[6:9], v[46:49], v[74:77]
	v_mfma_f32_16x16x32_bf16 v[78:81], v[14:17], v[46:49], v[78:81]
	v_mfma_f32_16x16x32_bf16 v[82:85], v[6:9], v[54:57], v[82:85]
	v_mfma_f32_16x16x32_bf16 v[106:109], v[14:17], v[62:65], v[86:89]
	v_mfma_f32_16x16x32_bf16 v[86:89], v[18:21], v[34:37], 0
	v_mfma_f32_16x16x32_bf16 v[34:37], v[26:29], v[34:37], 0
	v_mfma_f32_16x16x32_bf16 v[110:113], v[22:25], v[38:41], v[86:89]
	v_mfma_f32_16x16x32_bf16 v[34:37], v[30:33], v[38:41], v[34:37]
	v_mfma_f32_16x16x32_bf16 v[38:41], v[18:21], v[42:45], 0
	v_mfma_f32_16x16x32_bf16 v[42:45], v[26:29], v[42:45], 0
	v_mfma_f32_16x16x32_bf16 v[38:41], v[22:25], v[46:49], v[38:41]
	v_mfma_f32_16x16x32_bf16 v[42:45], v[30:33], v[46:49], v[42:45]
	v_mfma_f32_16x16x32_bf16 v[46:49], v[18:21], v[50:53], 0
	v_mfma_f32_16x16x32_bf16 v[50:53], v[26:29], v[50:53], 0
	v_mfma_f32_16x16x32_bf16 v[46:49], v[22:25], v[54:57], v[46:49]
	v_mfma_f32_16x16x32_bf16 v[50:53], v[30:33], v[54:57], v[50:53]
	v_mfma_f32_16x16x32_bf16 v[54:57], v[18:21], v[58:61], 0
	v_mfma_f32_16x16x32_bf16 v[144:147], v[22:25], v[62:65], v[54:57]
	v_mfma_f32_16x16x32_bf16 v[54:57], v[26:29], v[58:61], 0
	v_mfma_f32_16x16x32_bf16 v[58:61], v[30:33], v[62:65], v[54:57]
	s_barrier
	s_add_i32 s80, s82, s14
	s_add_i32 s81, s80, 0x2000
	s_mov_b32 m0, s80
	s_add_u32 s84, s60, 0x4000
	s_nop 0
	ds_read_b128 v[54:57], v142 offset:16384
	ds_read_b128 v[62:65], v142 offset:17408
	ds_read_b128 v[86:89], v142 offset:18432
	ds_read_b128 v[98:101], v142 offset:19456
	ds_read_b128 v[102:105], v142 offset:20480
	ds_read_b128 v[114:117], v142 offset:21504
	ds_read_b128 v[118:121], v142 offset:22528
	ds_read_b128 v[122:125], v142 offset:23552
	s_addc_u32 s85, s61, 0
	global_load_lds_dwordx4 v137, s[60:61]
	s_mov_b32 m0, s81
	s_add_i32 s82, s83, s14
	s_add_i32 s83, s82, 0x2000
	global_load_lds_dwordx4 v139, s[60:61]
	s_mov_b32 m0, s82
	s_nop 0
	global_load_lds_dwordx4 v137, s[84:85]
	s_mov_b32 m0, s83
	s_nop 0
	global_load_lds_dwordx4 v139, s[84:85]
	s_mov_b32 m0, s15
	s_nop 0
	global_load_lds_dwordx4 v136, s[64:65]
	s_mov_b32 m0, s18
	s_nop 0
	global_load_lds_dwordx4 v138, s[64:65]
	s_waitcnt vmcnt(8)
	s_waitcnt lgkmcnt(0)
	s_barrier
	s_waitcnt lgkmcnt(0)
	v_mfma_f32_16x16x32_bf16 v[126:129], v[2:5], v[54:57], 0
	v_mfma_f32_16x16x32_bf16 v[148:151], v[6:9], v[62:65], v[126:129]
	v_mfma_f32_16x16x32_bf16 v[126:129], v[10:13], v[54:57], 0
	v_mfma_f32_16x16x32_bf16 v[152:155], v[14:17], v[62:65], v[126:129]
	v_mfma_f32_16x16x32_bf16 v[126:129], v[2:5], v[86:89], 0
	v_mfma_f32_16x16x32_bf16 v[156:159], v[6:9], v[98:101], v[126:129]
	v_mfma_f32_16x16x32_bf16 v[126:129], v[10:13], v[86:89], 0
	v_mfma_f32_16x16x32_bf16 v[160:163], v[14:17], v[98:101], v[126:129]
	v_mfma_f32_16x16x32_bf16 v[126:129], v[2:5], v[102:105], 0
	v_mfma_f32_16x16x32_bf16 v[2:5], v[2:5], v[118:121], 0
	v_mfma_f32_16x16x32_bf16 v[164:167], v[6:9], v[114:117], v[126:129]
	v_mfma_f32_16x16x32_bf16 v[2:5], v[6:9], v[122:125], v[2:5]
	v_mfma_f32_16x16x32_bf16 v[6:9], v[10:13], v[118:121], 0
	v_mfma_f32_16x16x32_bf16 v[126:129], v[10:13], v[102:105], 0
	v_mfma_f32_16x16x32_bf16 v[10:13], v[14:17], v[122:125], v[6:9]
	v_mfma_f32_16x16x32_bf16 v[168:171], v[14:17], v[114:117], v[126:129]
	v_mfma_f32_16x16x32_bf16 v[6:9], v[18:21], v[54:57], 0
	v_mfma_f32_16x16x32_bf16 v[14:17], v[22:25], v[62:65], v[6:9]
	v_mfma_f32_16x16x32_bf16 v[6:9], v[26:29], v[54:57], 0
	v_mfma_f32_16x16x32_bf16 v[172:175], v[30:33], v[62:65], v[6:9]
	v_mfma_f32_16x16x32_bf16 v[6:9], v[18:21], v[86:89], 0
	v_mfma_f32_16x16x32_bf16 v[176:179], v[22:25], v[98:101], v[6:9]
	v_mfma_f32_16x16x32_bf16 v[6:9], v[26:29], v[86:89], 0
	v_mfma_f32_16x16x32_bf16 v[180:183], v[30:33], v[98:101], v[6:9]
	v_mfma_f32_16x16x32_bf16 v[6:9], v[18:21], v[102:105], 0
	v_mfma_f32_16x16x32_bf16 v[184:187], v[22:25], v[114:117], v[6:9]
	v_mfma_f32_16x16x32_bf16 v[6:9], v[26:29], v[102:105], 0
	v_mfma_f32_16x16x32_bf16 v[188:191], v[30:33], v[114:117], v[6:9]
	v_mfma_f32_16x16x32_bf16 v[6:9], v[18:21], v[118:121], 0
	v_mfma_f32_16x16x32_bf16 v[194:197], v[22:25], v[122:125], v[6:9]
	v_mfma_f32_16x16x32_bf16 v[6:9], v[26:29], v[118:121], 0
	v_mfma_f32_16x16x32_bf16 v[198:201], v[30:33], v[122:125], v[6:9]
	s_barrier
	s_add_i32 s84, 0, 0x18000
	s_add_i32 s85, 0, 0x1c000
	v_add_u32_e32 v134, s84, v140
	v_add_u32_e32 v135, s85, v140
	s_nop 0
	ds_read_b128 v[6:9], v134
	ds_read_b128 v[26:29], v134 offset:1024
	ds_read_b128 v[30:33], v134 offset:2048
	ds_read_b128 v[202:205], v134 offset:3072
	ds_read_b128 v[206:209], v135
	ds_read_b128 v[210:213], v135 offset:1024
	ds_read_b128 v[214:217], v135 offset:2048
	ds_read_b128 v[218:221], v135 offset:3072
	s_add_u32 s64, s64, 0x4000
	s_addc_u32 s65, s65, 0
	s_mov_b32 m0, s20
	ds_read_b128 v[18:21], v142 offset:32768
	ds_read_b128 v[22:25], v142 offset:33792
	ds_read_b128 v[222:225], v142 offset:34816
	ds_read_b128 v[226:229], v142 offset:35840
	ds_read_b128 v[232:235], v142 offset:36864
	ds_read_b128 v[236:239], v142 offset:37888
	ds_read_b128 v[240:243], v142 offset:38912
	ds_read_b128 v[244:247], v142 offset:39936
	s_nop 0
	global_load_lds_dwordx4 v136, s[64:65]
	s_mov_b32 m0, s21
	s_nop 0
	global_load_lds_dwordx4 v138, s[64:65]
	s_waitcnt vmcnt(8)
	s_waitcnt lgkmcnt(0)
	s_barrier
	s_waitcnt lgkmcnt(0)
	v_mfma_f32_16x16x32_bf16 v[54:57], v[6:9], v[18:21], v[66:69]
	v_mfma_f32_16x16x32_bf16 v[118:121], v[26:29], v[22:25], v[54:57]
	v_mfma_f32_16x16x32_bf16 v[54:57], v[30:33], v[18:21], v[70:73]
	v_mfma_f32_16x16x32_bf16 v[114:117], v[202:205], v[22:25], v[54:57]
	v_mfma_f32_16x16x32_bf16 v[54:57], v[6:9], v[222:225], v[74:77]
	v_mfma_f32_16x16x32_bf16 v[102:105], v[26:29], v[226:229], v[54:57]
	v_mfma_f32_16x16x32_bf16 v[54:57], v[30:33], v[222:225], v[78:81]
	v_mfma_f32_16x16x32_bf16 v[98:101], v[202:205], v[226:229], v[54:57]
	v_mfma_f32_16x16x32_bf16 v[54:57], v[6:9], v[232:235], v[82:85]
	v_mfma_f32_16x16x32_bf16 v[86:89], v[26:29], v[236:239], v[54:57]
	v_mfma_f32_16x16x32_bf16 v[54:57], v[30:33], v[232:235], v[90:93]
	v_mfma_f32_16x16x32_bf16 v[82:85], v[202:205], v[236:239], v[54:57]
	v_mfma_f32_16x16x32_bf16 v[54:57], v[6:9], v[240:243], v[94:97]
	v_mfma_f32_16x16x32_bf16 v[62:65], v[26:29], v[244:247], v[54:57]
	v_mfma_f32_16x16x32_bf16 v[54:57], v[30:33], v[240:243], v[106:109]
	v_mfma_f32_16x16x32_bf16 v[54:57], v[202:205], v[244:247], v[54:57]
	v_mfma_f32_16x16x32_bf16 v[66:69], v[206:209], v[18:21], v[110:113]
	v_mfma_f32_16x16x32_bf16 v[18:21], v[214:217], v[18:21], v[34:37]
	v_mfma_f32_16x16x32_bf16 v[122:125], v[218:221], v[22:25], v[18:21]
	v_mfma_f32_16x16x32_bf16 v[18:21], v[206:209], v[222:225], v[38:41]
	v_mfma_f32_16x16x32_bf16 v[110:113], v[210:213], v[226:229], v[18:21]
	v_mfma_f32_16x16x32_bf16 v[18:21], v[214:217], v[222:225], v[42:45]
	v_mfma_f32_16x16x32_bf16 v[106:109], v[218:221], v[226:229], v[18:21]
	v_mfma_f32_16x16x32_bf16 v[18:21], v[206:209], v[232:235], v[46:49]
	v_mfma_f32_16x16x32_bf16 v[94:97], v[210:213], v[236:239], v[18:21]
	v_mfma_f32_16x16x32_bf16 v[18:21], v[214:217], v[232:235], v[50:53]
	v_mfma_f32_16x16x32_bf16 v[90:93], v[218:221], v[236:239], v[18:21]
	v_mfma_f32_16x16x32_bf16 v[18:21], v[206:209], v[240:243], v[144:147]
	v_mfma_f32_16x16x32_bf16 v[78:81], v[210:213], v[244:247], v[18:21]
	v_mfma_f32_16x16x32_bf16 v[18:21], v[214:217], v[240:243], v[58:61]
	v_mfma_f32_16x16x32_bf16 v[126:129], v[210:213], v[22:25], v[66:69]
	v_mfma_f32_16x16x32_bf16 v[70:73], v[218:221], v[244:247], v[18:21]
	s_barrier
	s_add_i32 s64, s84, s14
	s_add_i32 s65, s64, 0x2000
	s_mov_b32 m0, s64
	s_add_u32 s60, s60, 0xc000
	ds_read_b128 v[42:45], v142 offset:49152
	ds_read_b128 v[46:49], v142 offset:50176
	ds_read_b128 v[144:147], v142 offset:51200
	ds_read_b128 v[222:225], v142 offset:52224
	ds_read_b128 v[226:229], v142 offset:53248
	ds_read_b128 v[232:235], v142 offset:54272
	ds_read_b128 v[236:239], v142 offset:55296
	ds_read_b128 v[240:243], v142 offset:56320
	s_addc_u32 s61, s61, 0
	global_load_lds_dwordx4 v137, s[62:63]
	s_mov_b32 m0, s65
	s_add_i32 s84, s85, s14
	s_add_i32 s85, s84, 0x2000
	global_load_lds_dwordx4 v139, s[62:63]
	s_mov_b32 m0, s84
	s_nop 0
	global_load_lds_dwordx4 v137, s[60:61]
	s_mov_b32 m0, s85
	s_nop 0
	global_load_lds_dwordx4 v139, s[60:61]
	s_mov_b32 m0, s67
	s_nop 0
	global_load_lds_dwordx4 v136, s[58:59]
	s_mov_b32 m0, s68
	s_nop 0
	global_load_lds_dwordx4 v138, s[58:59]
	s_waitcnt vmcnt(8)
	s_waitcnt lgkmcnt(0)
	s_barrier
	s_waitcnt lgkmcnt(0)
	v_mfma_f32_16x16x32_bf16 v[18:21], v[6:9], v[42:45], v[148:151]
	v_mfma_f32_16x16x32_bf16 v[58:61], v[26:29], v[46:49], v[18:21]
	v_mfma_f32_16x16x32_bf16 v[18:21], v[30:33], v[42:45], v[152:155]
	v_mfma_f32_16x16x32_bf16 v[50:53], v[202:205], v[46:49], v[18:21]
	v_mfma_f32_16x16x32_bf16 v[18:21], v[6:9], v[144:147], v[156:159]
	v_mfma_f32_16x16x32_bf16 v[38:41], v[26:29], v[222:225], v[18:21]
	v_mfma_f32_16x16x32_bf16 v[18:21], v[30:33], v[144:147], v[160:163]
	v_mfma_f32_16x16x32_bf16 v[34:37], v[202:205], v[222:225], v[18:21]
	v_mfma_f32_16x16x32_bf16 v[18:21], v[6:9], v[226:229], v[164:167]
	v_mfma_f32_16x16x32_bf16 v[2:5], v[6:9], v[236:239], v[2:5]
	v_mfma_f32_16x16x32_bf16 v[22:25], v[26:29], v[232:235], v[18:21]
	v_mfma_f32_16x16x32_bf16 v[18:21], v[30:33], v[226:229], v[168:171]
	v_mfma_f32_16x16x32_bf16 v[6:9], v[26:29], v[240:243], v[2:5]
	v_mfma_f32_16x16x32_bf16 v[2:5], v[30:33], v[236:239], v[10:13]
	v_mfma_f32_16x16x32_bf16 v[18:21], v[202:205], v[232:235], v[18:21]
	v_mfma_f32_16x16x32_bf16 v[2:5], v[202:205], v[240:243], v[2:5]
	v_mfma_f32_16x16x32_bf16 v[10:13], v[206:209], v[42:45], v[14:17]
	v_mfma_f32_16x16x32_bf16 v[74:77], v[210:213], v[46:49], v[10:13]
	v_mfma_f32_16x16x32_bf16 v[10:13], v[214:217], v[42:45], v[172:175]
	v_mfma_f32_16x16x32_bf16 v[66:69], v[218:221], v[46:49], v[10:13]
	v_mfma_f32_16x16x32_bf16 v[10:13], v[206:209], v[144:147], v[176:179]
	v_mfma_f32_16x16x32_bf16 v[46:49], v[210:213], v[222:225], v[10:13]
	v_mfma_f32_16x16x32_bf16 v[10:13], v[214:217], v[144:147], v[180:183]
	v_mfma_f32_16x16x32_bf16 v[42:45], v[218:221], v[222:225], v[10:13]
	v_mfma_f32_16x16x32_bf16 v[10:13], v[206:209], v[226:229], v[184:187]
	v_mfma_f32_16x16x32_bf16 v[30:33], v[210:213], v[232:235], v[10:13]
	v_mfma_f32_16x16x32_bf16 v[10:13], v[214:217], v[226:229], v[188:191]
	v_mfma_f32_16x16x32_bf16 v[26:29], v[218:221], v[232:235], v[10:13]
	v_mfma_f32_16x16x32_bf16 v[10:13], v[206:209], v[236:239], v[194:197]
	v_mfma_f32_16x16x32_bf16 v[14:17], v[210:213], v[240:243], v[10:13]
	v_mfma_f32_16x16x32_bf16 v[10:13], v[214:217], v[236:239], v[198:201]
	v_mfma_f32_16x16x32_bf16 v[10:13], v[218:221], v[240:243], v[10:13]
	s_barrier
	s_andn2_b64 vcc, exec, s[38:39]
	s_cbranch_vccnz .LBB0_1153
	s_lshl_b32 s58, s72, 10
	s_xor_b32 s86, s58, 0x400
	s_add_u32 s87, s56, 0x20000
	s_addc_u32 s88, s57, 0
	v_ashrrev_i32_e32 v131, 31, v130
	s_add_u32 s54, s54, 0x1c000
	v_lshl_add_u64 v[130:131], v[130:131], 3, s[26:27]
	s_addc_u32 s55, s55, 0
	s_mov_b32 s89, 4

.LBB0_1151:
	s_or_b64 exec, exec, s[58:59]
	ds_read_b128 v[144:147], v132
	ds_read_b128 v[148:151], v132 offset:1024
	ds_read_b128 v[152:155], v132 offset:2048
	ds_read_b128 v[156:159], v132 offset:3072
	ds_read_b128 v[160:163], v133
	ds_read_b128 v[164:167], v133 offset:1024
	ds_read_b128 v[168:171], v133 offset:2048
	ds_read_b128 v[172:175], v133 offset:3072
	s_add_u32 s58, s54, 0x4000
	s_addc_u32 s59, s55, 0
	s_and_b64 s[56:57], s[56:57], exec
	s_cselect_b32 s62, s48, s58
	s_cselect_b32 s63, s49, s59
	s_cselect_b32 s59, s51, s88
	s_cselect_b32 s58, s50, s87
	s_add_u32 s56, s62, 0x8000
	s_addc_u32 s57, s63, 0
	s_add_u32 s60, s58, 0x8000
	s_addc_u32 s61, s59, 0
	s_mov_b32 m0, s78
	ds_read_b128 v[176:179], v142
	ds_read_b128 v[180:183], v142 offset:1024
	ds_read_b128 v[184:187], v142 offset:2048
	ds_read_b128 v[188:191], v142 offset:3072
	ds_read_b128 v[194:197], v142 offset:4096
	ds_read_b128 v[198:201], v142 offset:5120
	ds_read_b128 v[202:205], v142 offset:6144
	ds_read_b128 v[206:209], v142 offset:7168
	s_nop 0
	global_load_lds_dwordx4 v136, s[54:55]
	s_mov_b32 m0, s79
	s_nop 0
	global_load_lds_dwordx4 v138, s[54:55]
	s_waitcnt vmcnt(8)
	s_waitcnt lgkmcnt(0)
	s_barrier
	s_waitcnt lgkmcnt(0)
	v_mfma_f32_16x16x32_bf16 v[118:121], v[144:147], v[176:179], v[118:121]
	v_mfma_f32_16x16x32_bf16 v[114:117], v[152:155], v[176:179], v[114:117]
	v_mfma_f32_16x16x32_bf16 v[102:105], v[144:147], v[184:187], v[102:105]
	v_mfma_f32_16x16x32_bf16 v[98:101], v[152:155], v[184:187], v[98:101]
	v_mfma_f32_16x16x32_bf16 v[86:89], v[144:147], v[194:197], v[86:89]
	v_mfma_f32_16x16x32_bf16 v[82:85], v[152:155], v[194:197], v[82:85]
	v_mfma_f32_16x16x32_bf16 v[62:65], v[144:147], v[202:205], v[62:65]
	v_mfma_f32_16x16x32_bf16 v[54:57], v[152:155], v[202:205], v[54:57]
	v_mfma_f32_16x16x32_bf16 v[118:121], v[148:151], v[180:183], v[118:121]
	v_mfma_f32_16x16x32_bf16 v[114:117], v[156:159], v[180:183], v[114:117]
	v_mfma_f32_16x16x32_bf16 v[102:105], v[148:151], v[188:191], v[102:105]
	v_mfma_f32_16x16x32_bf16 v[98:101], v[156:159], v[188:191], v[98:101]
	v_mfma_f32_16x16x32_bf16 v[86:89], v[148:151], v[198:201], v[86:89]
	v_mfma_f32_16x16x32_bf16 v[82:85], v[156:159], v[198:201], v[82:85]
	v_mfma_f32_16x16x32_bf16 v[62:65], v[148:151], v[206:209], v[62:65]
	v_mfma_f32_16x16x32_bf16 v[54:57], v[156:159], v[206:209], v[54:57]
	v_mfma_f32_16x16x32_bf16 v[126:129], v[160:163], v[176:179], v[126:129]
	v_mfma_f32_16x16x32_bf16 v[122:125], v[168:171], v[176:179], v[122:125]
	v_mfma_f32_16x16x32_bf16 v[110:113], v[160:163], v[184:187], v[110:113]
	v_mfma_f32_16x16x32_bf16 v[106:109], v[168:171], v[184:187], v[106:109]
	v_mfma_f32_16x16x32_bf16 v[94:97], v[160:163], v[194:197], v[94:97]
	v_mfma_f32_16x16x32_bf16 v[90:93], v[168:171], v[194:197], v[90:93]
	v_mfma_f32_16x16x32_bf16 v[78:81], v[160:163], v[202:205], v[78:81]
	v_mfma_f32_16x16x32_bf16 v[70:73], v[168:171], v[202:205], v[70:73]
	v_mfma_f32_16x16x32_bf16 v[126:129], v[164:167], v[180:183], v[126:129]
	v_mfma_f32_16x16x32_bf16 v[122:125], v[172:175], v[180:183], v[122:125]
	v_mfma_f32_16x16x32_bf16 v[110:113], v[164:167], v[188:191], v[110:113]
	v_mfma_f32_16x16x32_bf16 v[106:109], v[172:175], v[188:191], v[106:109]
	v_mfma_f32_16x16x32_bf16 v[94:97], v[164:167], v[198:201], v[94:97]
	v_mfma_f32_16x16x32_bf16 v[90:93], v[172:175], v[198:201], v[90:93]
	v_mfma_f32_16x16x32_bf16 v[78:81], v[164:167], v[206:209], v[78:81]
	v_mfma_f32_16x16x32_bf16 v[70:73], v[172:175], v[206:209], v[70:73]
	s_barrier
	s_mov_b32 m0, s80
	ds_read_b128 v[176:179], v142 offset:16384
	ds_read_b128 v[180:183], v142 offset:17408
	ds_read_b128 v[184:187], v142 offset:18432
	ds_read_b128 v[188:191], v142 offset:19456
	ds_read_b128 v[194:197], v142 offset:20480
	ds_read_b128 v[198:201], v142 offset:21504
	ds_read_b128 v[202:205], v142 offset:22528
	ds_read_b128 v[206:209], v142 offset:23552
	s_add_u32 s90, s58, 0x4000
	global_load_lds_dwordx4 v137, s[58:59]
	s_mov_b32 m0, s81
	s_addc_u32 s91, s59, 0
	global_load_lds_dwordx4 v139, s[58:59]
	s_mov_b32 m0, s82
	s_nop 0
	global_load_lds_dwordx4 v137, s[90:91]
	s_mov_b32 m0, s83
	s_nop 0
	global_load_lds_dwordx4 v139, s[90:91]
	s_mov_b32 m0, s15
	s_nop 0
	global_load_lds_dwordx4 v136, s[62:63]
	s_mov_b32 m0, s18
	s_nop 0
	global_load_lds_dwordx4 v138, s[62:63]
	s_waitcnt vmcnt(8)
	s_waitcnt lgkmcnt(0)
	s_barrier
	s_waitcnt lgkmcnt(0)
	v_mfma_f32_16x16x32_bf16 v[58:61], v[144:147], v[176:179], v[58:61]
	v_mfma_f32_16x16x32_bf16 v[50:53], v[152:155], v[176:179], v[50:53]
	v_mfma_f32_16x16x32_bf16 v[38:41], v[144:147], v[184:187], v[38:41]
	v_mfma_f32_16x16x32_bf16 v[34:37], v[152:155], v[184:187], v[34:37]
	v_mfma_f32_16x16x32_bf16 v[22:25], v[144:147], v[194:197], v[22:25]
	v_mfma_f32_16x16x32_bf16 v[18:21], v[152:155], v[194:197], v[18:21]
	v_mfma_f32_16x16x32_bf16 v[6:9], v[144:147], v[202:205], v[6:9]
	v_mfma_f32_16x16x32_bf16 v[2:5], v[152:155], v[202:205], v[2:5]
	v_mfma_f32_16x16x32_bf16 v[58:61], v[148:151], v[180:183], v[58:61]
	v_mfma_f32_16x16x32_bf16 v[50:53], v[156:159], v[180:183], v[50:53]
	v_mfma_f32_16x16x32_bf16 v[38:41], v[148:151], v[188:191], v[38:41]
	v_mfma_f32_16x16x32_bf16 v[34:37], v[156:159], v[188:191], v[34:37]
	v_mfma_f32_16x16x32_bf16 v[22:25], v[148:151], v[198:201], v[22:25]
	v_mfma_f32_16x16x32_bf16 v[18:21], v[156:159], v[198:201], v[18:21]
	v_mfma_f32_16x16x32_bf16 v[6:9], v[148:151], v[206:209], v[6:9]
	v_mfma_f32_16x16x32_bf16 v[2:5], v[156:159], v[206:209], v[2:5]
	v_mfma_f32_16x16x32_bf16 v[74:77], v[160:163], v[176:179], v[74:77]
	v_mfma_f32_16x16x32_bf16 v[66:69], v[168:171], v[176:179], v[66:69]
	v_mfma_f32_16x16x32_bf16 v[46:49], v[160:163], v[184:187], v[46:49]
	v_mfma_f32_16x16x32_bf16 v[42:45], v[168:171], v[184:187], v[42:45]
	v_mfma_f32_16x16x32_bf16 v[30:33], v[160:163], v[194:197], v[30:33]
	v_mfma_f32_16x16x32_bf16 v[26:29], v[168:171], v[194:197], v[26:29]
	v_mfma_f32_16x16x32_bf16 v[14:17], v[160:163], v[202:205], v[14:17]
	v_mfma_f32_16x16x32_bf16 v[10:13], v[168:171], v[202:205], v[10:13]
	v_mfma_f32_16x16x32_bf16 v[74:77], v[164:167], v[180:183], v[74:77]
	v_mfma_f32_16x16x32_bf16 v[66:69], v[172:175], v[180:183], v[66:69]
	v_mfma_f32_16x16x32_bf16 v[46:49], v[164:167], v[188:191], v[46:49]
	v_mfma_f32_16x16x32_bf16 v[42:45], v[172:175], v[188:191], v[42:45]
	v_mfma_f32_16x16x32_bf16 v[30:33], v[164:167], v[198:201], v[30:33]
	v_mfma_f32_16x16x32_bf16 v[26:29], v[172:175], v[198:201], v[26:29]
	v_mfma_f32_16x16x32_bf16 v[14:17], v[164:167], v[206:209], v[14:17]
	v_mfma_f32_16x16x32_bf16 v[10:13], v[172:175], v[206:209], v[10:13]
	s_barrier
	ds_read_b128 v[144:147], v134
	ds_read_b128 v[148:151], v134 offset:1024
	ds_read_b128 v[152:155], v134 offset:2048
	ds_read_b128 v[156:159], v134 offset:3072
	ds_read_b128 v[160:163], v135
	ds_read_b128 v[164:167], v135 offset:1024
	ds_read_b128 v[168:171], v135 offset:2048
	ds_read_b128 v[172:175], v135 offset:3072
	s_add_u32 s62, s62, 0x4000
	s_addc_u32 s63, s63, 0
	s_mov_b32 m0, s20
	ds_read_b128 v[176:179], v142 offset:32768
	ds_read_b128 v[180:183], v142 offset:33792
	ds_read_b128 v[184:187], v142 offset:34816
	ds_read_b128 v[188:191], v142 offset:35840
	ds_read_b128 v[194:197], v142 offset:36864
	ds_read_b128 v[198:201], v142 offset:37888
	ds_read_b128 v[202:205], v142 offset:38912
	ds_read_b128 v[206:209], v142 offset:39936
	s_nop 0
	global_load_lds_dwordx4 v136, s[62:63]
	s_mov_b32 m0, s21
	s_nop 0
	global_load_lds_dwordx4 v138, s[62:63]
	s_waitcnt vmcnt(8)
	s_waitcnt lgkmcnt(0)
	s_barrier
	s_waitcnt lgkmcnt(0)
	v_mfma_f32_16x16x32_bf16 v[118:121], v[144:147], v[176:179], v[118:121]
	v_mfma_f32_16x16x32_bf16 v[114:117], v[152:155], v[176:179], v[114:117]
	v_mfma_f32_16x16x32_bf16 v[102:105], v[144:147], v[184:187], v[102:105]
	v_mfma_f32_16x16x32_bf16 v[98:101], v[152:155], v[184:187], v[98:101]
	v_mfma_f32_16x16x32_bf16 v[86:89], v[144:147], v[194:197], v[86:89]
	v_mfma_f32_16x16x32_bf16 v[82:85], v[152:155], v[194:197], v[82:85]
	v_mfma_f32_16x16x32_bf16 v[62:65], v[144:147], v[202:205], v[62:65]
	v_mfma_f32_16x16x32_bf16 v[54:57], v[152:155], v[202:205], v[54:57]
	v_mfma_f32_16x16x32_bf16 v[118:121], v[148:151], v[180:183], v[118:121]
	v_mfma_f32_16x16x32_bf16 v[114:117], v[156:159], v[180:183], v[114:117]
	v_mfma_f32_16x16x32_bf16 v[102:105], v[148:151], v[188:191], v[102:105]
	v_mfma_f32_16x16x32_bf16 v[98:101], v[156:159], v[188:191], v[98:101]
	v_mfma_f32_16x16x32_bf16 v[86:89], v[148:151], v[198:201], v[86:89]
	v_mfma_f32_16x16x32_bf16 v[82:85], v[156:159], v[198:201], v[82:85]
	v_mfma_f32_16x16x32_bf16 v[62:65], v[148:151], v[206:209], v[62:65]
	v_mfma_f32_16x16x32_bf16 v[54:57], v[156:159], v[206:209], v[54:57]
	v_mfma_f32_16x16x32_bf16 v[126:129], v[160:163], v[176:179], v[126:129]
	v_mfma_f32_16x16x32_bf16 v[122:125], v[168:171], v[176:179], v[122:125]
	v_mfma_f32_16x16x32_bf16 v[110:113], v[160:163], v[184:187], v[110:113]
	v_mfma_f32_16x16x32_bf16 v[106:109], v[168:171], v[184:187], v[106:109]
	v_mfma_f32_16x16x32_bf16 v[94:97], v[160:163], v[194:197], v[94:97]
	v_mfma_f32_16x16x32_bf16 v[90:93], v[168:171], v[194:197], v[90:93]
	v_mfma_f32_16x16x32_bf16 v[78:81], v[160:163], v[202:205], v[78:81]
	v_mfma_f32_16x16x32_bf16 v[70:73], v[168:171], v[202:205], v[70:73]
	v_mfma_f32_16x16x32_bf16 v[126:129], v[164:167], v[180:183], v[126:129]
	v_mfma_f32_16x16x32_bf16 v[122:125], v[172:175], v[180:183], v[122:125]
	v_mfma_f32_16x16x32_bf16 v[110:113], v[164:167], v[188:191], v[110:113]
	v_mfma_f32_16x16x32_bf16 v[106:109], v[172:175], v[188:191], v[106:109]
	v_mfma_f32_16x16x32_bf16 v[94:97], v[164:167], v[198:201], v[94:97]
	v_mfma_f32_16x16x32_bf16 v[90:93], v[172:175], v[198:201], v[90:93]
	v_mfma_f32_16x16x32_bf16 v[78:81], v[164:167], v[206:209], v[78:81]
	v_mfma_f32_16x16x32_bf16 v[70:73], v[172:175], v[206:209], v[70:73]
	s_barrier
	s_mov_b32 m0, s64
	ds_read_b128 v[176:179], v142 offset:49152
	ds_read_b128 v[180:183], v142 offset:50176
	ds_read_b128 v[184:187], v142 offset:51200
	ds_read_b128 v[188:191], v142 offset:52224
	ds_read_b128 v[194:197], v142 offset:53248
	ds_read_b128 v[198:201], v142 offset:54272
	ds_read_b128 v[202:205], v142 offset:55296
	ds_read_b128 v[206:209], v142 offset:56320
	s_add_u32 s58, s58, 0xc000
	global_load_lds_dwordx4 v137, s[60:61]
	s_mov_b32 m0, s65
	s_addc_u32 s59, s59, 0
	global_load_lds_dwordx4 v139, s[60:61]
	s_mov_b32 m0, s84
	s_nop 0
	global_load_lds_dwordx4 v137, s[58:59]
	s_mov_b32 m0, s85
	s_nop 0
	global_load_lds_dwordx4 v139, s[58:59]
	s_mov_b32 m0, s67
	s_nop 0
	global_load_lds_dwordx4 v136, s[56:57]
	s_mov_b32 m0, s68
	s_nop 0
	global_load_lds_dwordx4 v138, s[56:57]
	s_waitcnt vmcnt(8)
	s_waitcnt lgkmcnt(0)
	s_barrier
	s_waitcnt lgkmcnt(0)
	v_mfma_f32_16x16x32_bf16 v[58:61], v[144:147], v[176:179], v[58:61]
	v_mfma_f32_16x16x32_bf16 v[50:53], v[152:155], v[176:179], v[50:53]
	v_mfma_f32_16x16x32_bf16 v[38:41], v[144:147], v[184:187], v[38:41]
	v_mfma_f32_16x16x32_bf16 v[34:37], v[152:155], v[184:187], v[34:37]
	v_mfma_f32_16x16x32_bf16 v[22:25], v[144:147], v[194:197], v[22:25]
	v_mfma_f32_16x16x32_bf16 v[18:21], v[152:155], v[194:197], v[18:21]
	v_mfma_f32_16x16x32_bf16 v[6:9], v[144:147], v[202:205], v[6:9]
	v_mfma_f32_16x16x32_bf16 v[2:5], v[152:155], v[202:205], v[2:5]
	v_mfma_f32_16x16x32_bf16 v[58:61], v[148:151], v[180:183], v[58:61]
	v_mfma_f32_16x16x32_bf16 v[50:53], v[156:159], v[180:183], v[50:53]
	v_mfma_f32_16x16x32_bf16 v[38:41], v[148:151], v[188:191], v[38:41]
	v_mfma_f32_16x16x32_bf16 v[34:37], v[156:159], v[188:191], v[34:37]
	v_mfma_f32_16x16x32_bf16 v[22:25], v[148:151], v[198:201], v[22:25]
	v_mfma_f32_16x16x32_bf16 v[18:21], v[156:159], v[198:201], v[18:21]
	v_mfma_f32_16x16x32_bf16 v[6:9], v[148:151], v[206:209], v[6:9]
	v_mfma_f32_16x16x32_bf16 v[2:5], v[156:159], v[206:209], v[2:5]
	v_mfma_f32_16x16x32_bf16 v[74:77], v[160:163], v[176:179], v[74:77]
	v_mfma_f32_16x16x32_bf16 v[66:69], v[168:171], v[176:179], v[66:69]
	v_mfma_f32_16x16x32_bf16 v[46:49], v[160:163], v[184:187], v[46:49]
	v_mfma_f32_16x16x32_bf16 v[42:45], v[168:171], v[184:187], v[42:45]
	v_mfma_f32_16x16x32_bf16 v[30:33], v[160:163], v[194:197], v[30:33]
	v_mfma_f32_16x16x32_bf16 v[26:29], v[168:171], v[194:197], v[26:29]
	v_mfma_f32_16x16x32_bf16 v[14:17], v[160:163], v[202:205], v[14:17]
	v_mfma_f32_16x16x32_bf16 v[10:13], v[168:171], v[202:205], v[10:13]
	v_mfma_f32_16x16x32_bf16 v[74:77], v[164:167], v[180:183], v[74:77]
	v_mfma_f32_16x16x32_bf16 v[66:69], v[172:175], v[180:183], v[66:69]
	v_mfma_f32_16x16x32_bf16 v[46:49], v[164:167], v[188:191], v[46:49]
	v_mfma_f32_16x16x32_bf16 v[42:45], v[172:175], v[188:191], v[42:45]
	v_mfma_f32_16x16x32_bf16 v[30:33], v[164:167], v[198:201], v[30:33]
	v_mfma_f32_16x16x32_bf16 v[26:29], v[172:175], v[198:201], v[26:29]
	v_mfma_f32_16x16x32_bf16 v[14:17], v[164:167], v[206:209], v[14:17]
	v_mfma_f32_16x16x32_bf16 v[10:13], v[172:175], v[206:209], v[10:13]
	s_barrier
	s_add_i32 s56, s89, 2
	s_add_u32 s87, s87, 0x10000
	s_addc_u32 s88, s88, 0
	s_add_u32 s54, s54, 0x10000
	s_addc_u32 s55, s55, 0
	s_cmp_lt_i32 s89, s25
	s_cbranch_scc0 .LBB0_1153
	s_mov_b32 s89, s56
	s_branch .LBB0_1149

.LBB0_1225:
	s_add_u32 s34, s26, 0x10000
	s_addc_u32 s35, s27, 0
	s_and_b64 s[30:31], s[46:47], exec
	s_cselect_b32 s53, s39, s35
	s_cselect_b32 s52, s38, s34
	s_add_u32 s65, s28, 0x10000
	s_addc_u32 s66, s29, 0
	s_add_u32 s30, s52, 0x8000
	s_addc_u32 s31, s53, 0
	s_add_i32 s67, 0, 0x10000
	s_and_b64 s[34:35], s[46:47], exec
	s_cselect_b32 s35, s41, s66
	s_cselect_b32 s34, s40, s65
	s_add_i32 s70, 0, 0x14000
	v_add_u32_e32 v114, s67, v236
	v_add_u32_e32 v115, s70, v236
	ds_read_b128 v[2:5], v114
	s_waitcnt lgkmcnt(0)
	ds_read_b128 v[6:9], v114 offset:1024
	ds_read_b128 v[10:13], v114 offset:2048
	ds_read_b128 v[14:17], v114 offset:3072
	ds_read_b128 v[18:21], v115
	ds_read_b128 v[22:25], v115 offset:1024
	ds_read_b128 v[26:29], v115 offset:2048
	ds_read_b128 v[30:33], v115 offset:3072
	s_add_u32 s68, s26, 0xc000
	s_addc_u32 s69, s27, 0
	s_add_i32 s65, s20, 0xc000
	s_mov_b32 m0, s65
	s_add_i32 s66, s20, 0xe000
	ds_read_b128 v[34:37], v237
	ds_read_b128 v[38:41], v237 offset:1024
	ds_read_b128 v[42:45], v237 offset:2048
	ds_read_b128 v[46:49], v237 offset:3072
	ds_read_b128 v[50:53], v237 offset:4096
	ds_read_b128 v[54:57], v237 offset:5120
	ds_read_b128 v[58:61], v237 offset:6144
	ds_read_b128 v[62:65], v237 offset:7168
	s_nop 0
	global_load_lds_dwordx4 v235, s[68:69]
	s_mov_b32 m0, s66
	s_nop 0
	global_load_lds_dwordx4 v226, s[68:69]
	s_waitcnt vmcnt(8)
	s_waitcnt lgkmcnt(0)
	s_barrier
	s_waitcnt lgkmcnt(0)
	v_mfma_f32_16x16x32_bf16 v[90:93], v[2:5], v[58:61], 0
	v_mfma_f32_16x16x32_bf16 v[66:69], v[2:5], v[34:37], 0
	v_mfma_f32_16x16x32_bf16 v[70:73], v[10:13], v[34:37], 0
	v_mfma_f32_16x16x32_bf16 v[74:77], v[2:5], v[42:45], 0
	v_mfma_f32_16x16x32_bf16 v[78:81], v[10:13], v[42:45], 0
	v_mfma_f32_16x16x32_bf16 v[82:85], v[2:5], v[50:53], 0
	v_mfma_f32_16x16x32_bf16 v[86:89], v[10:13], v[50:53], 0
	v_mfma_f32_16x16x32_bf16 v[98:101], v[6:9], v[62:65], v[90:93]
	v_mfma_f32_16x16x32_bf16 v[90:93], v[10:13], v[58:61], 0
	v_mfma_f32_16x16x32_bf16 v[66:69], v[6:9], v[38:41], v[66:69]
	v_mfma_f32_16x16x32_bf16 v[70:73], v[14:17], v[38:41], v[70:73]
	v_mfma_f32_16x16x32_bf16 v[74:77], v[6:9], v[46:49], v[74:77]
	v_mfma_f32_16x16x32_bf16 v[78:81], v[14:17], v[46:49], v[78:81]
	v_mfma_f32_16x16x32_bf16 v[82:85], v[6:9], v[54:57], v[82:85]
	v_mfma_f32_16x16x32_bf16 v[86:89], v[14:17], v[54:57], v[86:89]
	v_mfma_f32_16x16x32_bf16 v[102:105], v[14:17], v[62:65], v[90:93]
	v_mfma_f32_16x16x32_bf16 v[90:93], v[18:21], v[34:37], 0
	v_mfma_f32_16x16x32_bf16 v[34:37], v[26:29], v[34:37], 0
	v_mfma_f32_16x16x32_bf16 v[118:121], v[22:25], v[38:41], v[90:93]
	v_mfma_f32_16x16x32_bf16 v[34:37], v[30:33], v[38:41], v[34:37]
	v_mfma_f32_16x16x32_bf16 v[38:41], v[18:21], v[42:45], 0
	v_mfma_f32_16x16x32_bf16 v[42:45], v[26:29], v[42:45], 0
	v_mfma_f32_16x16x32_bf16 v[38:41], v[22:25], v[46:49], v[38:41]
	v_mfma_f32_16x16x32_bf16 v[42:45], v[30:33], v[46:49], v[42:45]
	v_mfma_f32_16x16x32_bf16 v[46:49], v[18:21], v[50:53], 0
	v_mfma_f32_16x16x32_bf16 v[50:53], v[26:29], v[50:53], 0
	v_mfma_f32_16x16x32_bf16 v[46:49], v[22:25], v[54:57], v[46:49]
	v_mfma_f32_16x16x32_bf16 v[50:53], v[30:33], v[54:57], v[50:53]
	v_mfma_f32_16x16x32_bf16 v[54:57], v[18:21], v[58:61], 0
	v_mfma_f32_16x16x32_bf16 v[58:61], v[26:29], v[58:61], 0
	v_mfma_f32_16x16x32_bf16 v[54:57], v[22:25], v[62:65], v[54:57]
	v_mfma_f32_16x16x32_bf16 v[58:61], v[30:33], v[62:65], v[58:61]
	s_barrier
	s_add_i32 s67, s67, s18
	s_add_i32 s68, s67, 0x2000
	s_mov_b32 m0, s67
	s_add_u32 s72, s34, 0x4000
	ds_read_b128 v[62:65], v237 offset:16384
	ds_read_b128 v[90:93], v237 offset:17408
	ds_read_b128 v[94:97], v237 offset:18432
	ds_read_b128 v[106:109], v237 offset:19456
	ds_read_b128 v[110:113], v237 offset:20480
	ds_read_b128 v[122:125], v237 offset:21504
	ds_read_b128 v[126:129], v237 offset:22528
	ds_read_b128 v[130:133], v237 offset:23552
	s_addc_u32 s73, s35, 0
	global_load_lds_dwordx4 v227, s[34:35]
	s_mov_b32 m0, s68
	s_add_i32 s69, s70, s18
	s_add_i32 s70, s69, 0x2000
	global_load_lds_dwordx4 v0, s[34:35]
	s_mov_b32 m0, s69
	s_nop 0
	global_load_lds_dwordx4 v227, s[72:73]
	s_mov_b32 m0, s70
	s_nop 0
	global_load_lds_dwordx4 v0, s[72:73]
	s_mov_b32 m0, s20
	s_nop 0
	global_load_lds_dwordx4 v235, s[52:53]
	s_mov_b32 m0, s25
	s_nop 0
	global_load_lds_dwordx4 v226, s[52:53]
	s_waitcnt vmcnt(8)
	s_waitcnt lgkmcnt(0)
	s_barrier
	s_waitcnt lgkmcnt(0)
	v_mfma_f32_16x16x32_bf16 v[134:137], v[2:5], v[62:65], 0
	v_mfma_f32_16x16x32_bf16 v[142:145], v[2:5], v[94:97], 0
	v_mfma_f32_16x16x32_bf16 v[150:153], v[2:5], v[110:113], 0
	v_mfma_f32_16x16x32_bf16 v[2:5], v[2:5], v[126:129], 0
	v_mfma_f32_16x16x32_bf16 v[134:137], v[6:9], v[90:93], v[134:137]
	v_mfma_f32_16x16x32_bf16 v[142:145], v[6:9], v[106:109], v[142:145]
	v_mfma_f32_16x16x32_bf16 v[150:153], v[6:9], v[122:125], v[150:153]
	v_mfma_f32_16x16x32_bf16 v[2:5], v[6:9], v[130:133], v[2:5]
	v_mfma_f32_16x16x32_bf16 v[6:9], v[10:13], v[126:129], 0
	v_mfma_f32_16x16x32_bf16 v[138:141], v[10:13], v[62:65], 0
	v_mfma_f32_16x16x32_bf16 v[146:149], v[10:13], v[94:97], 0
	v_mfma_f32_16x16x32_bf16 v[154:157], v[10:13], v[110:113], 0
	v_mfma_f32_16x16x32_bf16 v[6:9], v[14:17], v[130:133], v[6:9]
	v_mfma_f32_16x16x32_bf16 v[138:141], v[14:17], v[90:93], v[138:141]
	v_mfma_f32_16x16x32_bf16 v[146:149], v[14:17], v[106:109], v[146:149]
	v_mfma_f32_16x16x32_bf16 v[154:157], v[14:17], v[122:125], v[154:157]
	v_mfma_f32_16x16x32_bf16 v[10:13], v[18:21], v[62:65], 0
	v_mfma_f32_16x16x32_bf16 v[158:161], v[22:25], v[90:93], v[10:13]
	v_mfma_f32_16x16x32_bf16 v[10:13], v[26:29], v[62:65], 0
	v_mfma_f32_16x16x32_bf16 v[162:165], v[30:33], v[90:93], v[10:13]
	v_mfma_f32_16x16x32_bf16 v[10:13], v[18:21], v[94:97], 0
	v_mfma_f32_16x16x32_bf16 v[174:177], v[22:25], v[106:109], v[10:13]
	v_mfma_f32_16x16x32_bf16 v[10:13], v[26:29], v[94:97], 0
	v_mfma_f32_16x16x32_bf16 v[178:181], v[30:33], v[106:109], v[10:13]
	v_mfma_f32_16x16x32_bf16 v[10:13], v[18:21], v[110:113], 0
	v_mfma_f32_16x16x32_bf16 v[182:185], v[22:25], v[122:125], v[10:13]
	v_mfma_f32_16x16x32_bf16 v[10:13], v[26:29], v[110:113], 0
	v_mfma_f32_16x16x32_bf16 v[122:125], v[30:33], v[122:125], v[10:13]
	v_mfma_f32_16x16x32_bf16 v[10:13], v[18:21], v[126:129], 0
	v_mfma_f32_16x16x32_bf16 v[186:189], v[22:25], v[130:133], v[10:13]
	v_mfma_f32_16x16x32_bf16 v[10:13], v[26:29], v[126:129], 0
	v_mfma_f32_16x16x32_bf16 v[130:133], v[30:33], v[130:133], v[10:13]
	s_barrier
	s_add_i32 s71, 0, 0x18000
	s_add_i32 s74, 0, 0x1c000
	v_add_u32_e32 v116, s71, v236
	v_add_u32_e32 v117, s74, v236
	s_nop 0
	ds_read_b128 v[10:13], v116
	ds_read_b128 v[14:17], v116 offset:1024
	ds_read_b128 v[18:21], v116 offset:2048
	ds_read_b128 v[22:25], v116 offset:3072
	ds_read_b128 v[194:197], v117
	ds_read_b128 v[198:201], v117 offset:1024
	ds_read_b128 v[202:205], v117 offset:2048
	ds_read_b128 v[206:209], v117 offset:3072
	s_add_u32 s52, s52, 0x4000
	s_addc_u32 s53, s53, 0
	s_mov_b32 m0, s54
	ds_read_b128 v[26:29], v237 offset:32768
	ds_read_b128 v[30:33], v237 offset:33792
	ds_read_b128 v[62:65], v237 offset:34816
	ds_read_b128 v[210:213], v237 offset:35840
	ds_read_b128 v[214:217], v237 offset:36864
	ds_read_b128 v[218:221], v237 offset:37888
	ds_read_b128 v[222:225], v237 offset:38912
	ds_read_b128 v[238:241], v237 offset:39936
	s_nop 0
	global_load_lds_dwordx4 v235, s[52:53]
	s_mov_b32 m0, s55
	s_nop 0
	global_load_lds_dwordx4 v226, s[52:53]
	s_waitcnt vmcnt(8)
	s_waitcnt lgkmcnt(0)
	s_barrier
	s_waitcnt lgkmcnt(0)
	v_mfma_f32_16x16x32_bf16 v[66:69], v[10:13], v[26:29], v[66:69]
	v_mfma_f32_16x16x32_bf16 v[166:169], v[14:17], v[30:33], v[66:69]
	v_mfma_f32_16x16x32_bf16 v[66:69], v[18:21], v[26:29], v[70:73]
	v_mfma_f32_16x16x32_bf16 v[170:173], v[22:25], v[30:33], v[66:69]
	v_mfma_f32_16x16x32_bf16 v[66:69], v[10:13], v[62:65], v[74:77]
	v_mfma_f32_16x16x32_bf16 v[110:113], v[14:17], v[210:213], v[66:69]
	v_mfma_f32_16x16x32_bf16 v[66:69], v[18:21], v[62:65], v[78:81]
	v_mfma_f32_16x16x32_bf16 v[106:109], v[22:25], v[210:213], v[66:69]
	v_mfma_f32_16x16x32_bf16 v[66:69], v[10:13], v[214:217], v[82:85]
	v_mfma_f32_16x16x32_bf16 v[94:97], v[14:17], v[218:221], v[66:69]
	v_mfma_f32_16x16x32_bf16 v[66:69], v[18:21], v[214:217], v[86:89]
	v_mfma_f32_16x16x32_bf16 v[90:93], v[22:25], v[218:221], v[66:69]
	v_mfma_f32_16x16x32_bf16 v[66:69], v[10:13], v[222:225], v[98:101]
	v_mfma_f32_16x16x32_bf16 v[78:81], v[14:17], v[238:241], v[66:69]
	v_mfma_f32_16x16x32_bf16 v[66:69], v[18:21], v[222:225], v[102:105]
	v_mfma_f32_16x16x32_bf16 v[70:73], v[22:25], v[238:241], v[66:69]
	v_mfma_f32_16x16x32_bf16 v[66:69], v[194:197], v[26:29], v[118:121]
	v_mfma_f32_16x16x32_bf16 v[26:29], v[202:205], v[26:29], v[34:37]
	v_mfma_f32_16x16x32_bf16 v[118:121], v[206:209], v[30:33], v[26:29]
	v_mfma_f32_16x16x32_bf16 v[26:29], v[194:197], v[62:65], v[38:41]
	v_mfma_f32_16x16x32_bf16 v[102:105], v[198:201], v[210:213], v[26:29]
	v_mfma_f32_16x16x32_bf16 v[26:29], v[202:205], v[62:65], v[42:45]
	v_mfma_f32_16x16x32_bf16 v[98:101], v[206:209], v[210:213], v[26:29]
	v_mfma_f32_16x16x32_bf16 v[26:29], v[194:197], v[214:217], v[46:49]
	v_mfma_f32_16x16x32_bf16 v[86:89], v[198:201], v[218:221], v[26:29]
	v_mfma_f32_16x16x32_bf16 v[26:29], v[202:205], v[214:217], v[50:53]
	v_mfma_f32_16x16x32_bf16 v[82:85], v[206:209], v[218:221], v[26:29]
	v_mfma_f32_16x16x32_bf16 v[26:29], v[194:197], v[222:225], v[54:57]
	v_mfma_f32_16x16x32_bf16 v[62:65], v[198:201], v[238:241], v[26:29]
	v_mfma_f32_16x16x32_bf16 v[26:29], v[202:205], v[222:225], v[58:61]
	v_mfma_f32_16x16x32_bf16 v[126:129], v[198:201], v[30:33], v[66:69]
	v_mfma_f32_16x16x32_bf16 v[54:57], v[206:209], v[238:241], v[26:29]
	s_barrier
	s_add_u32 s72, s34, 0x8000
	s_addc_u32 s73, s35, 0
	s_add_i32 s52, s71, s18
	s_add_i32 s53, s52, 0x2000
	s_mov_b32 m0, s52
	s_add_u32 s34, s34, 0xc000
	ds_read_b128 v[34:37], v237 offset:49152
	ds_read_b128 v[38:41], v237 offset:50176
	ds_read_b128 v[210:213], v237 offset:51200
	ds_read_b128 v[214:217], v237 offset:52224
	ds_read_b128 v[218:221], v237 offset:53248
	ds_read_b128 v[222:225], v237 offset:54272
	ds_read_b128 v[238:241], v237 offset:55296
	ds_read_b128 v[242:245], v237 offset:56320
	s_addc_u32 s35, s35, 0
	global_load_lds_dwordx4 v227, s[72:73]
	s_mov_b32 m0, s53
	s_add_i32 s71, s74, s18
	s_nop 0
	global_load_lds_dwordx4 v0, s[72:73]
	s_mov_b32 m0, s71
	s_add_i32 s72, s71, 0x2000
	s_nop 0
	global_load_lds_dwordx4 v227, s[34:35]
	s_mov_b32 m0, s72
	s_nop 0
	global_load_lds_dwordx4 v0, s[34:35]
	s_mov_b32 m0, s58
	s_nop 0
	global_load_lds_dwordx4 v235, s[30:31]
	s_mov_b32 m0, s59
	s_nop 0
	global_load_lds_dwordx4 v226, s[30:31]
	s_waitcnt vmcnt(8)
	s_waitcnt lgkmcnt(0)
	s_barrier
	s_waitcnt lgkmcnt(0)
	v_mfma_f32_16x16x32_bf16 v[26:29], v[10:13], v[34:37], v[134:137]
	v_mfma_f32_16x16x32_bf16 v[74:77], v[14:17], v[38:41], v[26:29]
	v_mfma_f32_16x16x32_bf16 v[26:29], v[18:21], v[34:37], v[138:141]
	v_mfma_f32_16x16x32_bf16 v[66:69], v[22:25], v[38:41], v[26:29]
	v_mfma_f32_16x16x32_bf16 v[26:29], v[10:13], v[210:213], v[142:145]
	v_mfma_f32_16x16x32_bf16 v[46:49], v[14:17], v[214:217], v[26:29]
	v_mfma_f32_16x16x32_bf16 v[26:29], v[18:21], v[210:213], v[146:149]
	v_mfma_f32_16x16x32_bf16 v[42:45], v[22:25], v[214:217], v[26:29]
	v_mfma_f32_16x16x32_bf16 v[26:29], v[10:13], v[218:221], v[150:153]
	v_mfma_f32_16x16x32_bf16 v[2:5], v[10:13], v[238:241], v[2:5]
	v_mfma_f32_16x16x32_bf16 v[30:33], v[14:17], v[222:225], v[26:29]
	v_mfma_f32_16x16x32_bf16 v[26:29], v[18:21], v[218:221], v[154:157]
	v_mfma_f32_16x16x32_bf16 v[14:17], v[14:17], v[242:245], v[2:5]
	v_mfma_f32_16x16x32_bf16 v[2:5], v[18:21], v[238:241], v[6:9]
	v_mfma_f32_16x16x32_bf16 v[26:29], v[22:25], v[222:225], v[26:29]
	v_mfma_f32_16x16x32_bf16 v[10:13], v[22:25], v[242:245], v[2:5]
	v_mfma_f32_16x16x32_bf16 v[2:5], v[194:197], v[34:37], v[158:161]
	v_mfma_f32_16x16x32_bf16 v[58:61], v[198:201], v[38:41], v[2:5]
	v_mfma_f32_16x16x32_bf16 v[2:5], v[202:205], v[34:37], v[162:165]
	v_mfma_f32_16x16x32_bf16 v[50:53], v[206:209], v[38:41], v[2:5]
	v_mfma_f32_16x16x32_bf16 v[2:5], v[194:197], v[210:213], v[174:177]
	v_mfma_f32_16x16x32_bf16 v[38:41], v[198:201], v[214:217], v[2:5]
	v_mfma_f32_16x16x32_bf16 v[2:5], v[202:205], v[210:213], v[178:181]
	v_mfma_f32_16x16x32_bf16 v[34:37], v[206:209], v[214:217], v[2:5]
	v_mfma_f32_16x16x32_bf16 v[2:5], v[194:197], v[218:221], v[182:185]
	v_mfma_f32_16x16x32_bf16 v[22:25], v[198:201], v[222:225], v[2:5]
	v_mfma_f32_16x16x32_bf16 v[2:5], v[202:205], v[218:221], v[122:125]
	v_mfma_f32_16x16x32_bf16 v[18:21], v[206:209], v[222:225], v[2:5]
	v_mfma_f32_16x16x32_bf16 v[2:5], v[194:197], v[238:241], v[186:189]
	v_mfma_f32_16x16x32_bf16 v[6:9], v[198:201], v[242:245], v[2:5]
	v_mfma_f32_16x16x32_bf16 v[2:5], v[202:205], v[238:241], v[130:133]
	v_mfma_f32_16x16x32_bf16 v[2:5], v[206:209], v[242:245], v[2:5]
	s_barrier
	s_andn2_b64 vcc, exec, s[48:49]
	s_cbranch_vccnz .LBB0_1228
	s_add_u32 s73, s28, 0x20000
	s_addc_u32 s74, s29, 0
	s_add_u32 s26, s26, 0x1c000
	s_addc_u32 s27, s27, 0
	s_mov_b32 s75, 4
.LBB0_1227:
	ds_read_b128 v[122:125], v114
	ds_read_b128 v[130:133], v114 offset:1024
	ds_read_b128 v[134:137], v114 offset:2048
	ds_read_b128 v[138:141], v114 offset:3072
	ds_read_b128 v[142:145], v115
	ds_read_b128 v[146:149], v115 offset:1024
	ds_read_b128 v[150:153], v115 offset:2048
	ds_read_b128 v[154:157], v115 offset:3072
	s_add_u32 s28, s26, 0x4000
	s_addc_u32 s29, s27, 0
	s_cmp_eq_u32 s56, s75
	s_cselect_b32 s34, s38, s28
	s_cselect_b32 s35, s39, s29
	s_cselect_b32 s30, s40, s73
	s_cselect_b32 s31, s41, s74
	s_add_u32 s28, s34, 0x8000
	s_addc_u32 s29, s35, 0
	s_mov_b32 m0, s65
	ds_read_b128 v[158:161], v237
	ds_read_b128 v[162:165], v237 offset:1024
	ds_read_b128 v[174:177], v237 offset:2048
	ds_read_b128 v[178:181], v237 offset:3072
	ds_read_b128 v[182:185], v237 offset:4096
	ds_read_b128 v[186:189], v237 offset:5120
	ds_read_b128 v[194:197], v237 offset:6144
	ds_read_b128 v[198:201], v237 offset:7168
	s_nop 0
	global_load_lds_dwordx4 v235, s[26:27]
	s_mov_b32 m0, s66
	s_nop 0
	global_load_lds_dwordx4 v226, s[26:27]
	s_waitcnt vmcnt(8)
	s_waitcnt lgkmcnt(0)
	s_barrier
	s_waitcnt lgkmcnt(0)
	v_mfma_f32_16x16x32_bf16 v[166:169], v[122:125], v[158:161], v[166:169]
	v_mfma_f32_16x16x32_bf16 v[170:173], v[134:137], v[158:161], v[170:173]
	v_mfma_f32_16x16x32_bf16 v[110:113], v[122:125], v[174:177], v[110:113]
	v_mfma_f32_16x16x32_bf16 v[106:109], v[134:137], v[174:177], v[106:109]
	v_mfma_f32_16x16x32_bf16 v[94:97], v[122:125], v[182:185], v[94:97]
	v_mfma_f32_16x16x32_bf16 v[90:93], v[134:137], v[182:185], v[90:93]
	v_mfma_f32_16x16x32_bf16 v[78:81], v[122:125], v[194:197], v[78:81]
	v_mfma_f32_16x16x32_bf16 v[70:73], v[134:137], v[194:197], v[70:73]
	v_mfma_f32_16x16x32_bf16 v[166:169], v[130:133], v[162:165], v[166:169]
	v_mfma_f32_16x16x32_bf16 v[170:173], v[138:141], v[162:165], v[170:173]
	v_mfma_f32_16x16x32_bf16 v[110:113], v[130:133], v[178:181], v[110:113]
	v_mfma_f32_16x16x32_bf16 v[106:109], v[138:141], v[178:181], v[106:109]
	v_mfma_f32_16x16x32_bf16 v[94:97], v[130:133], v[186:189], v[94:97]
	v_mfma_f32_16x16x32_bf16 v[90:93], v[138:141], v[186:189], v[90:93]
	v_mfma_f32_16x16x32_bf16 v[78:81], v[130:133], v[198:201], v[78:81]
	v_mfma_f32_16x16x32_bf16 v[70:73], v[138:141], v[198:201], v[70:73]
	v_mfma_f32_16x16x32_bf16 v[126:129], v[142:145], v[158:161], v[126:129]
	v_mfma_f32_16x16x32_bf16 v[118:121], v[150:153], v[158:161], v[118:121]
	v_mfma_f32_16x16x32_bf16 v[102:105], v[142:145], v[174:177], v[102:105]
	v_mfma_f32_16x16x32_bf16 v[98:101], v[150:153], v[174:177], v[98:101]
	v_mfma_f32_16x16x32_bf16 v[86:89], v[142:145], v[182:185], v[86:89]
	v_mfma_f32_16x16x32_bf16 v[82:85], v[150:153], v[182:185], v[82:85]
	v_mfma_f32_16x16x32_bf16 v[62:65], v[142:145], v[194:197], v[62:65]
	v_mfma_f32_16x16x32_bf16 v[54:57], v[150:153], v[194:197], v[54:57]
	v_mfma_f32_16x16x32_bf16 v[126:129], v[146:149], v[162:165], v[126:129]
	v_mfma_f32_16x16x32_bf16 v[118:121], v[154:157], v[162:165], v[118:121]
	v_mfma_f32_16x16x32_bf16 v[102:105], v[146:149], v[178:181], v[102:105]
	v_mfma_f32_16x16x32_bf16 v[98:101], v[154:157], v[178:181], v[98:101]
	v_mfma_f32_16x16x32_bf16 v[86:89], v[146:149], v[186:189], v[86:89]
	v_mfma_f32_16x16x32_bf16 v[82:85], v[154:157], v[186:189], v[82:85]
	v_mfma_f32_16x16x32_bf16 v[62:65], v[146:149], v[198:201], v[62:65]
	v_mfma_f32_16x16x32_bf16 v[54:57], v[154:157], v[198:201], v[54:57]
	s_barrier
	s_mov_b32 m0, s67
	ds_read_b128 v[158:161], v237 offset:16384
	ds_read_b128 v[162:165], v237 offset:17408
	ds_read_b128 v[174:177], v237 offset:18432
	ds_read_b128 v[178:181], v237 offset:19456
	ds_read_b128 v[182:185], v237 offset:20480
	ds_read_b128 v[186:189], v237 offset:21504
	ds_read_b128 v[194:197], v237 offset:22528
	ds_read_b128 v[198:201], v237 offset:23552
	s_add_u32 s76, s30, 0x4000
	global_load_lds_dwordx4 v227, s[30:31]
	s_mov_b32 m0, s68
	s_addc_u32 s77, s31, 0
	global_load_lds_dwordx4 v0, s[30:31]
	s_mov_b32 m0, s69
	s_nop 0
	global_load_lds_dwordx4 v227, s[76:77]
	s_mov_b32 m0, s70
	s_nop 0
	global_load_lds_dwordx4 v0, s[76:77]
	s_mov_b32 m0, s20
	s_nop 0
	global_load_lds_dwordx4 v235, s[34:35]
	s_mov_b32 m0, s25
	s_nop 0
	global_load_lds_dwordx4 v226, s[34:35]
	s_waitcnt vmcnt(8)
	s_waitcnt lgkmcnt(0)
	s_barrier
	s_waitcnt lgkmcnt(0)
	v_mfma_f32_16x16x32_bf16 v[74:77], v[122:125], v[158:161], v[74:77]
	v_mfma_f32_16x16x32_bf16 v[66:69], v[134:137], v[158:161], v[66:69]
	v_mfma_f32_16x16x32_bf16 v[46:49], v[122:125], v[174:177], v[46:49]
	v_mfma_f32_16x16x32_bf16 v[42:45], v[134:137], v[174:177], v[42:45]
	v_mfma_f32_16x16x32_bf16 v[30:33], v[122:125], v[182:185], v[30:33]
	v_mfma_f32_16x16x32_bf16 v[26:29], v[134:137], v[182:185], v[26:29]
	v_mfma_f32_16x16x32_bf16 v[14:17], v[122:125], v[194:197], v[14:17]
	v_mfma_f32_16x16x32_bf16 v[10:13], v[134:137], v[194:197], v[10:13]
	v_mfma_f32_16x16x32_bf16 v[74:77], v[130:133], v[162:165], v[74:77]
	v_mfma_f32_16x16x32_bf16 v[66:69], v[138:141], v[162:165], v[66:69]
	v_mfma_f32_16x16x32_bf16 v[46:49], v[130:133], v[178:181], v[46:49]
	v_mfma_f32_16x16x32_bf16 v[42:45], v[138:141], v[178:181], v[42:45]
	v_mfma_f32_16x16x32_bf16 v[30:33], v[130:133], v[186:189], v[30:33]
	v_mfma_f32_16x16x32_bf16 v[26:29], v[138:141], v[186:189], v[26:29]
	v_mfma_f32_16x16x32_bf16 v[14:17], v[130:133], v[198:201], v[14:17]
	v_mfma_f32_16x16x32_bf16 v[10:13], v[138:141], v[198:201], v[10:13]
	v_mfma_f32_16x16x32_bf16 v[58:61], v[142:145], v[158:161], v[58:61]
	v_mfma_f32_16x16x32_bf16 v[50:53], v[150:153], v[158:161], v[50:53]
	v_mfma_f32_16x16x32_bf16 v[38:41], v[142:145], v[174:177], v[38:41]
	v_mfma_f32_16x16x32_bf16 v[34:37], v[150:153], v[174:177], v[34:37]
	v_mfma_f32_16x16x32_bf16 v[22:25], v[142:145], v[182:185], v[22:25]
	v_mfma_f32_16x16x32_bf16 v[18:21], v[150:153], v[182:185], v[18:21]
	v_mfma_f32_16x16x32_bf16 v[6:9], v[142:145], v[194:197], v[6:9]
	v_mfma_f32_16x16x32_bf16 v[2:5], v[150:153], v[194:197], v[2:5]
	v_mfma_f32_16x16x32_bf16 v[58:61], v[146:149], v[162:165], v[58:61]
	v_mfma_f32_16x16x32_bf16 v[50:53], v[154:157], v[162:165], v[50:53]
	v_mfma_f32_16x16x32_bf16 v[38:41], v[146:149], v[178:181], v[38:41]
	v_mfma_f32_16x16x32_bf16 v[34:37], v[154:157], v[178:181], v[34:37]
	v_mfma_f32_16x16x32_bf16 v[22:25], v[146:149], v[186:189], v[22:25]
	v_mfma_f32_16x16x32_bf16 v[18:21], v[154:157], v[186:189], v[18:21]
	v_mfma_f32_16x16x32_bf16 v[6:9], v[146:149], v[198:201], v[6:9]
	v_mfma_f32_16x16x32_bf16 v[2:5], v[154:157], v[198:201], v[2:5]
	s_barrier
	ds_read_b128 v[122:125], v116
	ds_read_b128 v[130:133], v116 offset:1024
	ds_read_b128 v[134:137], v116 offset:2048
	ds_read_b128 v[138:141], v116 offset:3072
	ds_read_b128 v[142:145], v117
	ds_read_b128 v[146:149], v117 offset:1024
	ds_read_b128 v[150:153], v117 offset:2048
	ds_read_b128 v[154:157], v117 offset:3072
	s_add_u32 s34, s34, 0x4000
	s_addc_u32 s35, s35, 0
	s_mov_b32 m0, s54
	ds_read_b128 v[158:161], v237 offset:32768
	ds_read_b128 v[162:165], v237 offset:33792
	ds_read_b128 v[174:177], v237 offset:34816
	ds_read_b128 v[178:181], v237 offset:35840
	ds_read_b128 v[182:185], v237 offset:36864
	ds_read_b128 v[186:189], v237 offset:37888
	ds_read_b128 v[194:197], v237 offset:38912
	ds_read_b128 v[198:201], v237 offset:39936
	s_nop 0
	global_load_lds_dwordx4 v235, s[34:35]
	s_mov_b32 m0, s55
	s_nop 0
	global_load_lds_dwordx4 v226, s[34:35]
	s_waitcnt vmcnt(8)
	s_waitcnt lgkmcnt(0)
	s_barrier
	s_waitcnt lgkmcnt(0)
	v_mfma_f32_16x16x32_bf16 v[166:169], v[122:125], v[158:161], v[166:169]
	v_mfma_f32_16x16x32_bf16 v[170:173], v[134:137], v[158:161], v[170:173]
	v_mfma_f32_16x16x32_bf16 v[110:113], v[122:125], v[174:177], v[110:113]
	v_mfma_f32_16x16x32_bf16 v[106:109], v[134:137], v[174:177], v[106:109]
	v_mfma_f32_16x16x32_bf16 v[94:97], v[122:125], v[182:185], v[94:97]
	v_mfma_f32_16x16x32_bf16 v[90:93], v[134:137], v[182:185], v[90:93]
	v_mfma_f32_16x16x32_bf16 v[78:81], v[122:125], v[194:197], v[78:81]
	v_mfma_f32_16x16x32_bf16 v[70:73], v[134:137], v[194:197], v[70:73]
	v_mfma_f32_16x16x32_bf16 v[166:169], v[130:133], v[162:165], v[166:169]
	v_mfma_f32_16x16x32_bf16 v[170:173], v[138:141], v[162:165], v[170:173]
	v_mfma_f32_16x16x32_bf16 v[110:113], v[130:133], v[178:181], v[110:113]
	v_mfma_f32_16x16x32_bf16 v[106:109], v[138:141], v[178:181], v[106:109]
	v_mfma_f32_16x16x32_bf16 v[94:97], v[130:133], v[186:189], v[94:97]
	v_mfma_f32_16x16x32_bf16 v[90:93], v[138:141], v[186:189], v[90:93]
	v_mfma_f32_16x16x32_bf16 v[78:81], v[130:133], v[198:201], v[78:81]
	v_mfma_f32_16x16x32_bf16 v[70:73], v[138:141], v[198:201], v[70:73]
	v_mfma_f32_16x16x32_bf16 v[126:129], v[142:145], v[158:161], v[126:129]
	v_mfma_f32_16x16x32_bf16 v[118:121], v[150:153], v[158:161], v[118:121]
	v_mfma_f32_16x16x32_bf16 v[102:105], v[142:145], v[174:177], v[102:105]
	v_mfma_f32_16x16x32_bf16 v[98:101], v[150:153], v[174:177], v[98:101]
	v_mfma_f32_16x16x32_bf16 v[86:89], v[142:145], v[182:185], v[86:89]
	v_mfma_f32_16x16x32_bf16 v[82:85], v[150:153], v[182:185], v[82:85]
	v_mfma_f32_16x16x32_bf16 v[62:65], v[142:145], v[194:197], v[62:65]
	v_mfma_f32_16x16x32_bf16 v[54:57], v[150:153], v[194:197], v[54:57]
	v_mfma_f32_16x16x32_bf16 v[126:129], v[146:149], v[162:165], v[126:129]
	v_mfma_f32_16x16x32_bf16 v[118:121], v[154:157], v[162:165], v[118:121]
	v_mfma_f32_16x16x32_bf16 v[102:105], v[146:149], v[178:181], v[102:105]
	v_mfma_f32_16x16x32_bf16 v[98:101], v[154:157], v[178:181], v[98:101]
	v_mfma_f32_16x16x32_bf16 v[86:89], v[146:149], v[186:189], v[86:89]
	v_mfma_f32_16x16x32_bf16 v[82:85], v[154:157], v[186:189], v[82:85]
	v_mfma_f32_16x16x32_bf16 v[62:65], v[146:149], v[198:201], v[62:65]
	v_mfma_f32_16x16x32_bf16 v[54:57], v[154:157], v[198:201], v[54:57]
	s_barrier
	s_add_u32 s34, s30, 0x8000
	s_mov_b32 m0, s52
	s_addc_u32 s35, s31, 0
	ds_read_b128 v[158:161], v237 offset:49152
	ds_read_b128 v[162:165], v237 offset:50176
	ds_read_b128 v[174:177], v237 offset:51200
	ds_read_b128 v[178:181], v237 offset:52224
	ds_read_b128 v[182:185], v237 offset:53248
	ds_read_b128 v[186:189], v237 offset:54272
	ds_read_b128 v[194:197], v237 offset:55296
	ds_read_b128 v[198:201], v237 offset:56320
	s_add_u32 s30, s30, 0xc000
	global_load_lds_dwordx4 v227, s[34:35]
	s_mov_b32 m0, s53
	s_addc_u32 s31, s31, 0
	global_load_lds_dwordx4 v0, s[34:35]
	s_mov_b32 m0, s71
	s_nop 0
	global_load_lds_dwordx4 v227, s[30:31]
	s_mov_b32 m0, s72
	s_nop 0
	global_load_lds_dwordx4 v0, s[30:31]
	s_mov_b32 m0, s58
	s_nop 0
	global_load_lds_dwordx4 v235, s[28:29]
	s_mov_b32 m0, s59
	s_nop 0
	global_load_lds_dwordx4 v226, s[28:29]
	s_waitcnt vmcnt(8)
	s_waitcnt lgkmcnt(0)
	s_barrier
	s_waitcnt lgkmcnt(0)
	v_mfma_f32_16x16x32_bf16 v[74:77], v[122:125], v[158:161], v[74:77]
	v_mfma_f32_16x16x32_bf16 v[66:69], v[134:137], v[158:161], v[66:69]
	v_mfma_f32_16x16x32_bf16 v[46:49], v[122:125], v[174:177], v[46:49]
	v_mfma_f32_16x16x32_bf16 v[42:45], v[134:137], v[174:177], v[42:45]
	v_mfma_f32_16x16x32_bf16 v[30:33], v[122:125], v[182:185], v[30:33]
	v_mfma_f32_16x16x32_bf16 v[26:29], v[134:137], v[182:185], v[26:29]
	v_mfma_f32_16x16x32_bf16 v[14:17], v[122:125], v[194:197], v[14:17]
	v_mfma_f32_16x16x32_bf16 v[10:13], v[134:137], v[194:197], v[10:13]
	v_mfma_f32_16x16x32_bf16 v[74:77], v[130:133], v[162:165], v[74:77]
	v_mfma_f32_16x16x32_bf16 v[66:69], v[138:141], v[162:165], v[66:69]
	v_mfma_f32_16x16x32_bf16 v[46:49], v[130:133], v[178:181], v[46:49]
	v_mfma_f32_16x16x32_bf16 v[42:45], v[138:141], v[178:181], v[42:45]
	v_mfma_f32_16x16x32_bf16 v[30:33], v[130:133], v[186:189], v[30:33]
	v_mfma_f32_16x16x32_bf16 v[26:29], v[138:141], v[186:189], v[26:29]
	v_mfma_f32_16x16x32_bf16 v[14:17], v[130:133], v[198:201], v[14:17]
	v_mfma_f32_16x16x32_bf16 v[10:13], v[138:141], v[198:201], v[10:13]
	v_mfma_f32_16x16x32_bf16 v[58:61], v[142:145], v[158:161], v[58:61]
	v_mfma_f32_16x16x32_bf16 v[50:53], v[150:153], v[158:161], v[50:53]
	v_mfma_f32_16x16x32_bf16 v[38:41], v[142:145], v[174:177], v[38:41]
	v_mfma_f32_16x16x32_bf16 v[34:37], v[150:153], v[174:177], v[34:37]
	v_mfma_f32_16x16x32_bf16 v[22:25], v[142:145], v[182:185], v[22:25]
	v_mfma_f32_16x16x32_bf16 v[18:21], v[150:153], v[182:185], v[18:21]
	v_mfma_f32_16x16x32_bf16 v[6:9], v[142:145], v[194:197], v[6:9]
	v_mfma_f32_16x16x32_bf16 v[2:5], v[150:153], v[194:197], v[2:5]
	v_mfma_f32_16x16x32_bf16 v[58:61], v[146:149], v[162:165], v[58:61]
	v_mfma_f32_16x16x32_bf16 v[50:53], v[154:157], v[162:165], v[50:53]
	v_mfma_f32_16x16x32_bf16 v[38:41], v[146:149], v[178:181], v[38:41]
	v_mfma_f32_16x16x32_bf16 v[34:37], v[154:157], v[178:181], v[34:37]
	v_mfma_f32_16x16x32_bf16 v[22:25], v[146:149], v[186:189], v[22:25]
	v_mfma_f32_16x16x32_bf16 v[18:21], v[154:157], v[186:189], v[18:21]
	v_mfma_f32_16x16x32_bf16 v[6:9], v[146:149], v[198:201], v[6:9]
	v_mfma_f32_16x16x32_bf16 v[2:5], v[154:157], v[198:201], v[2:5]
	s_barrier
	s_add_i32 s28, s75, 2
	s_add_u32 s73, s73, 0x10000
	s_addc_u32 s74, s74, 0
	s_add_u32 s26, s26, 0x10000
	s_addc_u32 s27, s27, 0
	s_cmp_lt_i32 s75, s56
	s_mov_b32 s75, s28
	s_cbranch_scc1 .LBB0_1227
